# 184 dead destination-initialising v_mov before packed fp8 conversions (both halves rewritten by the two cvt) replaced by same-size s_nop
# speedup vs baseline: 1.0047x; 1.0047x over previous
.LBB0_228:
	v_mov_b32_e32 v3, v168
	v_mov_b32_e32 v4, v167
	v_exp_f32_e64 v5, -v150
	v_exp_f32_e64 v7, -v151
	s_lshl_b32 s7, s23, 8
	s_lshl_b32 s6, s84, 7
	v_lshlrev_b32_e32 v2, 4, v3
	v_lshlrev_b32_e32 v3, 3, v3
	v_and_or_b32 v2, v2, 16, s6
	s_mov_b32 s6, 0x3e38aa3b
	v_and_b32_e32 v3, -16, v3
	s_add_i32 s7, s7, s77
	v_add3_u32 v6, s7, v4, v3
	v_fma_f32 v4, v5, s6, s6
	v_fma_f32 v5, v7, s6, s6
	v_exp_f32_e64 v7, -v153
	v_exp_f32_e64 v8, -v152
	v_rcp_f32_e32 v4, v4
	v_rcp_f32_e32 v5, v5
	v_fma_f32 v7, v7, s6, s6
	v_fma_f32 v8, v8, s6, s6
	v_rcp_f32_e32 v9, v7
	v_exp_f32_e64 v7, -v146
	v_rcp_f32_e32 v8, v8
	v_pk_mul_f32 v[10:11], v[152:153], v[160:161]
	v_pk_mul_f32 v[12:13], v[150:151], v[158:159]
	v_fma_f32 v7, v7, s6, s6
	v_pk_mul_f32 v[10:11], v[10:11], v[8:9]
	v_pk_mul_f32 v[4:5], v[12:13], v[4:5]
	v_exp_f32_e64 v8, -v147
	v_exp_f32_e64 v9, -v148
	v_rcp_f32_e32 v12, v7
	v_exp_f32_e64 v7, -v149
	v_fma_f32 v13, v8, s6, s6
	v_fma_f32 v8, v9, s6, s6
	v_rcp_f32_e32 v8, v8
	v_fma_f32 v7, v7, s6, s6
	v_rcp_f32_e32 v9, v7
	v_pk_mul_f32 v[14:15], v[148:149], v[156:157]
	v_rcp_f32_e32 v13, v13
	v_med3_f32 v4, v4, s33, v236
	v_pk_mul_f32 v[14:15], v[14:15], v[8:9]
	v_med3_f32 v5, v5, s33, v236
	s_nop 0
	v_cvt_pk_fp8_f32 v8, v4, v5
	v_pk_mul_f32 v[16:17], v[146:147], v[154:155]
	v_med3_f32 v7, v10, s33, v236
	v_pk_mul_f32 v[4:5], v[16:17], v[12:13]
	v_med3_f32 v9, v11, s33, v236
	v_cvt_pk_fp8_f32 v8, v7, v9 op_sel:[0,0,1]
	v_med3_f32 v4, v4, s33, v236
	v_med3_f32 v5, v5, s33, v236
	s_nop 0
	v_cvt_pk_fp8_f32 v9, v4, v5
	v_med3_f32 v4, v14, s33, v236
	v_med3_f32 v7, v15, s33, v236
	v_exp_f32_e64 v5, -v134
	v_cvt_pk_fp8_f32 v9, v4, v7 op_sel:[0,0,1]
	v_exp_f32_e64 v7, -v135
	v_exp_f32_e64 v10, -v136
	v_fma_f32 v4, v5, s6, s6
	v_rcp_f32_e32 v4, v4
	v_fma_f32 v5, v7, s6, s6
	v_exp_f32_e64 v7, -v137
	v_fma_f32 v10, v10, s6, s6
	v_rcp_f32_e32 v10, v10
	v_rcp_f32_e32 v5, v5
	v_fma_f32 v7, v7, s6, s6
	v_rcp_f32_e32 v11, v7
	v_exp_f32_e64 v7, -v130
	v_pk_mul_f32 v[12:13], v[136:137], v[144:145]
	v_pk_mul_f32 v[14:15], v[134:135], v[142:143]
	v_pk_mul_f32 v[10:11], v[12:13], v[10:11]
	v_fma_f32 v7, v7, s6, s6
	v_exp_f32_e64 v13, -v131
	v_pk_mul_f32 v[4:5], v[14:15], v[4:5]
	v_exp_f32_e64 v14, -v132
	v_rcp_f32_e32 v12, v7
	v_exp_f32_e64 v7, -v133
	v_fma_f32 v13, v13, s6, s6
	v_fma_f32 v14, v14, s6, s6
	v_rcp_f32_e32 v13, v13
	v_fma_f32 v7, v7, s6, s6
	v_rcp_f32_e32 v14, v14
	v_rcp_f32_e32 v15, v7
	v_pk_mul_f32 v[18:19], v[130:131], v[138:139]
	v_pk_mul_f32 v[16:17], v[132:133], v[140:141]
	v_pk_mul_f32 v[12:13], v[18:19], v[12:13]
	v_med3_f32 v4, v4, s33, v236
	v_med3_f32 v5, v5, s33, v236
	v_med3_f32 v7, v10, s33, v236
	s_nop 0
	v_pk_mul_f32 v[14:15], v[16:17], v[14:15]
	v_med3_f32 v16, v11, s33, v236
	v_cvt_pk_fp8_f32 v10, v4, v5
	v_med3_f32 v4, v12, s33, v236
	v_med3_f32 v5, v13, s33, v236
	s_nop 0
	v_cvt_pk_fp8_f32 v11, v4, v5
	v_med3_f32 v4, v14, s33, v236
	v_med3_f32 v5, v15, s33, v236
	v_cvt_pk_fp8_f32 v10, v7, v16 op_sel:[0,0,1]
	v_cvt_pk_fp8_f32 v11, v4, v5 op_sel:[0,0,1]
	v_exp_f32_e64 v7, -v118
	v_or_b32_e32 v2, s78, v2
	v_mov_b64_e32 v[4:5], s[34:35]
	s_movk_i32 s7, 0x1600
	v_ashrrev_i32_e32 v3, 31, v2
	v_mad_i64_i32 v[12:13], s[14:15], v6, s7, v[4:5]
	v_permlane32_swap_b32_e32 v8, v10
	v_permlane32_swap_b32_e32 v9, v11
	v_lshl_add_u64 v[12:13], v[12:13], 0, v[2:3]
	v_fma_f32 v7, v7, s6, s6
	global_store_dwordx4 v[12:13], v[8:11], off
	v_pk_mul_f32 v[12:13], v[120:121], v[128:129]
	v_pk_mul_f32 v[14:15], v[118:119], v[126:127]
	v_rcp_f32_e32 v8, v7
	v_exp_f32_e64 v7, -v120
	v_exp_f32_e64 v11, -v121
	v_exp_f32_e64 v9, -v119
	v_pk_mul_f32 v[18:19], v[114:115], v[122:123]
	v_fma_f32 v7, v7, s6, s6
	v_rcp_f32_e32 v10, v7
	v_fma_f32 v7, v11, s6, s6
	v_rcp_f32_e32 v11, v7
	v_exp_f32_e64 v7, -v114
	v_fma_f32 v9, v9, s6, s6
	v_rcp_f32_e32 v9, v9
	v_pk_mul_f32 v[10:11], v[12:13], v[10:11]
	v_fma_f32 v7, v7, s6, s6
	v_exp_f32_e64 v13, -v115
	v_rcp_f32_e32 v12, v7
	v_exp_f32_e64 v7, -v117
	v_pk_mul_f32 v[8:9], v[14:15], v[8:9]
	v_exp_f32_e64 v14, -v116
	v_fma_f32 v13, v13, s6, s6
	v_fma_f32 v7, v7, s6, s6
	v_rcp_f32_e32 v15, v7
	v_rcp_f32_e32 v13, v13
	v_med3_f32 v7, v8, s33, v236
	v_med3_f32 v9, v9, s33, v236
	s_nop 0
	v_cvt_pk_fp8_f32 v8, v7, v9
	v_fma_f32 v14, v14, s6, s6
	v_rcp_f32_e32 v14, v14
	v_pk_mul_f32 v[12:13], v[18:19], v[12:13]
	v_med3_f32 v7, v10, s33, v236
	v_med3_f32 v9, v11, s33, v236
	v_cvt_pk_fp8_f32 v8, v7, v9 op_sel:[0,0,1]
	v_med3_f32 v7, v12, s33, v236
	v_med3_f32 v10, v13, s33, v236
	s_nop 0
	v_cvt_pk_fp8_f32 v9, v7, v10
	v_pk_mul_f32 v[16:17], v[116:117], v[124:125]
	v_exp_f32_e64 v12, -v100
	v_pk_mul_f32 v[14:15], v[16:17], v[14:15]
	v_exp_f32_e64 v13, -v101
	v_med3_f32 v7, v14, s33, v236
	v_med3_f32 v11, v15, s33, v236
	v_cvt_pk_fp8_f32 v9, v7, v11 op_sel:[0,0,1]
	v_exp_f32_e64 v7, -v99
	v_exp_f32_e64 v10, -v98
	v_pk_mul_f32 v[14:15], v[100:101], v[112:113]
	v_pk_mul_f32 v[16:17], v[98:99], v[110:111]
	v_fma_f32 v7, v7, s6, s6
	v_rcp_f32_e32 v11, v7
	v_fma_f32 v7, v12, s6, s6
	v_rcp_f32_e32 v12, v7
	v_fma_f32 v7, v13, s6, s6
	v_rcp_f32_e32 v13, v7
	v_fma_f32 v10, v10, s6, s6
	v_exp_f32_e64 v7, -v90
	v_rcp_f32_e32 v10, v10
	v_pk_mul_f32 v[12:13], v[14:15], v[12:13]
	v_exp_f32_e64 v15, -v91
	v_fma_f32 v7, v7, s6, s6
	v_pk_mul_f32 v[10:11], v[16:17], v[10:11]
	v_exp_f32_e64 v16, -v92
	v_rcp_f32_e32 v14, v7
	v_exp_f32_e64 v7, -v93
	v_fma_f32 v15, v15, s6, s6
	v_rcp_f32_e32 v15, v15
	v_fma_f32 v16, v16, s6, s6
	v_fma_f32 v7, v7, s6, s6
	v_pk_mul_f32 v[20:21], v[90:91], v[106:107]
	v_rcp_f32_e32 v16, v16
	v_rcp_f32_e32 v17, v7
	v_pk_mul_f32 v[14:15], v[20:21], v[14:15]
	v_med3_f32 v7, v10, s33, v236
	v_med3_f32 v11, v11, s33, v236
	s_nop 0
	v_cvt_pk_fp8_f32 v10, v7, v11
	v_med3_f32 v7, v14, s33, v236
	v_med3_f32 v14, v15, s33, v236
	s_nop 0
	v_cvt_pk_fp8_f32 v11, v7, v14
	v_pk_mul_f32 v[18:19], v[92:93], v[108:109]
	v_med3_f32 v12, v12, s33, v236
	v_pk_mul_f32 v[16:17], v[18:19], v[16:17]
	v_med3_f32 v13, v13, s33, v236
	v_cvt_pk_fp8_f32 v10, v12, v13 op_sel:[0,0,1]
	v_med3_f32 v7, v16, s33, v236
	v_med3_f32 v12, v17, s33, v236
	v_cvt_pk_fp8_f32 v11, v7, v12 op_sel:[0,0,1]
	v_add_u32_e32 v7, 32, v6
	v_mad_i64_i32 v[12:13], s[14:15], v7, s7, v[4:5]
	v_exp_f32_e64 v7, -v86
	v_permlane32_swap_b32_e32 v8, v10
	v_permlane32_swap_b32_e32 v9, v11
	v_lshl_add_u64 v[12:13], v[12:13], 0, v[2:3]
	v_fma_f32 v7, v7, s6, s6
	global_store_dwordx4 v[12:13], v[8:11], off
	v_pk_mul_f32 v[12:13], v[88:89], v[104:105]
	v_pk_mul_f32 v[14:15], v[86:87], v[102:103]
	v_rcp_f32_e32 v8, v7
	v_exp_f32_e64 v7, -v88
	v_exp_f32_e64 v11, -v89
	v_exp_f32_e64 v9, -v87
	v_pk_mul_f32 v[18:19], v[82:83], v[94:95]
	v_fma_f32 v7, v7, s6, s6
	v_rcp_f32_e32 v10, v7
	v_fma_f32 v7, v11, s6, s6
	v_rcp_f32_e32 v11, v7
	v_exp_f32_e64 v7, -v82
	v_fma_f32 v9, v9, s6, s6
	v_rcp_f32_e32 v9, v9
	v_pk_mul_f32 v[10:11], v[12:13], v[10:11]
	v_fma_f32 v7, v7, s6, s6
	v_exp_f32_e64 v13, -v83
	v_rcp_f32_e32 v12, v7
	v_exp_f32_e64 v7, -v85
	v_pk_mul_f32 v[8:9], v[14:15], v[8:9]
	v_exp_f32_e64 v14, -v84
	v_fma_f32 v13, v13, s6, s6
	v_fma_f32 v7, v7, s6, s6
	v_rcp_f32_e32 v15, v7
	v_rcp_f32_e32 v13, v13
	v_med3_f32 v7, v8, s33, v236
	v_med3_f32 v9, v9, s33, v236
	s_nop 0
	v_cvt_pk_fp8_f32 v8, v7, v9
	v_fma_f32 v14, v14, s6, s6
	v_rcp_f32_e32 v14, v14
	v_pk_mul_f32 v[12:13], v[18:19], v[12:13]
	v_med3_f32 v7, v10, s33, v236
	v_med3_f32 v9, v11, s33, v236
	v_cvt_pk_fp8_f32 v8, v7, v9 op_sel:[0,0,1]
	v_med3_f32 v7, v12, s33, v236
	v_med3_f32 v10, v13, s33, v236
	s_nop 0
	v_cvt_pk_fp8_f32 v9, v7, v10
	v_pk_mul_f32 v[16:17], v[84:85], v[96:97]
	v_exp_f32_e64 v12, -v72
	v_pk_mul_f32 v[14:15], v[16:17], v[14:15]
	v_exp_f32_e64 v13, -v73
	v_med3_f32 v7, v14, s33, v236
	v_med3_f32 v11, v15, s33, v236
	v_cvt_pk_fp8_f32 v9, v7, v11 op_sel:[0,0,1]
	v_exp_f32_e64 v7, -v71
	v_exp_f32_e64 v10, -v70
	v_pk_mul_f32 v[14:15], v[72:73], v[80:81]
	v_pk_mul_f32 v[16:17], v[70:71], v[78:79]
	v_fma_f32 v7, v7, s6, s6
	v_rcp_f32_e32 v11, v7
	v_fma_f32 v7, v12, s6, s6
	v_rcp_f32_e32 v12, v7
	v_fma_f32 v7, v13, s6, s6
	v_rcp_f32_e32 v13, v7
	v_fma_f32 v10, v10, s6, s6
	v_exp_f32_e64 v7, -v66
	v_rcp_f32_e32 v10, v10
	v_pk_mul_f32 v[12:13], v[14:15], v[12:13]
	v_exp_f32_e64 v15, -v67
	v_fma_f32 v7, v7, s6, s6
	v_pk_mul_f32 v[10:11], v[16:17], v[10:11]
	v_exp_f32_e64 v16, -v68
	v_rcp_f32_e32 v14, v7
	v_exp_f32_e64 v7, -v69
	v_fma_f32 v15, v15, s6, s6
	v_rcp_f32_e32 v15, v15
	v_fma_f32 v16, v16, s6, s6
	v_fma_f32 v7, v7, s6, s6
	v_pk_mul_f32 v[20:21], v[66:67], v[74:75]
	v_rcp_f32_e32 v16, v16
	v_rcp_f32_e32 v17, v7
	v_pk_mul_f32 v[14:15], v[20:21], v[14:15]
	v_med3_f32 v7, v10, s33, v236
	v_med3_f32 v11, v11, s33, v236
	s_nop 0
	v_cvt_pk_fp8_f32 v10, v7, v11
	v_med3_f32 v7, v14, s33, v236
	v_med3_f32 v14, v15, s33, v236
	s_nop 0
	v_cvt_pk_fp8_f32 v11, v7, v14
	v_pk_mul_f32 v[18:19], v[68:69], v[76:77]
	v_med3_f32 v12, v12, s33, v236
	v_pk_mul_f32 v[16:17], v[18:19], v[16:17]
	v_med3_f32 v13, v13, s33, v236
	v_cvt_pk_fp8_f32 v10, v12, v13 op_sel:[0,0,1]
	v_med3_f32 v7, v16, s33, v236
	v_med3_f32 v12, v17, s33, v236
	v_cvt_pk_fp8_f32 v11, v7, v12 op_sel:[0,0,1]
	v_exp_f32_e64 v7, -v58
	v_add_u32_e32 v22, 0x80, v6
	v_mad_i64_i32 v[12:13], s[14:15], v22, s7, v[4:5]
	v_permlane32_swap_b32_e32 v8, v10
	v_permlane32_swap_b32_e32 v9, v11
	v_lshl_add_u64 v[12:13], v[12:13], 0, v[2:3]
	v_fma_f32 v7, v7, s6, s6
	global_store_dwordx4 v[12:13], v[8:11], off
	v_pk_mul_f32 v[12:13], v[60:61], v[64:65]
	v_pk_mul_f32 v[14:15], v[58:59], v[62:63]
	v_rcp_f32_e32 v8, v7
	v_exp_f32_e64 v7, -v60
	v_exp_f32_e64 v11, -v61
	v_exp_f32_e64 v9, -v59
	v_pk_mul_f32 v[18:19], v[50:51], v[54:55]
	v_fma_f32 v7, v7, s6, s6
	v_rcp_f32_e32 v10, v7
	v_fma_f32 v7, v11, s6, s6
	v_rcp_f32_e32 v11, v7
	v_exp_f32_e64 v7, -v50
	v_fma_f32 v9, v9, s6, s6
	v_rcp_f32_e32 v9, v9
	v_pk_mul_f32 v[10:11], v[12:13], v[10:11]
	v_fma_f32 v7, v7, s6, s6
	v_exp_f32_e64 v13, -v51
	v_rcp_f32_e32 v12, v7
	v_exp_f32_e64 v7, -v53
	v_pk_mul_f32 v[8:9], v[14:15], v[8:9]
	v_exp_f32_e64 v14, -v52
	v_fma_f32 v13, v13, s6, s6
	v_fma_f32 v7, v7, s6, s6
	v_rcp_f32_e32 v15, v7
	v_rcp_f32_e32 v13, v13
	v_med3_f32 v7, v8, s33, v236
	v_med3_f32 v9, v9, s33, v236
	s_nop 0
	v_cvt_pk_fp8_f32 v8, v7, v9
	v_fma_f32 v14, v14, s6, s6
	v_rcp_f32_e32 v14, v14
	v_pk_mul_f32 v[12:13], v[18:19], v[12:13]
	v_med3_f32 v7, v10, s33, v236
	v_med3_f32 v9, v11, s33, v236
	v_cvt_pk_fp8_f32 v8, v7, v9 op_sel:[0,0,1]
	v_med3_f32 v7, v12, s33, v236
	v_med3_f32 v10, v13, s33, v236
	s_nop 0
	v_cvt_pk_fp8_f32 v9, v7, v10
	v_pk_mul_f32 v[16:17], v[52:53], v[56:57]
	v_exp_f32_e64 v12, -v44
	v_pk_mul_f32 v[14:15], v[16:17], v[14:15]
	v_exp_f32_e64 v13, -v45
	v_med3_f32 v7, v14, s33, v236
	v_med3_f32 v11, v15, s33, v236
	v_cvt_pk_fp8_f32 v9, v7, v11 op_sel:[0,0,1]
	v_exp_f32_e64 v7, -v43
	v_exp_f32_e64 v10, -v42
	v_pk_mul_f32 v[14:15], v[44:45], v[48:49]
	v_pk_mul_f32 v[16:17], v[42:43], v[46:47]
	v_fma_f32 v7, v7, s6, s6
	v_rcp_f32_e32 v11, v7
	v_fma_f32 v7, v12, s6, s6
	v_rcp_f32_e32 v12, v7
	v_fma_f32 v7, v13, s6, s6
	v_rcp_f32_e32 v13, v7
	v_fma_f32 v10, v10, s6, s6
	v_exp_f32_e64 v7, -v34
	v_rcp_f32_e32 v10, v10
	v_pk_mul_f32 v[12:13], v[14:15], v[12:13]
	v_exp_f32_e64 v15, -v35
	v_fma_f32 v7, v7, s6, s6
	v_pk_mul_f32 v[10:11], v[16:17], v[10:11]
	v_exp_f32_e64 v16, -v36
	v_rcp_f32_e32 v14, v7
	v_exp_f32_e64 v7, -v37
	v_fma_f32 v15, v15, s6, s6
	v_rcp_f32_e32 v15, v15
	v_fma_f32 v16, v16, s6, s6
	v_fma_f32 v7, v7, s6, s6
	v_pk_mul_f32 v[20:21], v[34:35], v[38:39]
	v_rcp_f32_e32 v16, v16
	v_rcp_f32_e32 v17, v7
	v_pk_mul_f32 v[14:15], v[20:21], v[14:15]
	v_med3_f32 v7, v10, s33, v236
	v_med3_f32 v11, v11, s33, v236
	s_nop 0
	v_cvt_pk_fp8_f32 v10, v7, v11
	v_med3_f32 v7, v14, s33, v236
	v_med3_f32 v14, v15, s33, v236
	s_nop 0
	v_cvt_pk_fp8_f32 v11, v7, v14
	v_pk_mul_f32 v[18:19], v[36:37], v[40:41]
	v_med3_f32 v12, v12, s33, v236
	v_pk_mul_f32 v[16:17], v[18:19], v[16:17]
	v_med3_f32 v13, v13, s33, v236
	v_cvt_pk_fp8_f32 v10, v12, v13 op_sel:[0,0,1]
	v_med3_f32 v7, v16, s33, v236
	v_med3_f32 v12, v17, s33, v236
	v_cvt_pk_fp8_f32 v11, v7, v12 op_sel:[0,0,1]
	v_add_u32_e32 v6, 0xa0, v6
	v_mad_i64_i32 v[4:5], s[6:7], v6, s7, v[4:5]
	s_mov_b32 s62, 0x41200000
	v_permlane32_swap_b32_e32 v8, v10
	v_permlane32_swap_b32_e32 v9, v11
	v_lshl_add_u64 v[2:3], v[4:5], 0, v[2:3]
	s_andn2_b64 vcc, exec, s[38:39]
	s_mov_b64 s[6:7], -1
	s_mov_b32 s63, 0x41300000
	global_store_dwordx4 v[2:3], v[8:11], off
	s_cbranch_vccnz .LBB0_221
	s_andn2_b64 vcc, exec, s[2:3]
	s_cbranch_vccnz .LBB0_220
	s_barrier
	s_branch .LBB0_220

.LBB0_368:
	s_or_b64 exec, exec, s[30:31]
	s_add_u32 s30, s14, 0x32e00000
	s_addc_u32 s31, s15, 0
	s_xor_b64 s[0:1], s[24:25], -1
	s_or_b64 s[20:21], s[42:43], s[0:1]
	s_add_u32 s6, s14, 0x4e200000
	s_addc_u32 s7, s15, 0
	s_lshl_b64 s[0:1], s[12:13], 2
	s_add_u32 s8, s28, s0
	s_addc_u32 s9, s29, s1
	s_add_u32 s0, s26, s0
	s_addc_u32 s1, s27, s1
	v_lshlrev_b64 v[138:139], 2, v[170:171]
	s_waitcnt lgkmcnt(0)
	s_barrier
	v_lshl_add_u64 v[150:151], s[8:9], 0, v[138:139]
	v_lshl_add_u64 v[148:149], s[0:1], 0, v[138:139]
	global_load_dwordx4 v[130:133], v[150:151], off offset:16
	global_load_dwordx4 v[134:137], v[150:151], off
	global_load_dwordx4 v[138:141], v[148:149], off offset:16
	global_load_dwordx4 v[142:145], v[148:149], off
	v_lshl_add_u32 v0, v180, 3, 0
	ds_read_b64 v[162:163], v0 offset:8192
	v_lshlrev_b64 v[146:147], 11, v[178:179]
	v_lshl_add_u64 v[152:153], v[146:147], 0, v[170:171]
	v_lshl_add_u64 v[166:167], v[152:153], 1, s[30:31]
	s_andn2_b64 vcc, exec, s[20:21]
	s_waitcnt lgkmcnt(0)
	v_pk_fma_f32 v[164:165], v[102:103], v[162:163], v[162:163] op_sel:[0,1,0] op_sel_hi:[1,1,0]
	v_pk_fma_f32 v[102:103], v[104:105], v[162:163], v[162:163] op_sel:[0,1,0] op_sel_hi:[1,1,0]
	s_waitcnt vmcnt(0)
	v_pk_fma_f32 v[104:105], v[134:135], v[164:165], v[142:143]
	v_pk_fma_f32 v[164:165], v[98:99], v[162:163], v[162:163] op_sel:[0,1,0] op_sel_hi:[1,1,0]
	v_pk_fma_f32 v[98:99], v[100:101], v[162:163], v[162:163] op_sel:[0,1,0] op_sel_hi:[1,1,0]
	v_cvt_pk_bf16_f32 v162, v104, v105
	v_pk_fma_f32 v[102:103], v[136:137], v[102:103], v[144:145]
	v_pk_fma_f32 v[98:99], v[132:133], v[98:99], v[140:141]
	v_pk_fma_f32 v[100:101], v[130:131], v[164:165], v[138:139]
	v_cvt_pk_bf16_f32 v163, v102, v103
	s_nop 0
	v_cvt_pk_bf16_f32 v164, v100, v101
	v_cvt_pk_bf16_f32 v165, v98, v99
	global_store_dwordx4 v[166:167], v[162:165], off
	s_nop 1
	v_cndmask_b32_e64 v162, 0, 1, s[20:21]
	v_cmp_ne_u32_e64 s[0:1], 1, v162
	s_cbranch_vccnz .LBB0_370
	v_mul_f32_e32 v104, s5, v104
	v_mul_f32_e32 v105, s5, v105
	v_mul_f32_e32 v162, s5, v102
	v_med3_f32 v104, v104, s33, v236
	v_med3_f32 v105, v105, s33, v236
	s_nop 0
	v_cvt_pk_fp8_f32 v102, v104, v105
	v_mul_f32_e32 v103, s5, v103
	v_med3_f32 v104, v162, s33, v236
	v_med3_f32 v103, v103, s33, v236
	v_mul_f32_e32 v100, s5, v100
	v_mul_f32_e32 v101, s5, v101
	v_cvt_pk_fp8_f32 v102, v104, v103 op_sel:[0,0,1]
	v_med3_f32 v100, v100, s33, v236
	v_med3_f32 v101, v101, s33, v236
	s_nop 0
	v_cvt_pk_fp8_f32 v103, v100, v101
	v_mul_f32_e32 v98, s5, v98
	v_mul_f32_e32 v99, s5, v99
	v_med3_f32 v98, v98, s33, v236
	v_med3_f32 v99, v99, s33, v236
	v_cvt_pk_fp8_f32 v103, v98, v99 op_sel:[0,0,1]
	v_lshl_add_u64 v[98:99], s[6:7], 0, v[152:153]
	global_store_dwordx2 v[98:99], v[102:103], off
.LBB0_370:
	ds_read_b64 v[100:101], v0 offset:8320
	v_lshlrev_b64 v[102:103], 11, v[176:177]
	v_lshl_add_u64 v[98:99], v[102:103], 0, v[170:171]
	s_and_b64 vcc, exec, s[0:1]
	s_waitcnt lgkmcnt(0)
	v_pk_fma_f32 v[104:105], v[86:87], v[100:101], v[100:101] op_sel:[0,1,0] op_sel_hi:[1,1,0]
	v_pk_fma_f32 v[86:87], v[88:89], v[100:101], v[100:101] op_sel:[0,1,0] op_sel_hi:[1,1,0]
	v_pk_fma_f32 v[88:89], v[134:135], v[104:105], v[142:143]
	v_pk_fma_f32 v[104:105], v[82:83], v[100:101], v[100:101] op_sel:[0,1,0] op_sel_hi:[1,1,0]
	v_pk_fma_f32 v[82:83], v[84:85], v[100:101], v[100:101] op_sel:[0,1,0] op_sel_hi:[1,1,0]
	v_pk_fma_f32 v[86:87], v[136:137], v[86:87], v[144:145]
	v_pk_fma_f32 v[82:83], v[132:133], v[82:83], v[140:141]
	v_pk_fma_f32 v[84:85], v[130:131], v[104:105], v[138:139]
	v_lshl_add_u64 v[100:101], v[98:99], 1, s[30:31]
	v_cvt_pk_bf16_f32 v162, v88, v89
	v_cvt_pk_bf16_f32 v163, v86, v87
	v_cvt_pk_bf16_f32 v164, v84, v85
	v_cvt_pk_bf16_f32 v165, v82, v83
	global_store_dwordx4 v[100:101], v[162:165], off
	s_cbranch_vccnz .LBB0_372
	v_mul_f32_e32 v88, s5, v88
	v_mul_f32_e32 v89, s5, v89
	v_mul_f32_e32 v100, s5, v86
	v_med3_f32 v88, v88, s33, v236
	v_med3_f32 v89, v89, s33, v236
	s_nop 0
	v_cvt_pk_fp8_f32 v86, v88, v89
	v_mul_f32_e32 v87, s5, v87
	v_med3_f32 v88, v100, s33, v236
	v_med3_f32 v87, v87, s33, v236
	v_mul_f32_e32 v84, s5, v84
	v_mul_f32_e32 v85, s5, v85
	v_cvt_pk_fp8_f32 v86, v88, v87 op_sel:[0,0,1]
	v_med3_f32 v84, v84, s33, v236
	v_med3_f32 v85, v85, s33, v236
	s_nop 0
	v_cvt_pk_fp8_f32 v87, v84, v85
	v_mul_f32_e32 v82, s5, v82
	v_mul_f32_e32 v83, s5, v83
	v_med3_f32 v82, v82, s33, v236
	v_med3_f32 v83, v83, s33, v236
	v_cvt_pk_fp8_f32 v87, v82, v83 op_sel:[0,0,1]
	v_lshl_add_u64 v[82:83], s[6:7], 0, v[98:99]
	global_store_dwordx2 v[82:83], v[86:87], off
.LBB0_372:
	ds_read_b64 v[84:85], v0 offset:8448
	v_lshlrev_b64 v[100:101], 11, v[174:175]
	v_lshl_add_u64 v[82:83], v[100:101], 0, v[170:171]
	v_lshl_add_u64 v[88:89], v[82:83], 1, s[30:31]
	s_and_b64 vcc, exec, s[0:1]
	s_waitcnt lgkmcnt(0)
	v_pk_fma_f32 v[86:87], v[78:79], v[84:85], v[84:85] op_sel:[0,1,0] op_sel_hi:[1,1,0]
	v_pk_fma_f32 v[78:79], v[80:81], v[84:85], v[84:85] op_sel:[0,1,0] op_sel_hi:[1,1,0]
	v_pk_fma_f32 v[80:81], v[134:135], v[86:87], v[142:143]
	v_pk_fma_f32 v[86:87], v[74:75], v[84:85], v[84:85] op_sel:[0,1,0] op_sel_hi:[1,1,0]
	v_pk_fma_f32 v[74:75], v[76:77], v[84:85], v[84:85] op_sel:[0,1,0] op_sel_hi:[1,1,0]
	v_pk_fma_f32 v[78:79], v[136:137], v[78:79], v[144:145]
	v_pk_fma_f32 v[74:75], v[132:133], v[74:75], v[140:141]
	v_pk_fma_f32 v[76:77], v[130:131], v[86:87], v[138:139]
	v_cvt_pk_bf16_f32 v84, v80, v81
	v_cvt_pk_bf16_f32 v85, v78, v79
	s_nop 0
	v_cvt_pk_bf16_f32 v86, v76, v77
	v_cvt_pk_bf16_f32 v87, v74, v75
	global_store_dwordx4 v[88:89], v[84:87], off
	s_cbranch_vccnz .LBB0_374
	v_mul_f32_e32 v80, s5, v80
	v_mul_f32_e32 v81, s5, v81
	v_mul_f32_e32 v84, s5, v78
	v_med3_f32 v80, v80, s33, v236
	v_med3_f32 v81, v81, s33, v236
	s_nop 0
	v_cvt_pk_fp8_f32 v78, v80, v81
	v_mul_f32_e32 v79, s5, v79
	v_med3_f32 v80, v84, s33, v236
	v_med3_f32 v79, v79, s33, v236
	v_mul_f32_e32 v76, s5, v76
	v_mul_f32_e32 v77, s5, v77
	v_cvt_pk_fp8_f32 v78, v80, v79 op_sel:[0,0,1]
	v_med3_f32 v76, v76, s33, v236
	v_med3_f32 v77, v77, s33, v236
	s_nop 0
	v_cvt_pk_fp8_f32 v79, v76, v77
	v_mul_f32_e32 v74, s5, v74
	v_mul_f32_e32 v75, s5, v75
	v_med3_f32 v74, v74, s33, v236
	v_med3_f32 v75, v75, s33, v236
	v_cvt_pk_fp8_f32 v79, v74, v75 op_sel:[0,0,1]
	v_lshl_add_u64 v[74:75], s[6:7], 0, v[82:83]
	global_store_dwordx2 v[74:75], v[78:79], off
.LBB0_374:
	ds_read_b64 v[76:77], v0 offset:8576
	v_lshlrev_b64 v[98:99], 11, v[172:173]
	v_lshl_add_u64 v[74:75], v[98:99], 0, v[170:171]
	v_lshl_add_u64 v[80:81], v[74:75], 1, s[30:31]
	s_and_b64 vcc, exec, s[0:1]
	s_waitcnt lgkmcnt(0)
	v_pk_fma_f32 v[78:79], v[70:71], v[76:77], v[76:77] op_sel:[0,1,0] op_sel_hi:[1,1,0]
	v_pk_fma_f32 v[70:71], v[72:73], v[76:77], v[76:77] op_sel:[0,1,0] op_sel_hi:[1,1,0]
	v_pk_fma_f32 v[72:73], v[134:135], v[78:79], v[142:143]
	v_pk_fma_f32 v[78:79], v[66:67], v[76:77], v[76:77] op_sel:[0,1,0] op_sel_hi:[1,1,0]
	v_pk_fma_f32 v[66:67], v[68:69], v[76:77], v[76:77] op_sel:[0,1,0] op_sel_hi:[1,1,0]
	v_pk_fma_f32 v[70:71], v[136:137], v[70:71], v[144:145]
	v_pk_fma_f32 v[66:67], v[132:133], v[66:67], v[140:141]
	v_pk_fma_f32 v[68:69], v[130:131], v[78:79], v[138:139]
	v_cvt_pk_bf16_f32 v76, v72, v73
	v_cvt_pk_bf16_f32 v77, v70, v71
	s_nop 0
	v_cvt_pk_bf16_f32 v78, v68, v69
	v_cvt_pk_bf16_f32 v79, v66, v67
	global_store_dwordx4 v[80:81], v[76:79], off
	s_cbranch_vccnz .LBB0_376
	v_mul_f32_e32 v72, s5, v72
	v_mul_f32_e32 v73, s5, v73
	v_mul_f32_e32 v76, s5, v70
	v_med3_f32 v72, v72, s33, v236
	v_med3_f32 v73, v73, s33, v236
	s_nop 0
	v_cvt_pk_fp8_f32 v70, v72, v73
	v_mul_f32_e32 v71, s5, v71
	v_med3_f32 v72, v76, s33, v236
	v_med3_f32 v71, v71, s33, v236
	v_mul_f32_e32 v68, s5, v68
	v_mul_f32_e32 v69, s5, v69
	v_cvt_pk_fp8_f32 v70, v72, v71 op_sel:[0,0,1]
	v_med3_f32 v68, v68, s33, v236
	v_med3_f32 v69, v69, s33, v236
	s_nop 0
	v_cvt_pk_fp8_f32 v71, v68, v69
	v_mul_f32_e32 v66, s5, v66
	v_mul_f32_e32 v67, s5, v67
	v_med3_f32 v66, v66, s33, v236
	v_med3_f32 v67, v67, s33, v236
	v_cvt_pk_fp8_f32 v71, v66, v67 op_sel:[0,0,1]
	v_lshl_add_u64 v[66:67], s[6:7], 0, v[74:75]
	global_store_dwordx2 v[66:67], v[70:71], off
.LBB0_376:
	ds_read_b64 v[68:69], v0 offset:9216
	v_lshlrev_b64 v[88:89], 11, v[154:155]
	v_lshl_add_u64 v[66:67], v[88:89], 0, v[170:171]
	v_lshl_add_u64 v[80:81], v[66:67], 1, s[30:31]
	s_and_b64 vcc, exec, s[0:1]
	s_waitcnt lgkmcnt(0)
	v_pk_fma_f32 v[72:73], v[126:127], v[68:69], v[68:69] op_sel:[0,1,0] op_sel_hi:[1,1,0]
	v_pk_fma_f32 v[70:71], v[128:129], v[68:69], v[68:69] op_sel:[0,1,0] op_sel_hi:[1,1,0]
	v_pk_fma_f32 v[74:75], v[134:135], v[72:73], v[142:143]
	v_pk_fma_f32 v[72:73], v[122:123], v[68:69], v[68:69] op_sel:[0,1,0] op_sel_hi:[1,1,0]
	v_pk_fma_f32 v[68:69], v[124:125], v[68:69], v[68:69] op_sel:[0,1,0] op_sel_hi:[1,1,0]
	v_pk_fma_f32 v[70:71], v[136:137], v[70:71], v[144:145]
	v_pk_fma_f32 v[68:69], v[132:133], v[68:69], v[140:141]
	v_pk_fma_f32 v[72:73], v[130:131], v[72:73], v[138:139]
	v_cvt_pk_bf16_f32 v76, v74, v75
	v_cvt_pk_bf16_f32 v77, v70, v71
	s_nop 0
	v_cvt_pk_bf16_f32 v78, v72, v73
	v_cvt_pk_bf16_f32 v79, v68, v69
	global_store_dwordx4 v[80:81], v[76:79], off
	s_cbranch_vccnz .LBB0_378
	v_mul_f32_e32 v74, s5, v74
	v_mul_f32_e32 v75, s5, v75
	v_mul_f32_e32 v76, s5, v70
	v_med3_f32 v74, v74, s33, v236
	v_med3_f32 v75, v75, s33, v236
	s_nop 0
	v_cvt_pk_fp8_f32 v70, v74, v75
	v_mul_f32_e32 v71, s5, v71
	v_med3_f32 v74, v76, s33, v236
	v_med3_f32 v71, v71, s33, v236
	v_cvt_pk_fp8_f32 v70, v74, v71 op_sel:[0,0,1]
	v_mul_f32_e32 v71, s5, v72
	v_mul_f32_e32 v72, s5, v73
	v_med3_f32 v73, v71, s33, v236
	v_med3_f32 v72, v72, s33, v236
	s_nop 0
	v_cvt_pk_fp8_f32 v71, v73, v72
	v_mul_f32_e32 v68, s5, v68
	v_mul_f32_e32 v69, s5, v69
	v_med3_f32 v68, v68, s33, v236
	v_med3_f32 v69, v69, s33, v236
	v_cvt_pk_fp8_f32 v71, v68, v69 op_sel:[0,0,1]
	v_lshl_add_u64 v[66:67], s[6:7], 0, v[66:67]
	global_store_dwordx2 v[66:67], v[70:71], off
.LBB0_378:
	ds_read_b64 v[68:69], v0 offset:9344
	v_lshlrev_b64 v[86:87], 11, v[160:161]
	v_lshl_add_u64 v[66:67], v[86:87], 0, v[170:171]
	v_lshl_add_u64 v[80:81], v[66:67], 1, s[30:31]
	s_and_b64 vcc, exec, s[0:1]
	s_waitcnt lgkmcnt(0)
	v_pk_fma_f32 v[72:73], v[118:119], v[68:69], v[68:69] op_sel:[0,1,0] op_sel_hi:[1,1,0]
	v_pk_fma_f32 v[70:71], v[120:121], v[68:69], v[68:69] op_sel:[0,1,0] op_sel_hi:[1,1,0]
	v_pk_fma_f32 v[74:75], v[134:135], v[72:73], v[142:143]
	v_pk_fma_f32 v[72:73], v[114:115], v[68:69], v[68:69] op_sel:[0,1,0] op_sel_hi:[1,1,0]
	v_pk_fma_f32 v[68:69], v[116:117], v[68:69], v[68:69] op_sel:[0,1,0] op_sel_hi:[1,1,0]
	v_pk_fma_f32 v[70:71], v[136:137], v[70:71], v[144:145]
	v_pk_fma_f32 v[68:69], v[132:133], v[68:69], v[140:141]
	v_pk_fma_f32 v[72:73], v[130:131], v[72:73], v[138:139]
	v_cvt_pk_bf16_f32 v76, v74, v75
	v_cvt_pk_bf16_f32 v77, v70, v71
	s_nop 0
	v_cvt_pk_bf16_f32 v78, v72, v73
	v_cvt_pk_bf16_f32 v79, v68, v69
	global_store_dwordx4 v[80:81], v[76:79], off
	s_cbranch_vccnz .LBB0_380
	v_mul_f32_e32 v74, s5, v74
	v_mul_f32_e32 v75, s5, v75
	v_mul_f32_e32 v76, s5, v70
	v_med3_f32 v74, v74, s33, v236
	v_med3_f32 v75, v75, s33, v236
	s_nop 0
	v_cvt_pk_fp8_f32 v70, v74, v75
	v_mul_f32_e32 v71, s5, v71
	v_med3_f32 v74, v76, s33, v236
	v_med3_f32 v71, v71, s33, v236
	v_cvt_pk_fp8_f32 v70, v74, v71 op_sel:[0,0,1]
	v_mul_f32_e32 v71, s5, v72
	v_mul_f32_e32 v72, s5, v73
	v_med3_f32 v73, v71, s33, v236
	v_med3_f32 v72, v72, s33, v236
	s_nop 0
	v_cvt_pk_fp8_f32 v71, v73, v72
	v_mul_f32_e32 v68, s5, v68
	v_mul_f32_e32 v69, s5, v69
	v_med3_f32 v68, v68, s33, v236
	v_med3_f32 v69, v69, s33, v236
	v_cvt_pk_fp8_f32 v71, v68, v69 op_sel:[0,0,1]
	v_lshl_add_u64 v[66:67], s[6:7], 0, v[66:67]
	global_store_dwordx2 v[66:67], v[70:71], off
.LBB0_380:
	ds_read_b64 v[68:69], v0 offset:9472
	v_lshlrev_b64 v[84:85], 11, v[158:159]
	v_lshl_add_u64 v[66:67], v[84:85], 0, v[170:171]
	v_lshl_add_u64 v[80:81], v[66:67], 1, s[30:31]
	s_and_b64 vcc, exec, s[0:1]
	s_waitcnt lgkmcnt(0)
	v_pk_fma_f32 v[72:73], v[110:111], v[68:69], v[68:69] op_sel:[0,1,0] op_sel_hi:[1,1,0]
	v_pk_fma_f32 v[70:71], v[112:113], v[68:69], v[68:69] op_sel:[0,1,0] op_sel_hi:[1,1,0]
	v_pk_fma_f32 v[74:75], v[134:135], v[72:73], v[142:143]
	v_pk_fma_f32 v[72:73], v[106:107], v[68:69], v[68:69] op_sel:[0,1,0] op_sel_hi:[1,1,0]
	v_pk_fma_f32 v[68:69], v[108:109], v[68:69], v[68:69] op_sel:[0,1,0] op_sel_hi:[1,1,0]
	v_pk_fma_f32 v[70:71], v[136:137], v[70:71], v[144:145]
	v_pk_fma_f32 v[68:69], v[132:133], v[68:69], v[140:141]
	v_pk_fma_f32 v[72:73], v[130:131], v[72:73], v[138:139]
	v_cvt_pk_bf16_f32 v76, v74, v75
	v_cvt_pk_bf16_f32 v77, v70, v71
	s_nop 0
	v_cvt_pk_bf16_f32 v78, v72, v73
	v_cvt_pk_bf16_f32 v79, v68, v69
	global_store_dwordx4 v[80:81], v[76:79], off
	s_cbranch_vccnz .LBB0_382
	v_mul_f32_e32 v74, s5, v74
	v_mul_f32_e32 v75, s5, v75
	v_mul_f32_e32 v76, s5, v70
	v_med3_f32 v74, v74, s33, v236
	v_med3_f32 v75, v75, s33, v236
	s_nop 0
	v_cvt_pk_fp8_f32 v70, v74, v75
	v_mul_f32_e32 v71, s5, v71
	v_med3_f32 v74, v76, s33, v236
	v_med3_f32 v71, v71, s33, v236
	v_cvt_pk_fp8_f32 v70, v74, v71 op_sel:[0,0,1]
	v_mul_f32_e32 v71, s5, v72
	v_mul_f32_e32 v72, s5, v73
	v_med3_f32 v73, v71, s33, v236
	v_med3_f32 v72, v72, s33, v236
	s_nop 0
	v_cvt_pk_fp8_f32 v71, v73, v72
	v_mul_f32_e32 v68, s5, v68
	v_mul_f32_e32 v69, s5, v69
	v_med3_f32 v68, v68, s33, v236
	v_med3_f32 v69, v69, s33, v236
	v_cvt_pk_fp8_f32 v71, v68, v69 op_sel:[0,0,1]
	v_lshl_add_u64 v[66:67], s[6:7], 0, v[66:67]
	global_store_dwordx2 v[66:67], v[70:71], off
.LBB0_382:
	ds_read_b64 v[68:69], v0 offset:9600
	v_lshlrev_b64 v[82:83], 11, v[156:157]
	v_lshl_add_u64 v[66:67], v[82:83], 0, v[170:171]
	v_lshl_add_u64 v[80:81], v[66:67], 1, s[30:31]
	s_and_b64 vcc, exec, s[0:1]
	s_waitcnt lgkmcnt(0)
	v_pk_fma_f32 v[72:73], v[94:95], v[68:69], v[68:69] op_sel:[0,1,0] op_sel_hi:[1,1,0]
	v_pk_fma_f32 v[70:71], v[96:97], v[68:69], v[68:69] op_sel:[0,1,0] op_sel_hi:[1,1,0]
	v_pk_fma_f32 v[74:75], v[134:135], v[72:73], v[142:143]
	v_pk_fma_f32 v[72:73], v[90:91], v[68:69], v[68:69] op_sel:[0,1,0] op_sel_hi:[1,1,0]
	v_pk_fma_f32 v[68:69], v[92:93], v[68:69], v[68:69] op_sel:[0,1,0] op_sel_hi:[1,1,0]
	v_pk_fma_f32 v[70:71], v[136:137], v[70:71], v[144:145]
	v_pk_fma_f32 v[68:69], v[132:133], v[68:69], v[140:141]
	v_pk_fma_f32 v[72:73], v[130:131], v[72:73], v[138:139]
	v_cvt_pk_bf16_f32 v76, v74, v75
	v_cvt_pk_bf16_f32 v77, v70, v71
	s_nop 0
	v_cvt_pk_bf16_f32 v78, v72, v73
	v_cvt_pk_bf16_f32 v79, v68, v69
	global_store_dwordx4 v[80:81], v[76:79], off
	s_cbranch_vccnz .LBB0_384
	v_mul_f32_e32 v74, s5, v74
	v_mul_f32_e32 v75, s5, v75
	v_mul_f32_e32 v76, s5, v70
	v_med3_f32 v74, v74, s33, v236
	v_med3_f32 v75, v75, s33, v236
	s_nop 0
	v_cvt_pk_fp8_f32 v70, v74, v75
	v_mul_f32_e32 v71, s5, v71
	v_med3_f32 v74, v76, s33, v236
	v_med3_f32 v71, v71, s33, v236
	v_cvt_pk_fp8_f32 v70, v74, v71 op_sel:[0,0,1]
	v_mul_f32_e32 v71, s5, v72
	v_mul_f32_e32 v72, s5, v73
	v_med3_f32 v73, v71, s33, v236
	v_med3_f32 v72, v72, s33, v236
	s_nop 0
	v_cvt_pk_fp8_f32 v71, v73, v72
	v_mul_f32_e32 v68, s5, v68
	v_mul_f32_e32 v69, s5, v69
	v_med3_f32 v68, v68, s33, v236
	v_med3_f32 v69, v69, s33, v236
	v_cvt_pk_fp8_f32 v71, v68, v69 op_sel:[0,0,1]
	v_lshl_add_u64 v[66:67], s[6:7], 0, v[66:67]
	global_store_dwordx2 v[66:67], v[70:71], off
.LBB0_384:
	global_load_dwordx4 v[66:69], v[150:151], off offset:528
	global_load_dwordx4 v[74:77], v[150:151], off offset:512
	global_load_dwordx4 v[70:73], v[148:149], off offset:528
	global_load_dwordx4 v[78:81], v[148:149], off offset:512
	ds_read_b64 v[94:95], v0 offset:8192
	s_mov_b64 s[8:9], 0x80
	v_lshl_add_u64 v[90:91], v[170:171], 0, s[8:9]
	v_lshl_add_u64 v[92:93], v[146:147], 0, v[90:91]
	v_lshl_add_u64 v[104:105], v[92:93], 1, s[30:31]
	s_waitcnt lgkmcnt(0)
	v_pk_fma_f32 v[96:97], v[38:39], v[94:95], v[94:95] op_sel:[0,1,0] op_sel_hi:[1,1,0]
	v_pk_fma_f32 v[38:39], v[40:41], v[94:95], v[94:95] op_sel:[0,1,0] op_sel_hi:[1,1,0]
	s_and_b64 vcc, exec, s[0:1]
	s_waitcnt vmcnt(0)
	v_pk_fma_f32 v[40:41], v[74:75], v[96:97], v[78:79]
	v_pk_fma_f32 v[96:97], v[34:35], v[94:95], v[94:95] op_sel:[0,1,0] op_sel_hi:[1,1,0]
	v_pk_fma_f32 v[34:35], v[36:37], v[94:95], v[94:95] op_sel:[0,1,0] op_sel_hi:[1,1,0]
	v_pk_fma_f32 v[38:39], v[76:77], v[38:39], v[80:81]
	v_pk_fma_f32 v[34:35], v[68:69], v[34:35], v[72:73]
	v_pk_fma_f32 v[36:37], v[66:67], v[96:97], v[70:71]
	v_cvt_pk_bf16_f32 v94, v40, v41
	v_cvt_pk_bf16_f32 v95, v38, v39
	s_nop 0
	v_cvt_pk_bf16_f32 v96, v36, v37
	v_cvt_pk_bf16_f32 v97, v34, v35
	global_store_dwordx4 v[104:105], v[94:97], off
	s_cbranch_vccnz .LBB0_386
	v_mul_f32_e32 v40, s5, v40
	v_mul_f32_e32 v41, s5, v41
	v_mul_f32_e32 v94, s5, v38
	v_med3_f32 v40, v40, s33, v236
	v_med3_f32 v41, v41, s33, v236
	s_nop 0
	v_cvt_pk_fp8_f32 v38, v40, v41
	v_mul_f32_e32 v39, s5, v39
	v_med3_f32 v40, v94, s33, v236
	v_med3_f32 v39, v39, s33, v236
	v_mul_f32_e32 v36, s5, v36
	v_mul_f32_e32 v37, s5, v37
	v_cvt_pk_fp8_f32 v38, v40, v39 op_sel:[0,0,1]
	v_med3_f32 v36, v36, s33, v236
	v_med3_f32 v37, v37, s33, v236
	s_nop 0
	v_cvt_pk_fp8_f32 v39, v36, v37
	v_mul_f32_e32 v34, s5, v34
	v_mul_f32_e32 v35, s5, v35
	v_med3_f32 v34, v34, s33, v236
	v_med3_f32 v35, v35, s33, v236
	v_cvt_pk_fp8_f32 v39, v34, v35 op_sel:[0,0,1]
	v_lshl_add_u64 v[34:35], s[6:7], 0, v[92:93]
	global_store_dwordx2 v[34:35], v[38:39], off
.LBB0_386:
	ds_read_b64 v[36:37], v0 offset:8320
	v_lshl_add_u64 v[34:35], v[102:103], 0, v[90:91]
	s_and_b64 vcc, exec, s[0:1]
	s_waitcnt lgkmcnt(0)
	v_pk_fma_f32 v[38:39], v[22:23], v[36:37], v[36:37] op_sel:[0,1,0] op_sel_hi:[1,1,0]
	v_pk_fma_f32 v[22:23], v[24:25], v[36:37], v[36:37] op_sel:[0,1,0] op_sel_hi:[1,1,0]
	v_pk_fma_f32 v[40:41], v[18:19], v[36:37], v[36:37] op_sel:[0,1,0] op_sel_hi:[1,1,0]
	v_pk_fma_f32 v[18:19], v[20:21], v[36:37], v[36:37] op_sel:[0,1,0] op_sel_hi:[1,1,0]
	v_pk_fma_f32 v[22:23], v[76:77], v[22:23], v[80:81]
	v_pk_fma_f32 v[24:25], v[74:75], v[38:39], v[78:79]
	v_pk_fma_f32 v[18:19], v[68:69], v[18:19], v[72:73]
	v_pk_fma_f32 v[20:21], v[66:67], v[40:41], v[70:71]
	v_lshl_add_u64 v[40:41], v[34:35], 1, s[30:31]
	v_cvt_pk_bf16_f32 v36, v24, v25
	v_cvt_pk_bf16_f32 v37, v22, v23
	v_cvt_pk_bf16_f32 v38, v20, v21
	v_cvt_pk_bf16_f32 v39, v18, v19
	global_store_dwordx4 v[40:41], v[36:39], off
	s_cbranch_vccnz .LBB0_388
	v_mul_f32_e32 v24, s5, v24
	v_mul_f32_e32 v25, s5, v25
	v_mul_f32_e32 v36, s5, v22
	v_med3_f32 v24, v24, s33, v236
	v_med3_f32 v25, v25, s33, v236
	s_nop 0
	v_cvt_pk_fp8_f32 v22, v24, v25
	v_mul_f32_e32 v23, s5, v23
	v_med3_f32 v24, v36, s33, v236
	v_med3_f32 v23, v23, s33, v236
	v_mul_f32_e32 v20, s5, v20
	v_mul_f32_e32 v21, s5, v21
	v_cvt_pk_fp8_f32 v22, v24, v23 op_sel:[0,0,1]
	v_med3_f32 v20, v20, s33, v236
	v_med3_f32 v21, v21, s33, v236
	s_nop 0
	v_cvt_pk_fp8_f32 v23, v20, v21
	v_mul_f32_e32 v18, s5, v18
	v_mul_f32_e32 v19, s5, v19
	v_med3_f32 v18, v18, s33, v236
	v_med3_f32 v19, v19, s33, v236
	v_cvt_pk_fp8_f32 v23, v18, v19 op_sel:[0,0,1]
	v_lshl_add_u64 v[18:19], s[6:7], 0, v[34:35]
	global_store_dwordx2 v[18:19], v[22:23], off
.LBB0_388:
	ds_read_b64 v[20:21], v0 offset:8448
	v_lshl_add_u64 v[18:19], v[100:101], 0, v[90:91]
	s_and_b64 vcc, exec, s[0:1]
	s_waitcnt lgkmcnt(0)
	v_pk_fma_f32 v[22:23], v[14:15], v[20:21], v[20:21] op_sel:[0,1,0] op_sel_hi:[1,1,0]
	v_pk_fma_f32 v[14:15], v[16:17], v[20:21], v[20:21] op_sel:[0,1,0] op_sel_hi:[1,1,0]
	v_pk_fma_f32 v[24:25], v[10:11], v[20:21], v[20:21] op_sel:[0,1,0] op_sel_hi:[1,1,0]
	v_pk_fma_f32 v[10:11], v[12:13], v[20:21], v[20:21] op_sel:[0,1,0] op_sel_hi:[1,1,0]
	v_pk_fma_f32 v[14:15], v[76:77], v[14:15], v[80:81]
	v_pk_fma_f32 v[16:17], v[74:75], v[22:23], v[78:79]
	v_pk_fma_f32 v[10:11], v[68:69], v[10:11], v[72:73]
	v_pk_fma_f32 v[12:13], v[66:67], v[24:25], v[70:71]
	v_lshl_add_u64 v[24:25], v[18:19], 1, s[30:31]
	v_cvt_pk_bf16_f32 v20, v16, v17
	v_cvt_pk_bf16_f32 v21, v14, v15
	v_cvt_pk_bf16_f32 v22, v12, v13
	v_cvt_pk_bf16_f32 v23, v10, v11
	global_store_dwordx4 v[24:25], v[20:23], off
	s_cbranch_vccnz .LBB0_390
	v_mul_f32_e32 v16, s5, v16
	v_mul_f32_e32 v17, s5, v17
	v_mul_f32_e32 v20, s5, v14
	v_med3_f32 v16, v16, s33, v236
	v_med3_f32 v17, v17, s33, v236
	s_nop 0
	v_cvt_pk_fp8_f32 v14, v16, v17
	v_mul_f32_e32 v15, s5, v15
	v_med3_f32 v16, v20, s33, v236
	v_med3_f32 v15, v15, s33, v236
	v_mul_f32_e32 v12, s5, v12
	v_mul_f32_e32 v13, s5, v13
	v_cvt_pk_fp8_f32 v14, v16, v15 op_sel:[0,0,1]
	v_med3_f32 v12, v12, s33, v236
	v_med3_f32 v13, v13, s33, v236
	s_nop 0
	v_cvt_pk_fp8_f32 v15, v12, v13
	v_mul_f32_e32 v10, s5, v10
	v_mul_f32_e32 v11, s5, v11
	v_med3_f32 v10, v10, s33, v236
	v_med3_f32 v11, v11, s33, v236
	v_cvt_pk_fp8_f32 v15, v10, v11 op_sel:[0,0,1]
	v_lshl_add_u64 v[10:11], s[6:7], 0, v[18:19]
	global_store_dwordx2 v[10:11], v[14:15], off
.LBB0_390:
	ds_read_b64 v[12:13], v0 offset:8576
	v_lshl_add_u64 v[10:11], v[98:99], 0, v[90:91]
	s_and_b64 vcc, exec, s[0:1]
	s_waitcnt lgkmcnt(0)
	v_pk_fma_f32 v[14:15], v[6:7], v[12:13], v[12:13] op_sel:[0,1,0] op_sel_hi:[1,1,0]
	v_pk_fma_f32 v[6:7], v[8:9], v[12:13], v[12:13] op_sel:[0,1,0] op_sel_hi:[1,1,0]
	v_pk_fma_f32 v[16:17], v[2:3], v[12:13], v[12:13] op_sel:[0,1,0] op_sel_hi:[1,1,0]
	v_pk_fma_f32 v[2:3], v[4:5], v[12:13], v[12:13] op_sel:[0,1,0] op_sel_hi:[1,1,0]
	v_pk_fma_f32 v[6:7], v[76:77], v[6:7], v[80:81]
	v_pk_fma_f32 v[8:9], v[74:75], v[14:15], v[78:79]
	v_pk_fma_f32 v[2:3], v[68:69], v[2:3], v[72:73]
	v_pk_fma_f32 v[4:5], v[66:67], v[16:17], v[70:71]
	v_lshl_add_u64 v[16:17], v[10:11], 1, s[30:31]
	v_cvt_pk_bf16_f32 v12, v8, v9
	v_cvt_pk_bf16_f32 v13, v6, v7
	v_cvt_pk_bf16_f32 v14, v4, v5
	v_cvt_pk_bf16_f32 v15, v2, v3
	global_store_dwordx4 v[16:17], v[12:15], off
	s_cbranch_vccnz .LBB0_392
	v_mul_f32_e32 v8, s5, v8
	v_mul_f32_e32 v9, s5, v9
	v_mul_f32_e32 v12, s5, v6
	v_med3_f32 v8, v8, s33, v236
	v_med3_f32 v9, v9, s33, v236
	s_nop 0
	v_cvt_pk_fp8_f32 v6, v8, v9
	v_mul_f32_e32 v7, s5, v7
	v_med3_f32 v8, v12, s33, v236
	v_med3_f32 v7, v7, s33, v236
	v_mul_f32_e32 v4, s5, v4
	v_mul_f32_e32 v5, s5, v5
	v_cvt_pk_fp8_f32 v6, v8, v7 op_sel:[0,0,1]
	v_med3_f32 v4, v4, s33, v236
	v_med3_f32 v5, v5, s33, v236
	s_nop 0
	v_cvt_pk_fp8_f32 v7, v4, v5
	v_mul_f32_e32 v2, s5, v2
	v_mul_f32_e32 v3, s5, v3
	v_med3_f32 v2, v2, s33, v236
	v_med3_f32 v3, v3, s33, v236
	v_cvt_pk_fp8_f32 v7, v2, v3 op_sel:[0,0,1]
	v_lshl_add_u64 v[2:3], s[6:7], 0, v[10:11]
	global_store_dwordx2 v[2:3], v[6:7], off
.LBB0_392:
	ds_read_b64 v[4:5], v0 offset:9216
	v_lshl_add_u64 v[2:3], v[88:89], 0, v[90:91]
	v_lshl_add_u64 v[16:17], v[2:3], 1, s[30:31]
	s_and_b64 vcc, exec, s[0:1]
	s_waitcnt lgkmcnt(0)
	v_pk_fma_f32 v[8:9], v[62:63], v[4:5], v[4:5] op_sel:[0,1,0] op_sel_hi:[1,1,0]
	v_pk_fma_f32 v[6:7], v[64:65], v[4:5], v[4:5] op_sel:[0,1,0] op_sel_hi:[1,1,0]
	v_pk_fma_f32 v[12:13], v[58:59], v[4:5], v[4:5] op_sel:[0,1,0] op_sel_hi:[1,1,0]
	v_pk_fma_f32 v[4:5], v[60:61], v[4:5], v[4:5] op_sel:[0,1,0] op_sel_hi:[1,1,0]
	v_pk_fma_f32 v[6:7], v[76:77], v[6:7], v[80:81]
	v_pk_fma_f32 v[10:11], v[74:75], v[8:9], v[78:79]
	v_pk_fma_f32 v[4:5], v[68:69], v[4:5], v[72:73]
	v_pk_fma_f32 v[8:9], v[66:67], v[12:13], v[70:71]
	v_cvt_pk_bf16_f32 v12, v10, v11
	v_cvt_pk_bf16_f32 v13, v6, v7
	s_nop 0
	v_cvt_pk_bf16_f32 v14, v8, v9
	v_cvt_pk_bf16_f32 v15, v4, v5
	global_store_dwordx4 v[16:17], v[12:15], off
	s_cbranch_vccnz .LBB0_394
	v_mul_f32_e32 v10, s5, v10
	v_mul_f32_e32 v11, s5, v11
	v_mul_f32_e32 v12, s5, v6
	v_med3_f32 v10, v10, s33, v236
	v_med3_f32 v11, v11, s33, v236
	s_nop 0
	v_cvt_pk_fp8_f32 v6, v10, v11
	v_mul_f32_e32 v7, s5, v7
	v_med3_f32 v10, v12, s33, v236
	v_med3_f32 v7, v7, s33, v236
	v_cvt_pk_fp8_f32 v6, v10, v7 op_sel:[0,0,1]
	v_mul_f32_e32 v7, s5, v8
	v_mul_f32_e32 v8, s5, v9
	v_med3_f32 v9, v7, s33, v236
	v_med3_f32 v8, v8, s33, v236
	s_nop 0
	v_cvt_pk_fp8_f32 v7, v9, v8
	v_mul_f32_e32 v4, s5, v4
	v_mul_f32_e32 v5, s5, v5
	v_med3_f32 v4, v4, s33, v236
	v_med3_f32 v5, v5, s33, v236
	v_cvt_pk_fp8_f32 v7, v4, v5 op_sel:[0,0,1]
	v_lshl_add_u64 v[2:3], s[6:7], 0, v[2:3]
	global_store_dwordx2 v[2:3], v[6:7], off
.LBB0_394:
	ds_read_b64 v[4:5], v0 offset:9344
	v_lshl_add_u64 v[2:3], v[86:87], 0, v[90:91]
	v_lshl_add_u64 v[16:17], v[2:3], 1, s[30:31]
	s_and_b64 vcc, exec, s[0:1]
	s_waitcnt lgkmcnt(0)
	v_pk_fma_f32 v[8:9], v[54:55], v[4:5], v[4:5] op_sel:[0,1,0] op_sel_hi:[1,1,0]
	v_pk_fma_f32 v[6:7], v[56:57], v[4:5], v[4:5] op_sel:[0,1,0] op_sel_hi:[1,1,0]
	v_pk_fma_f32 v[12:13], v[50:51], v[4:5], v[4:5] op_sel:[0,1,0] op_sel_hi:[1,1,0]
	v_pk_fma_f32 v[4:5], v[52:53], v[4:5], v[4:5] op_sel:[0,1,0] op_sel_hi:[1,1,0]
	v_pk_fma_f32 v[6:7], v[76:77], v[6:7], v[80:81]
	v_pk_fma_f32 v[10:11], v[74:75], v[8:9], v[78:79]
	v_pk_fma_f32 v[4:5], v[68:69], v[4:5], v[72:73]
	v_pk_fma_f32 v[8:9], v[66:67], v[12:13], v[70:71]
	v_cvt_pk_bf16_f32 v12, v10, v11
	v_cvt_pk_bf16_f32 v13, v6, v7
	s_nop 0
	v_cvt_pk_bf16_f32 v14, v8, v9
	v_cvt_pk_bf16_f32 v15, v4, v5
	global_store_dwordx4 v[16:17], v[12:15], off
	s_cbranch_vccnz .LBB0_396
	v_mul_f32_e32 v10, s5, v10
	v_mul_f32_e32 v11, s5, v11
	v_mul_f32_e32 v12, s5, v6
	v_med3_f32 v10, v10, s33, v236
	v_med3_f32 v11, v11, s33, v236
	s_nop 0
	v_cvt_pk_fp8_f32 v6, v10, v11
	v_mul_f32_e32 v7, s5, v7
	v_med3_f32 v10, v12, s33, v236
	v_med3_f32 v7, v7, s33, v236
	v_cvt_pk_fp8_f32 v6, v10, v7 op_sel:[0,0,1]
	v_mul_f32_e32 v7, s5, v8
	v_mul_f32_e32 v8, s5, v9
	v_med3_f32 v9, v7, s33, v236
	v_med3_f32 v8, v8, s33, v236
	s_nop 0
	v_cvt_pk_fp8_f32 v7, v9, v8
	v_mul_f32_e32 v4, s5, v4
	v_mul_f32_e32 v5, s5, v5
	v_med3_f32 v4, v4, s33, v236
	v_med3_f32 v5, v5, s33, v236
	v_cvt_pk_fp8_f32 v7, v4, v5 op_sel:[0,0,1]
	v_lshl_add_u64 v[2:3], s[6:7], 0, v[2:3]
	global_store_dwordx2 v[2:3], v[6:7], off
.LBB0_396:
	ds_read_b64 v[4:5], v0 offset:9472
	v_lshl_add_u64 v[2:3], v[84:85], 0, v[90:91]
	v_lshl_add_u64 v[16:17], v[2:3], 1, s[30:31]
	s_and_b64 vcc, exec, s[0:1]
	s_waitcnt lgkmcnt(0)
	v_pk_fma_f32 v[8:9], v[46:47], v[4:5], v[4:5] op_sel:[0,1,0] op_sel_hi:[1,1,0]
	v_pk_fma_f32 v[6:7], v[48:49], v[4:5], v[4:5] op_sel:[0,1,0] op_sel_hi:[1,1,0]
	v_pk_fma_f32 v[12:13], v[42:43], v[4:5], v[4:5] op_sel:[0,1,0] op_sel_hi:[1,1,0]
	v_pk_fma_f32 v[4:5], v[44:45], v[4:5], v[4:5] op_sel:[0,1,0] op_sel_hi:[1,1,0]
	v_pk_fma_f32 v[6:7], v[76:77], v[6:7], v[80:81]
	v_pk_fma_f32 v[10:11], v[74:75], v[8:9], v[78:79]
	v_pk_fma_f32 v[4:5], v[68:69], v[4:5], v[72:73]
	v_pk_fma_f32 v[8:9], v[66:67], v[12:13], v[70:71]
	v_cvt_pk_bf16_f32 v12, v10, v11
	v_cvt_pk_bf16_f32 v13, v6, v7
	s_nop 0
	v_cvt_pk_bf16_f32 v14, v8, v9
	v_cvt_pk_bf16_f32 v15, v4, v5
	global_store_dwordx4 v[16:17], v[12:15], off
	s_cbranch_vccnz .LBB0_398
	v_mul_f32_e32 v10, s5, v10
	v_mul_f32_e32 v11, s5, v11
	v_mul_f32_e32 v12, s5, v6
	v_med3_f32 v10, v10, s33, v236
	v_med3_f32 v11, v11, s33, v236
	s_nop 0
	v_cvt_pk_fp8_f32 v6, v10, v11
	v_mul_f32_e32 v7, s5, v7
	v_med3_f32 v10, v12, s33, v236
	v_med3_f32 v7, v7, s33, v236
	v_cvt_pk_fp8_f32 v6, v10, v7 op_sel:[0,0,1]
	v_mul_f32_e32 v7, s5, v8
	v_mul_f32_e32 v8, s5, v9
	v_med3_f32 v9, v7, s33, v236
	v_med3_f32 v8, v8, s33, v236
	s_nop 0
	v_cvt_pk_fp8_f32 v7, v9, v8
	v_mul_f32_e32 v4, s5, v4
	v_mul_f32_e32 v5, s5, v5
	v_med3_f32 v4, v4, s33, v236
	v_med3_f32 v5, v5, s33, v236
	v_cvt_pk_fp8_f32 v7, v4, v5 op_sel:[0,0,1]
	v_lshl_add_u64 v[2:3], s[6:7], 0, v[2:3]
	global_store_dwordx2 v[2:3], v[6:7], off
.LBB0_398:
	ds_read_b64 v[4:5], v0 offset:9600
	v_lshl_add_u64 v[2:3], v[82:83], 0, v[90:91]
	v_lshl_add_u64 v[16:17], v[2:3], 1, s[30:31]
	s_and_b64 vcc, exec, s[0:1]
	s_waitcnt lgkmcnt(0)
	v_pk_fma_f32 v[8:9], v[30:31], v[4:5], v[4:5] op_sel:[0,1,0] op_sel_hi:[1,1,0]
	v_pk_fma_f32 v[6:7], v[32:33], v[4:5], v[4:5] op_sel:[0,1,0] op_sel_hi:[1,1,0]
	v_pk_fma_f32 v[12:13], v[26:27], v[4:5], v[4:5] op_sel:[0,1,0] op_sel_hi:[1,1,0]
	v_pk_fma_f32 v[4:5], v[28:29], v[4:5], v[4:5] op_sel:[0,1,0] op_sel_hi:[1,1,0]
	v_pk_fma_f32 v[6:7], v[76:77], v[6:7], v[80:81]
	v_pk_fma_f32 v[10:11], v[74:75], v[8:9], v[78:79]
	v_pk_fma_f32 v[4:5], v[68:69], v[4:5], v[72:73]
	v_pk_fma_f32 v[8:9], v[66:67], v[12:13], v[70:71]
	v_cvt_pk_bf16_f32 v12, v10, v11
	v_cvt_pk_bf16_f32 v13, v6, v7
	s_nop 0
	v_cvt_pk_bf16_f32 v14, v8, v9
	v_cvt_pk_bf16_f32 v15, v4, v5
	global_store_dwordx4 v[16:17], v[12:15], off
	s_cbranch_vccnz .LBB0_400
	v_mul_f32_e32 v0, s5, v10
	v_mul_f32_e32 v10, s5, v11
	v_mul_f32_e32 v11, s5, v6
	v_med3_f32 v0, v0, s33, v236
	v_med3_f32 v10, v10, s33, v236
	s_nop 0
	v_cvt_pk_fp8_f32 v6, v0, v10
	v_mul_f32_e32 v0, s5, v7
	v_med3_f32 v7, v11, s33, v236
	v_med3_f32 v0, v0, s33, v236
	v_cvt_pk_fp8_f32 v6, v7, v0 op_sel:[0,0,1]
	v_mul_f32_e32 v0, s5, v8
	v_mul_f32_e32 v7, s5, v9
	v_med3_f32 v0, v0, s33, v236
	v_med3_f32 v8, v7, s33, v236
	s_nop 0
	v_cvt_pk_fp8_f32 v7, v0, v8
	v_mul_f32_e32 v4, s5, v4
	v_mul_f32_e32 v0, s5, v5
	v_med3_f32 v4, v4, s33, v236
	v_med3_f32 v0, v0, s33, v236
	v_cvt_pk_fp8_f32 v7, v4, v0 op_sel:[0,0,1]
	v_lshl_add_u64 v[2:3], s[6:7], 0, v[2:3]
	global_store_dwordx2 v[2:3], v[6:7], off

.LBB0_451:
	s_and_b64 vcc, exec, s[18:19]
	s_cbranch_vccz .LBB0_453
	v_mul_f32_e32 v136, s5, v136
	v_mul_f32_e32 v137, s5, v137
	v_mul_f32_e32 v154, s5, v134
	v_med3_f32 v136, v136, s33, v236
	v_med3_f32 v137, v137, s33, v236
	s_nop 0
	v_cvt_pk_fp8_f32 v134, v136, v137
	v_mul_f32_e32 v135, s5, v135
	v_med3_f32 v136, v154, s33, v236
	v_med3_f32 v135, v135, s33, v236
	v_mul_f32_e32 v132, s5, v132
	v_mul_f32_e32 v133, s5, v133
	v_cvt_pk_fp8_f32 v134, v136, v135 op_sel:[0,0,1]
	v_med3_f32 v132, v132, s33, v236
	v_med3_f32 v133, v133, s33, v236
	s_nop 0
	v_cvt_pk_fp8_f32 v135, v132, v133
	v_mul_f32_e32 v130, s5, v130
	v_mul_f32_e32 v131, s5, v131
	v_med3_f32 v130, v130, s33, v236
	v_med3_f32 v131, v131, s33, v236
	v_cvt_pk_fp8_f32 v135, v130, v131 op_sel:[0,0,1]
	v_lshl_add_u64 v[130:131], s[6:7], 0, v[152:153]
	global_store_dwordx2 v[130:131], v[134:135], off

.LBB0_458:
	s_and_b64 vcc, exec, s[18:19]
	s_cbranch_vccz .LBB0_460
	v_mul_f32_e32 v120, s5, v120
	v_mul_f32_e32 v121, s5, v121
	v_mul_f32_e32 v134, s5, v118
	v_med3_f32 v120, v120, s33, v236
	v_med3_f32 v121, v121, s33, v236
	s_nop 0
	v_cvt_pk_fp8_f32 v118, v120, v121
	v_mul_f32_e32 v119, s5, v119
	v_med3_f32 v120, v134, s33, v236
	v_med3_f32 v119, v119, s33, v236
	v_mul_f32_e32 v116, s5, v116
	v_mul_f32_e32 v117, s5, v117
	v_cvt_pk_fp8_f32 v118, v120, v119 op_sel:[0,0,1]
	v_med3_f32 v116, v116, s33, v236
	v_med3_f32 v117, v117, s33, v236
	s_nop 0
	v_cvt_pk_fp8_f32 v119, v116, v117
	v_mul_f32_e32 v114, s5, v114
	v_mul_f32_e32 v115, s5, v115
	v_med3_f32 v114, v114, s33, v236
	v_med3_f32 v115, v115, s33, v236
	v_cvt_pk_fp8_f32 v119, v114, v115 op_sel:[0,0,1]
	v_lshl_add_u64 v[114:115], s[6:7], 0, v[132:133]
	global_store_dwordx2 v[114:115], v[118:119], off

.LBB0_465:
	s_and_b64 vcc, exec, s[18:19]
	s_cbranch_vccz .LBB0_467
	v_mul_f32_e32 v112, s5, v112
	v_mul_f32_e32 v113, s5, v113
	v_mul_f32_e32 v118, s5, v110
	v_med3_f32 v112, v112, s33, v236
	v_med3_f32 v113, v113, s33, v236
	s_nop 0
	v_cvt_pk_fp8_f32 v110, v112, v113
	v_mul_f32_e32 v111, s5, v111
	v_med3_f32 v112, v118, s33, v236
	v_med3_f32 v111, v111, s33, v236
	v_mul_f32_e32 v108, s5, v108
	v_mul_f32_e32 v109, s5, v109
	v_cvt_pk_fp8_f32 v110, v112, v111 op_sel:[0,0,1]
	v_med3_f32 v108, v108, s33, v236
	v_med3_f32 v109, v109, s33, v236
	s_nop 0
	v_cvt_pk_fp8_f32 v111, v108, v109
	v_mul_f32_e32 v106, s5, v106
	v_mul_f32_e32 v107, s5, v107
	v_med3_f32 v106, v106, s33, v236
	v_med3_f32 v107, v107, s33, v236
	v_cvt_pk_fp8_f32 v111, v106, v107 op_sel:[0,0,1]
	v_lshl_add_u64 v[106:107], s[6:7], 0, v[116:117]
	global_store_dwordx2 v[106:107], v[110:111], off

.LBB0_472:
	s_and_b64 vcc, exec, s[18:19]
	s_cbranch_vccz .LBB0_474
	v_mul_f32_e32 v104, s5, v104
	v_mul_f32_e32 v105, s5, v105
	v_mul_f32_e32 v110, s5, v102
	v_med3_f32 v104, v104, s33, v236
	v_med3_f32 v105, v105, s33, v236
	s_nop 0
	v_cvt_pk_fp8_f32 v102, v104, v105
	v_mul_f32_e32 v103, s5, v103
	v_med3_f32 v104, v110, s33, v236
	v_med3_f32 v103, v103, s33, v236
	v_mul_f32_e32 v100, s5, v100
	v_mul_f32_e32 v101, s5, v101
	v_cvt_pk_fp8_f32 v102, v104, v103 op_sel:[0,0,1]
	v_med3_f32 v100, v100, s33, v236
	v_med3_f32 v101, v101, s33, v236
	s_nop 0
	v_cvt_pk_fp8_f32 v103, v100, v101
	v_mul_f32_e32 v98, s5, v98
	v_mul_f32_e32 v99, s5, v99
	v_med3_f32 v98, v98, s33, v236
	v_med3_f32 v99, v99, s33, v236
	v_cvt_pk_fp8_f32 v103, v98, v99 op_sel:[0,0,1]
	v_lshl_add_u64 v[98:99], s[6:7], 0, v[108:109]
	global_store_dwordx2 v[98:99], v[102:103], off

.LBB0_479:
	s_and_b64 vcc, exec, s[18:19]
	s_cbranch_vccz .LBB0_481
	v_mul_f32_e32 v96, s5, v96
	v_mul_f32_e32 v97, s5, v97
	v_mul_f32_e32 v102, s5, v94
	v_med3_f32 v96, v96, s33, v236
	v_med3_f32 v97, v97, s33, v236
	s_nop 0
	v_cvt_pk_fp8_f32 v94, v96, v97
	v_mul_f32_e32 v95, s5, v95
	v_med3_f32 v96, v102, s33, v236
	v_med3_f32 v95, v95, s33, v236
	v_mul_f32_e32 v92, s5, v92
	v_mul_f32_e32 v93, s5, v93
	v_cvt_pk_fp8_f32 v94, v96, v95 op_sel:[0,0,1]
	v_med3_f32 v92, v92, s33, v236
	v_med3_f32 v93, v93, s33, v236
	s_nop 0
	v_cvt_pk_fp8_f32 v95, v92, v93
	v_mul_f32_e32 v90, s5, v90
	v_mul_f32_e32 v91, s5, v91
	v_med3_f32 v90, v90, s33, v236
	v_med3_f32 v91, v91, s33, v236
	v_cvt_pk_fp8_f32 v95, v90, v91 op_sel:[0,0,1]
	v_lshl_add_u64 v[90:91], s[6:7], 0, v[100:101]
	global_store_dwordx2 v[90:91], v[94:95], off

.LBB0_486:
	s_and_b64 vcc, exec, s[18:19]
	s_cbranch_vccz .LBB0_488
	v_mul_f32_e32 v88, s5, v88
	v_mul_f32_e32 v89, s5, v89
	v_mul_f32_e32 v94, s5, v86
	v_med3_f32 v88, v88, s33, v236
	v_med3_f32 v89, v89, s33, v236
	s_nop 0
	v_cvt_pk_fp8_f32 v86, v88, v89
	v_mul_f32_e32 v87, s5, v87
	v_med3_f32 v88, v94, s33, v236
	v_med3_f32 v87, v87, s33, v236
	v_mul_f32_e32 v84, s5, v84
	v_mul_f32_e32 v85, s5, v85
	v_cvt_pk_fp8_f32 v86, v88, v87 op_sel:[0,0,1]
	v_med3_f32 v84, v84, s33, v236
	v_med3_f32 v85, v85, s33, v236
	s_nop 0
	v_cvt_pk_fp8_f32 v87, v84, v85
	v_mul_f32_e32 v82, s5, v82
	v_mul_f32_e32 v83, s5, v83
	v_med3_f32 v82, v82, s33, v236
	v_med3_f32 v83, v83, s33, v236
	v_cvt_pk_fp8_f32 v87, v82, v83 op_sel:[0,0,1]
	v_lshl_add_u64 v[82:83], s[6:7], 0, v[92:93]
	global_store_dwordx2 v[82:83], v[86:87], off

.LBB0_493:
	s_and_b64 vcc, exec, s[18:19]
	s_cbranch_vccz .LBB0_495
	v_mul_f32_e32 v80, s5, v80
	v_mul_f32_e32 v81, s5, v81
	v_mul_f32_e32 v86, s5, v78
	v_med3_f32 v80, v80, s33, v236
	v_med3_f32 v81, v81, s33, v236
	s_nop 0
	v_cvt_pk_fp8_f32 v78, v80, v81
	v_mul_f32_e32 v79, s5, v79
	v_med3_f32 v80, v86, s33, v236
	v_med3_f32 v79, v79, s33, v236
	v_mul_f32_e32 v76, s5, v76
	v_mul_f32_e32 v77, s5, v77
	v_cvt_pk_fp8_f32 v78, v80, v79 op_sel:[0,0,1]
	v_med3_f32 v76, v76, s33, v236
	v_med3_f32 v77, v77, s33, v236
	s_nop 0
	v_cvt_pk_fp8_f32 v79, v76, v77
	v_mul_f32_e32 v74, s5, v74
	v_mul_f32_e32 v75, s5, v75
	v_med3_f32 v74, v74, s33, v236
	v_med3_f32 v75, v75, s33, v236
	v_cvt_pk_fp8_f32 v79, v74, v75 op_sel:[0,0,1]
	v_lshl_add_u64 v[74:75], s[6:7], 0, v[82:83]
	global_store_dwordx2 v[74:75], v[78:79], off

.LBB0_500:
	s_and_b64 vcc, exec, s[18:19]
	s_cbranch_vccz .LBB0_502
	v_mul_f32_e32 v72, s5, v72
	v_mul_f32_e32 v73, s5, v73
	v_mul_f32_e32 v76, s5, v70
	v_med3_f32 v72, v72, s33, v236
	v_med3_f32 v73, v73, s33, v236
	s_nop 0
	v_cvt_pk_fp8_f32 v70, v72, v73
	v_mul_f32_e32 v71, s5, v71
	v_med3_f32 v72, v76, s33, v236
	v_med3_f32 v71, v71, s33, v236
	v_mul_f32_e32 v68, s5, v68
	v_mul_f32_e32 v69, s5, v69
	v_cvt_pk_fp8_f32 v70, v72, v71 op_sel:[0,0,1]
	v_med3_f32 v68, v68, s33, v236
	v_med3_f32 v69, v69, s33, v236
	s_nop 0
	v_cvt_pk_fp8_f32 v71, v68, v69
	v_mul_f32_e32 v66, s5, v66
	v_mul_f32_e32 v67, s5, v67
	v_med3_f32 v66, v66, s33, v236
	v_med3_f32 v67, v67, s33, v236
	v_cvt_pk_fp8_f32 v71, v66, v67 op_sel:[0,0,1]
	v_lshl_add_u64 v[66:67], s[6:7], 0, v[74:75]
	global_store_dwordx2 v[66:67], v[70:71], off

.LBB0_507:
	s_and_b64 vcc, exec, s[18:19]
	s_cbranch_vccz .LBB0_509
	v_mul_f32_e32 v62, s5, v94
	v_mul_f32_e32 v63, s5, v95
	v_med3_f32 v65, v62, s33, v236
	v_med3_f32 v63, v63, s33, v236
	s_nop 0
	v_cvt_pk_fp8_f32 v62, v65, v63
	v_mul_f32_e32 v64, s5, v92
	v_mul_f32_e32 v63, s5, v93
	v_med3_f32 v64, v64, s33, v236
	v_med3_f32 v63, v63, s33, v236
	v_mul_f32_e32 v60, s5, v60
	v_mul_f32_e32 v61, s5, v61
	v_cvt_pk_fp8_f32 v62, v64, v63 op_sel:[0,0,1]
	v_med3_f32 v60, v60, s33, v236
	v_med3_f32 v61, v61, s33, v236
	s_nop 0
	v_cvt_pk_fp8_f32 v63, v60, v61
	v_mul_f32_e32 v58, s5, v58
	v_mul_f32_e32 v59, s5, v59
	v_med3_f32 v58, v58, s33, v236
	v_med3_f32 v59, v59, s33, v236
	v_cvt_pk_fp8_f32 v63, v58, v59 op_sel:[0,0,1]
	v_lshl_add_u64 v[58:59], s[6:7], 0, v[88:89]
	global_store_dwordx2 v[58:59], v[62:63], off

.LBB0_514:
	s_and_b64 vcc, exec, s[18:19]
	s_cbranch_vccz .LBB0_516
	v_mul_f32_e32 v56, s5, v56
	v_mul_f32_e32 v57, s5, v57
	v_mul_f32_e32 v60, s5, v54
	v_med3_f32 v56, v56, s33, v236
	v_med3_f32 v57, v57, s33, v236
	s_nop 0
	v_cvt_pk_fp8_f32 v54, v56, v57
	v_mul_f32_e32 v55, s5, v55
	v_med3_f32 v56, v60, s33, v236
	v_med3_f32 v55, v55, s33, v236
	v_mul_f32_e32 v52, s5, v52
	v_mul_f32_e32 v53, s5, v53
	v_cvt_pk_fp8_f32 v54, v56, v55 op_sel:[0,0,1]
	v_med3_f32 v52, v52, s33, v236
	v_med3_f32 v53, v53, s33, v236
	s_nop 0
	v_cvt_pk_fp8_f32 v55, v52, v53
	v_mul_f32_e32 v50, s5, v50
	v_mul_f32_e32 v51, s5, v51
	v_med3_f32 v50, v50, s33, v236
	v_med3_f32 v51, v51, s33, v236
	v_cvt_pk_fp8_f32 v55, v50, v51 op_sel:[0,0,1]
	v_lshl_add_u64 v[50:51], s[6:7], 0, v[58:59]
	global_store_dwordx2 v[50:51], v[54:55], off

.LBB0_521:
	s_and_b64 vcc, exec, s[18:19]
	s_cbranch_vccz .LBB0_523
	v_mul_f32_e32 v48, s5, v48
	v_mul_f32_e32 v49, s5, v49
	v_mul_f32_e32 v52, s5, v46
	v_med3_f32 v48, v48, s33, v236
	v_med3_f32 v49, v49, s33, v236
	s_nop 0
	v_cvt_pk_fp8_f32 v46, v48, v49
	v_mul_f32_e32 v47, s5, v47
	v_med3_f32 v48, v52, s33, v236
	v_med3_f32 v47, v47, s33, v236
	v_mul_f32_e32 v44, s5, v44
	v_mul_f32_e32 v45, s5, v45
	v_cvt_pk_fp8_f32 v46, v48, v47 op_sel:[0,0,1]
	v_med3_f32 v44, v44, s33, v236
	v_med3_f32 v45, v45, s33, v236
	s_nop 0
	v_cvt_pk_fp8_f32 v47, v44, v45
	v_mul_f32_e32 v42, s5, v42
	v_mul_f32_e32 v43, s5, v43
	v_med3_f32 v42, v42, s33, v236
	v_med3_f32 v43, v43, s33, v236
	v_cvt_pk_fp8_f32 v47, v42, v43 op_sel:[0,0,1]
	v_lshl_add_u64 v[42:43], s[6:7], 0, v[50:51]
	global_store_dwordx2 v[42:43], v[46:47], off

.LBB0_528:
	s_and_b64 vcc, exec, s[18:19]
	s_cbranch_vccz .LBB0_530
	v_mul_f32_e32 v40, s5, v40
	v_mul_f32_e32 v41, s5, v41
	v_mul_f32_e32 v44, s5, v38
	v_med3_f32 v40, v40, s33, v236
	v_med3_f32 v41, v41, s33, v236
	s_nop 0
	v_cvt_pk_fp8_f32 v38, v40, v41
	v_mul_f32_e32 v39, s5, v39
	v_med3_f32 v40, v44, s33, v236
	v_med3_f32 v39, v39, s33, v236
	v_mul_f32_e32 v36, s5, v36
	v_mul_f32_e32 v37, s5, v37
	v_cvt_pk_fp8_f32 v38, v40, v39 op_sel:[0,0,1]
	v_med3_f32 v36, v36, s33, v236
	v_med3_f32 v37, v37, s33, v236
	s_nop 0
	v_cvt_pk_fp8_f32 v39, v36, v37
	v_mul_f32_e32 v34, s5, v34
	v_mul_f32_e32 v35, s5, v35
	v_med3_f32 v34, v34, s33, v236
	v_med3_f32 v35, v35, s33, v236
	v_cvt_pk_fp8_f32 v39, v34, v35 op_sel:[0,0,1]
	v_lshl_add_u64 v[34:35], s[6:7], 0, v[42:43]
	global_store_dwordx2 v[34:35], v[38:39], off

.LBB0_535:
	s_and_b64 vcc, exec, s[18:19]
	s_cbranch_vccz .LBB0_537
	v_mul_f32_e32 v32, s5, v32
	v_mul_f32_e32 v33, s5, v33
	v_mul_f32_e32 v36, s5, v30
	v_med3_f32 v32, v32, s33, v236
	v_med3_f32 v33, v33, s33, v236
	s_nop 0
	v_cvt_pk_fp8_f32 v30, v32, v33
	v_mul_f32_e32 v31, s5, v31
	v_med3_f32 v32, v36, s33, v236
	v_med3_f32 v31, v31, s33, v236
	v_mul_f32_e32 v28, s5, v28
	v_mul_f32_e32 v29, s5, v29
	v_cvt_pk_fp8_f32 v30, v32, v31 op_sel:[0,0,1]
	v_med3_f32 v28, v28, s33, v236
	v_med3_f32 v29, v29, s33, v236
	s_nop 0
	v_cvt_pk_fp8_f32 v31, v28, v29
	v_mul_f32_e32 v26, s5, v26
	v_mul_f32_e32 v27, s5, v27
	v_med3_f32 v26, v26, s33, v236
	v_med3_f32 v27, v27, s33, v236
	v_cvt_pk_fp8_f32 v31, v26, v27 op_sel:[0,0,1]
	v_lshl_add_u64 v[26:27], s[6:7], 0, v[34:35]
	global_store_dwordx2 v[26:27], v[30:31], off

.LBB0_542:
	s_and_b64 vcc, exec, s[18:19]
	s_cbranch_vccz .LBB0_544
	v_mul_f32_e32 v24, s5, v24
	v_mul_f32_e32 v25, s5, v25
	v_mul_f32_e32 v28, s5, v22
	v_med3_f32 v24, v24, s33, v236
	v_med3_f32 v25, v25, s33, v236
	s_nop 0
	v_cvt_pk_fp8_f32 v22, v24, v25
	v_mul_f32_e32 v23, s5, v23
	v_med3_f32 v24, v28, s33, v236
	v_med3_f32 v23, v23, s33, v236
	v_mul_f32_e32 v20, s5, v20
	v_mul_f32_e32 v21, s5, v21
	v_cvt_pk_fp8_f32 v22, v24, v23 op_sel:[0,0,1]
	v_med3_f32 v20, v20, s33, v236
	v_med3_f32 v21, v21, s33, v236
	s_nop 0
	v_cvt_pk_fp8_f32 v23, v20, v21
	v_mul_f32_e32 v18, s5, v18
	v_mul_f32_e32 v19, s5, v19
	v_med3_f32 v18, v18, s33, v236
	v_med3_f32 v19, v19, s33, v236
	v_cvt_pk_fp8_f32 v23, v18, v19 op_sel:[0,0,1]
	v_lshl_add_u64 v[18:19], s[6:7], 0, v[26:27]
	global_store_dwordx2 v[18:19], v[22:23], off

.LBB0_549:
	s_and_b64 vcc, exec, s[18:19]
	s_cbranch_vccz .LBB0_551
	v_mul_f32_e32 v16, s5, v16
	v_mul_f32_e32 v17, s5, v17
	v_mul_f32_e32 v20, s5, v14
	v_med3_f32 v16, v16, s33, v236
	v_med3_f32 v17, v17, s33, v236
	s_nop 0
	v_cvt_pk_fp8_f32 v14, v16, v17
	v_mul_f32_e32 v15, s5, v15
	v_med3_f32 v16, v20, s33, v236
	v_med3_f32 v15, v15, s33, v236
	v_mul_f32_e32 v12, s5, v12
	v_mul_f32_e32 v13, s5, v13
	v_cvt_pk_fp8_f32 v14, v16, v15 op_sel:[0,0,1]
	v_med3_f32 v12, v12, s33, v236
	v_med3_f32 v13, v13, s33, v236
	s_nop 0
	v_cvt_pk_fp8_f32 v15, v12, v13
	v_mul_f32_e32 v10, s5, v10
	v_mul_f32_e32 v11, s5, v11
	v_med3_f32 v10, v10, s33, v236
	v_med3_f32 v11, v11, s33, v236
	v_cvt_pk_fp8_f32 v15, v10, v11 op_sel:[0,0,1]
	v_lshl_add_u64 v[10:11], s[6:7], 0, v[18:19]
	global_store_dwordx2 v[10:11], v[14:15], off

.LBB0_556:
	s_and_b64 vcc, exec, s[0:1]
	s_cbranch_vccz .LBB0_558
	v_mul_f32_e32 v0, s5, v8
	v_mul_f32_e32 v8, s5, v9
	v_mul_f32_e32 v9, s5, v6
	v_med3_f32 v0, v0, s33, v236
	v_med3_f32 v8, v8, s33, v236
	s_nop 0
	v_cvt_pk_fp8_f32 v6, v0, v8
	v_mul_f32_e32 v0, s5, v7
	v_med3_f32 v7, v9, s33, v236
	v_med3_f32 v0, v0, s33, v236
	v_cvt_pk_fp8_f32 v6, v7, v0 op_sel:[0,0,1]
	v_mul_f32_e32 v0, s5, v4
	v_mul_f32_e32 v4, s5, v5
	v_med3_f32 v0, v0, s33, v236
	v_med3_f32 v4, v4, s33, v236
	s_nop 0
	v_cvt_pk_fp8_f32 v7, v0, v4
	v_mul_f32_e32 v2, s5, v2
	v_mul_f32_e32 v0, s5, v3
	v_med3_f32 v2, v2, s33, v236
	v_med3_f32 v0, v0, s33, v236
	v_cvt_pk_fp8_f32 v7, v2, v0 op_sel:[0,0,1]
	v_lshl_add_u64 v[2:3], s[6:7], 0, v[10:11]
	global_store_dwordx2 v[2:3], v[6:7], off

.LBB0_712:
	s_add_u32 s16, s14, 0x4c100000
	v_readlane_b32 s2, v254, 48
	s_addc_u32 s17, s15, 0
	v_readlane_b32 s3, v254, 49
	s_add_u32 s14, s14, 0x4f200000
	s_addc_u32 s15, s15, 0
	v_cndmask_b32_e64 v152, 0, 1, s[2:3]
	v_cmp_ne_u32_e64 s[0:1], 1, v152
	s_andn2_b64 vcc, exec, s[2:3]
	s_cbranch_vccnz .LBB0_714
	v_cvt_pk_bf16_f32 v152, v62, v63
	v_mul_f32_e32 v62, s26, v62
	v_mul_f32_e32 v63, s26, v63
	v_med3_f32 v156, v62, s33, v236
	v_med3_f32 v63, v63, s33, v236
	s_nop 0
	v_cvt_pk_fp8_f32 v62, v156, v63
	v_cvt_pk_bf16_f32 v153, v64, v65
	v_mul_f32_e32 v64, s26, v64
	v_mul_f32_e32 v63, s26, v65
	v_cvt_pk_bf16_f32 v154, v58, v59
	v_med3_f32 v64, v64, s33, v236
	v_med3_f32 v63, v63, s33, v236
	v_mul_f32_e32 v58, s26, v58
	v_mul_f32_e32 v59, s26, v59
	v_cvt_pk_fp8_f32 v62, v64, v63 op_sel:[0,0,1]
	v_med3_f32 v58, v58, s33, v236
	v_med3_f32 v59, v59, s33, v236
	s_nop 0
	v_cvt_pk_fp8_f32 v63, v58, v59
	v_cvt_pk_bf16_f32 v155, v60, v61
	v_mul_f32_e32 v60, s26, v60
	v_mul_f32_e32 v58, s26, v61
	v_med3_f32 v59, v60, s33, v236
	v_med3_f32 v58, v58, s33, v236
	v_cvt_pk_fp8_f32 v63, v59, v58 op_sel:[0,0,1]
	v_lshl_add_u64 v[58:59], v[198:199], 1, s[16:17]
	global_store_dwordx4 v[58:59], v[152:155], off
	v_lshl_add_u64 v[58:59], s[14:15], 0, v[198:199]
	global_store_dwordx2 v[58:59], v[62:63], off

.LBB0_716:
	s_and_b64 vcc, exec, s[0:1]
	s_cbranch_vccnz .LBB0_718
	v_cvt_pk_bf16_f32 v74, v62, v63
	v_mul_f32_e32 v62, s26, v62
	v_mul_f32_e32 v63, s26, v63
	v_med3_f32 v78, v62, s33, v236
	v_med3_f32 v63, v63, s33, v236
	s_nop 0
	v_cvt_pk_fp8_f32 v62, v78, v63
	v_cvt_pk_bf16_f32 v75, v64, v65
	v_mul_f32_e32 v64, s26, v64
	v_mul_f32_e32 v63, s26, v65
	v_cvt_pk_bf16_f32 v76, v58, v59
	v_med3_f32 v64, v64, s33, v236
	v_med3_f32 v63, v63, s33, v236
	v_mul_f32_e32 v58, s26, v58
	v_mul_f32_e32 v59, s26, v59
	v_cvt_pk_fp8_f32 v62, v64, v63 op_sel:[0,0,1]
	v_med3_f32 v58, v58, s33, v236
	v_med3_f32 v59, v59, s33, v236
	s_nop 0
	v_cvt_pk_fp8_f32 v63, v58, v59
	v_cvt_pk_bf16_f32 v77, v60, v61
	v_mul_f32_e32 v60, s26, v60
	v_mul_f32_e32 v58, s26, v61
	v_med3_f32 v59, v60, s33, v236
	v_med3_f32 v58, v58, s33, v236
	v_cvt_pk_fp8_f32 v63, v59, v58 op_sel:[0,0,1]
	v_lshl_add_u64 v[58:59], v[196:197], 1, s[16:17]
	global_store_dwordx4 v[58:59], v[74:77], off
	v_lshl_add_u64 v[58:59], s[14:15], 0, v[196:197]
	global_store_dwordx2 v[58:59], v[62:63], off

.LBB0_720:
	s_and_b64 vcc, exec, s[0:1]
	s_cbranch_vccnz .LBB0_722
	v_cvt_pk_bf16_f32 v74, v62, v63
	v_mul_f32_e32 v62, s26, v62
	v_mul_f32_e32 v63, s26, v63
	v_med3_f32 v78, v62, s33, v236
	v_med3_f32 v63, v63, s33, v236
	s_nop 0
	v_cvt_pk_fp8_f32 v62, v78, v63
	v_cvt_pk_bf16_f32 v75, v64, v65
	v_mul_f32_e32 v64, s26, v64
	v_mul_f32_e32 v63, s26, v65
	v_cvt_pk_bf16_f32 v76, v58, v59
	v_med3_f32 v64, v64, s33, v236
	v_med3_f32 v63, v63, s33, v236
	v_mul_f32_e32 v58, s26, v58
	v_mul_f32_e32 v59, s26, v59
	v_cvt_pk_fp8_f32 v62, v64, v63 op_sel:[0,0,1]
	v_med3_f32 v58, v58, s33, v236
	v_med3_f32 v59, v59, s33, v236
	s_nop 0
	v_cvt_pk_fp8_f32 v63, v58, v59
	v_cvt_pk_bf16_f32 v77, v60, v61
	v_mul_f32_e32 v60, s26, v60
	v_mul_f32_e32 v58, s26, v61
	v_med3_f32 v59, v60, s33, v236
	v_med3_f32 v58, v58, s33, v236
	v_cvt_pk_fp8_f32 v63, v59, v58 op_sel:[0,0,1]
	v_lshl_add_u64 v[58:59], v[194:195], 1, s[16:17]
	global_store_dwordx4 v[58:59], v[74:77], off
	v_lshl_add_u64 v[58:59], s[14:15], 0, v[194:195]
	global_store_dwordx2 v[58:59], v[62:63], off

.LBB0_724:
	s_and_b64 vcc, exec, s[0:1]
	s_cbranch_vccnz .LBB0_726
	v_cvt_pk_bf16_f32 v74, v62, v63
	v_mul_f32_e32 v62, s26, v62
	v_mul_f32_e32 v63, s26, v63
	v_med3_f32 v78, v62, s33, v236
	v_med3_f32 v63, v63, s33, v236
	s_nop 0
	v_cvt_pk_fp8_f32 v62, v78, v63
	v_cvt_pk_bf16_f32 v75, v64, v65
	v_mul_f32_e32 v64, s26, v64
	v_mul_f32_e32 v63, s26, v65
	v_cvt_pk_bf16_f32 v76, v58, v59
	v_med3_f32 v64, v64, s33, v236
	v_med3_f32 v63, v63, s33, v236
	v_mul_f32_e32 v58, s26, v58
	v_mul_f32_e32 v59, s26, v59
	v_cvt_pk_fp8_f32 v62, v64, v63 op_sel:[0,0,1]
	v_med3_f32 v58, v58, s33, v236
	v_med3_f32 v59, v59, s33, v236
	s_nop 0
	v_cvt_pk_fp8_f32 v63, v58, v59
	v_cvt_pk_bf16_f32 v77, v60, v61
	v_mul_f32_e32 v60, s26, v60
	v_mul_f32_e32 v58, s26, v61
	v_med3_f32 v59, v60, s33, v236
	v_med3_f32 v58, v58, s33, v236
	v_cvt_pk_fp8_f32 v63, v59, v58 op_sel:[0,0,1]
	v_lshl_add_u64 v[58:59], v[192:193], 1, s[16:17]
	global_store_dwordx4 v[58:59], v[74:77], off
	v_lshl_add_u64 v[58:59], s[14:15], 0, v[192:193]
	global_store_dwordx2 v[58:59], v[62:63], off

.LBB0_728:
	s_and_b64 vcc, exec, s[0:1]
	s_cbranch_vccnz .LBB0_730
	v_cvt_pk_bf16_f32 v74, v62, v63
	v_mul_f32_e32 v62, s26, v62
	v_mul_f32_e32 v63, s26, v63
	v_med3_f32 v78, v62, s33, v236
	v_med3_f32 v63, v63, s33, v236
	s_nop 0
	v_cvt_pk_fp8_f32 v62, v78, v63
	v_cvt_pk_bf16_f32 v75, v64, v65
	v_mul_f32_e32 v64, s26, v64
	v_mul_f32_e32 v63, s26, v65
	v_cvt_pk_bf16_f32 v76, v58, v59
	v_med3_f32 v64, v64, s33, v236
	v_med3_f32 v63, v63, s33, v236
	v_mul_f32_e32 v58, s26, v58
	v_mul_f32_e32 v59, s26, v59
	v_cvt_pk_fp8_f32 v62, v64, v63 op_sel:[0,0,1]
	v_med3_f32 v58, v58, s33, v236
	v_med3_f32 v59, v59, s33, v236
	s_nop 0
	v_cvt_pk_fp8_f32 v63, v58, v59
	v_cvt_pk_bf16_f32 v77, v60, v61
	v_mul_f32_e32 v60, s26, v60
	v_mul_f32_e32 v58, s26, v61
	v_med3_f32 v59, v60, s33, v236
	v_med3_f32 v58, v58, s33, v236
	v_cvt_pk_fp8_f32 v63, v59, v58 op_sel:[0,0,1]
	v_lshl_add_u64 v[58:59], v[208:209], 1, s[16:17]
	global_store_dwordx4 v[58:59], v[74:77], off
	v_lshl_add_u64 v[58:59], s[14:15], 0, v[208:209]
	global_store_dwordx2 v[58:59], v[62:63], off

.LBB0_732:
	s_and_b64 vcc, exec, s[0:1]
	s_cbranch_vccnz .LBB0_734
	v_cvt_pk_bf16_f32 v74, v62, v63
	v_mul_f32_e32 v62, s26, v62
	v_mul_f32_e32 v63, s26, v63
	v_med3_f32 v78, v62, s33, v236
	v_med3_f32 v63, v63, s33, v236
	s_nop 0
	v_cvt_pk_fp8_f32 v62, v78, v63
	v_cvt_pk_bf16_f32 v75, v64, v65
	v_mul_f32_e32 v64, s26, v64
	v_mul_f32_e32 v63, s26, v65
	v_cvt_pk_bf16_f32 v76, v58, v59
	v_med3_f32 v64, v64, s33, v236
	v_med3_f32 v63, v63, s33, v236
	v_mul_f32_e32 v58, s26, v58
	v_mul_f32_e32 v59, s26, v59
	v_cvt_pk_fp8_f32 v62, v64, v63 op_sel:[0,0,1]
	v_med3_f32 v58, v58, s33, v236
	v_med3_f32 v59, v59, s33, v236
	s_nop 0
	v_cvt_pk_fp8_f32 v63, v58, v59
	v_cvt_pk_bf16_f32 v77, v60, v61
	v_mul_f32_e32 v60, s26, v60
	v_mul_f32_e32 v58, s26, v61
	v_med3_f32 v59, v60, s33, v236
	v_med3_f32 v58, v58, s33, v236
	v_cvt_pk_fp8_f32 v63, v59, v58 op_sel:[0,0,1]
	v_lshl_add_u64 v[58:59], v[206:207], 1, s[16:17]
	global_store_dwordx4 v[58:59], v[74:77], off
	v_lshl_add_u64 v[58:59], s[14:15], 0, v[206:207]
	global_store_dwordx2 v[58:59], v[62:63], off

.LBB0_736:
	s_and_b64 vcc, exec, s[0:1]
	s_cbranch_vccnz .LBB0_738
	v_cvt_pk_bf16_f32 v74, v62, v63
	v_mul_f32_e32 v62, s26, v62
	v_mul_f32_e32 v63, s26, v63
	v_med3_f32 v78, v62, s33, v236
	v_med3_f32 v63, v63, s33, v236
	s_nop 0
	v_cvt_pk_fp8_f32 v62, v78, v63
	v_cvt_pk_bf16_f32 v75, v64, v65
	v_mul_f32_e32 v64, s26, v64
	v_mul_f32_e32 v63, s26, v65
	v_cvt_pk_bf16_f32 v76, v58, v59
	v_med3_f32 v64, v64, s33, v236
	v_med3_f32 v63, v63, s33, v236
	v_mul_f32_e32 v58, s26, v58
	v_mul_f32_e32 v59, s26, v59
	v_cvt_pk_fp8_f32 v62, v64, v63 op_sel:[0,0,1]
	v_med3_f32 v58, v58, s33, v236
	v_med3_f32 v59, v59, s33, v236
	s_nop 0
	v_cvt_pk_fp8_f32 v63, v58, v59
	v_cvt_pk_bf16_f32 v77, v60, v61
	v_mul_f32_e32 v60, s26, v60
	v_mul_f32_e32 v58, s26, v61
	v_med3_f32 v59, v60, s33, v236
	v_med3_f32 v58, v58, s33, v236
	v_cvt_pk_fp8_f32 v63, v59, v58 op_sel:[0,0,1]
	v_lshl_add_u64 v[58:59], v[204:205], 1, s[16:17]
	global_store_dwordx4 v[58:59], v[74:77], off
	v_lshl_add_u64 v[58:59], s[14:15], 0, v[204:205]
	global_store_dwordx2 v[58:59], v[62:63], off

.LBB0_740:
	s_and_b64 vcc, exec, s[0:1]
	s_cbranch_vccnz .LBB0_742
	v_cvt_pk_bf16_f32 v74, v62, v63
	v_mul_f32_e32 v62, s26, v62
	v_mul_f32_e32 v63, s26, v63
	v_med3_f32 v78, v62, s33, v236
	v_med3_f32 v63, v63, s33, v236
	s_nop 0
	v_cvt_pk_fp8_f32 v62, v78, v63
	v_cvt_pk_bf16_f32 v75, v64, v65
	v_mul_f32_e32 v64, s26, v64
	v_mul_f32_e32 v63, s26, v65
	v_cvt_pk_bf16_f32 v76, v58, v59
	v_med3_f32 v64, v64, s33, v236
	v_med3_f32 v63, v63, s33, v236
	v_mul_f32_e32 v58, s26, v58
	v_mul_f32_e32 v59, s26, v59
	v_cvt_pk_fp8_f32 v62, v64, v63 op_sel:[0,0,1]
	v_med3_f32 v58, v58, s33, v236
	v_med3_f32 v59, v59, s33, v236
	s_nop 0
	v_cvt_pk_fp8_f32 v63, v58, v59
	v_cvt_pk_bf16_f32 v77, v60, v61
	v_mul_f32_e32 v60, s26, v60
	v_mul_f32_e32 v58, s26, v61
	v_med3_f32 v59, v60, s33, v236
	v_med3_f32 v58, v58, s33, v236
	v_cvt_pk_fp8_f32 v63, v59, v58 op_sel:[0,0,1]
	v_lshl_add_u64 v[58:59], v[200:201], 1, s[16:17]
	global_store_dwordx4 v[58:59], v[74:77], off
	v_lshl_add_u64 v[58:59], s[14:15], 0, v[200:201]
	global_store_dwordx2 v[58:59], v[62:63], off

.LBB0_744:
	s_mov_b64 s[8:9], 0x80
	s_and_b64 vcc, exec, s[0:1]
	v_lshl_add_u64 v[84:85], v[184:185], 0, s[8:9]
	s_cbranch_vccnz .LBB0_746
	v_cvt_pk_bf16_f32 v86, v6, v7
	v_mul_f32_e32 v6, s26, v6
	v_mul_f32_e32 v7, s26, v7
	v_med3_f32 v100, v6, s33, v236
	v_med3_f32 v7, v7, s33, v236
	s_nop 0
	v_cvt_pk_fp8_f32 v6, v100, v7
	v_cvt_pk_bf16_f32 v87, v8, v9
	v_mul_f32_e32 v8, s26, v8
	v_mul_f32_e32 v7, s26, v9
	v_cvt_pk_bf16_f32 v88, v2, v3
	v_med3_f32 v8, v8, s33, v236
	v_med3_f32 v7, v7, s33, v236
	v_mul_f32_e32 v2, s26, v2
	v_mul_f32_e32 v3, s26, v3
	v_cvt_pk_fp8_f32 v6, v8, v7 op_sel:[0,0,1]
	v_med3_f32 v2, v2, s33, v236
	v_med3_f32 v3, v3, s33, v236
	s_nop 0
	v_cvt_pk_fp8_f32 v7, v2, v3
	v_cvt_pk_bf16_f32 v89, v4, v5
	v_mul_f32_e32 v4, s26, v4
	v_mul_f32_e32 v2, s26, v5
	v_med3_f32 v3, v4, s33, v236
	v_med3_f32 v2, v2, s33, v236
	v_cvt_pk_fp8_f32 v7, v3, v2 op_sel:[0,0,1]
	v_lshl_add_u64 v[98:99], v[186:187], 0, v[84:85]
	v_lshl_add_u64 v[2:3], v[98:99], 1, s[16:17]
	global_store_dwordx4 v[2:3], v[86:89], off
	v_lshl_add_u64 v[2:3], s[14:15], 0, v[98:99]
	global_store_dwordx2 v[2:3], v[6:7], off

.LBB0_748:
	s_and_b64 vcc, exec, s[0:1]
	s_cbranch_vccnz .LBB0_750
	v_cvt_pk_bf16_f32 v10, v6, v7
	v_mul_f32_e32 v6, s26, v6
	v_mul_f32_e32 v7, s26, v7
	v_med3_f32 v16, v6, s33, v236
	v_med3_f32 v7, v7, s33, v236
	s_nop 0
	v_cvt_pk_fp8_f32 v6, v16, v7
	v_cvt_pk_bf16_f32 v11, v8, v9
	v_mul_f32_e32 v8, s26, v8
	v_mul_f32_e32 v7, s26, v9
	v_cvt_pk_bf16_f32 v12, v2, v3
	v_med3_f32 v8, v8, s33, v236
	v_med3_f32 v7, v7, s33, v236
	v_mul_f32_e32 v2, s26, v2
	v_mul_f32_e32 v3, s26, v3
	v_cvt_pk_fp8_f32 v6, v8, v7 op_sel:[0,0,1]
	v_med3_f32 v2, v2, s33, v236
	v_med3_f32 v3, v3, s33, v236
	s_nop 0
	v_cvt_pk_fp8_f32 v7, v2, v3
	v_cvt_pk_bf16_f32 v13, v4, v5
	v_mul_f32_e32 v4, s26, v4
	v_mul_f32_e32 v2, s26, v5
	v_med3_f32 v3, v4, s33, v236
	v_med3_f32 v2, v2, s33, v236
	v_cvt_pk_fp8_f32 v7, v3, v2 op_sel:[0,0,1]
	v_lshl_add_u64 v[14:15], v[182:183], 0, v[84:85]
	v_lshl_add_u64 v[2:3], v[14:15], 1, s[16:17]
	global_store_dwordx4 v[2:3], v[10:13], off
	v_lshl_add_u64 v[2:3], s[14:15], 0, v[14:15]
	global_store_dwordx2 v[2:3], v[6:7], off

.LBB0_752:
	s_and_b64 vcc, exec, s[0:1]
	s_cbranch_vccnz .LBB0_754
	v_cvt_pk_bf16_f32 v10, v6, v7
	v_mul_f32_e32 v6, s26, v6
	v_mul_f32_e32 v7, s26, v7
	v_med3_f32 v16, v6, s33, v236
	v_med3_f32 v7, v7, s33, v236
	s_nop 0
	v_cvt_pk_fp8_f32 v6, v16, v7
	v_cvt_pk_bf16_f32 v11, v8, v9
	v_mul_f32_e32 v8, s26, v8
	v_mul_f32_e32 v7, s26, v9
	v_cvt_pk_bf16_f32 v12, v2, v3
	v_med3_f32 v8, v8, s33, v236
	v_med3_f32 v7, v7, s33, v236
	v_mul_f32_e32 v2, s26, v2
	v_mul_f32_e32 v3, s26, v3
	v_cvt_pk_fp8_f32 v6, v8, v7 op_sel:[0,0,1]
	v_med3_f32 v2, v2, s33, v236
	v_med3_f32 v3, v3, s33, v236
	s_nop 0
	v_cvt_pk_fp8_f32 v7, v2, v3
	v_cvt_pk_bf16_f32 v13, v4, v5
	v_mul_f32_e32 v4, s26, v4
	v_mul_f32_e32 v2, s26, v5
	v_med3_f32 v3, v4, s33, v236
	v_med3_f32 v2, v2, s33, v236
	v_cvt_pk_fp8_f32 v7, v3, v2 op_sel:[0,0,1]
	v_lshl_add_u64 v[14:15], v[180:181], 0, v[84:85]
	v_lshl_add_u64 v[2:3], v[14:15], 1, s[16:17]
	global_store_dwordx4 v[2:3], v[10:13], off
	v_lshl_add_u64 v[2:3], s[14:15], 0, v[14:15]
	global_store_dwordx2 v[2:3], v[6:7], off

.LBB0_756:
	s_and_b64 vcc, exec, s[0:1]
	s_cbranch_vccnz .LBB0_758
	v_cvt_pk_bf16_f32 v10, v6, v7
	v_mul_f32_e32 v6, s26, v6
	v_mul_f32_e32 v7, s26, v7
	v_med3_f32 v16, v6, s33, v236
	v_med3_f32 v7, v7, s33, v236
	s_nop 0
	v_cvt_pk_fp8_f32 v6, v16, v7
	v_cvt_pk_bf16_f32 v11, v8, v9
	v_mul_f32_e32 v8, s26, v8
	v_mul_f32_e32 v7, s26, v9
	v_cvt_pk_bf16_f32 v12, v2, v3
	v_med3_f32 v8, v8, s33, v236
	v_med3_f32 v7, v7, s33, v236
	v_mul_f32_e32 v2, s26, v2
	v_mul_f32_e32 v3, s26, v3
	v_cvt_pk_fp8_f32 v6, v8, v7 op_sel:[0,0,1]
	v_med3_f32 v2, v2, s33, v236
	v_med3_f32 v3, v3, s33, v236
	s_nop 0
	v_cvt_pk_fp8_f32 v7, v2, v3
	v_cvt_pk_bf16_f32 v13, v4, v5
	v_mul_f32_e32 v4, s26, v4
	v_mul_f32_e32 v2, s26, v5
	v_med3_f32 v3, v4, s33, v236
	v_med3_f32 v2, v2, s33, v236
	v_cvt_pk_fp8_f32 v7, v3, v2 op_sel:[0,0,1]
	v_lshl_add_u64 v[14:15], v[178:179], 0, v[84:85]
	v_lshl_add_u64 v[2:3], v[14:15], 1, s[16:17]
	global_store_dwordx4 v[2:3], v[10:13], off
	v_lshl_add_u64 v[2:3], s[14:15], 0, v[14:15]
	global_store_dwordx2 v[2:3], v[6:7], off

.LBB0_760:
	s_and_b64 vcc, exec, s[0:1]
	s_cbranch_vccnz .LBB0_762
	v_cvt_pk_bf16_f32 v10, v6, v7
	v_mul_f32_e32 v6, s26, v6
	v_mul_f32_e32 v7, s26, v7
	v_med3_f32 v16, v6, s33, v236
	v_med3_f32 v7, v7, s33, v236
	s_nop 0
	v_cvt_pk_fp8_f32 v6, v16, v7
	v_cvt_pk_bf16_f32 v11, v8, v9
	v_mul_f32_e32 v8, s26, v8
	v_mul_f32_e32 v7, s26, v9
	v_cvt_pk_bf16_f32 v12, v2, v3
	v_med3_f32 v8, v8, s33, v236
	v_med3_f32 v7, v7, s33, v236
	v_mul_f32_e32 v2, s26, v2
	v_mul_f32_e32 v3, s26, v3
	v_cvt_pk_fp8_f32 v6, v8, v7 op_sel:[0,0,1]
	v_med3_f32 v2, v2, s33, v236
	v_med3_f32 v3, v3, s33, v236
	s_nop 0
	v_cvt_pk_fp8_f32 v7, v2, v3
	v_cvt_pk_bf16_f32 v13, v4, v5
	v_mul_f32_e32 v4, s26, v4
	v_mul_f32_e32 v2, s26, v5
	v_med3_f32 v3, v4, s33, v236
	v_med3_f32 v2, v2, s33, v236
	v_cvt_pk_fp8_f32 v7, v3, v2 op_sel:[0,0,1]
	v_lshl_add_u64 v[14:15], v[190:191], 0, v[84:85]
	v_lshl_add_u64 v[2:3], v[14:15], 1, s[16:17]
	global_store_dwordx4 v[2:3], v[10:13], off
	v_lshl_add_u64 v[2:3], s[14:15], 0, v[14:15]
	global_store_dwordx2 v[2:3], v[6:7], off

.LBB0_764:
	s_and_b64 vcc, exec, s[0:1]
	s_cbranch_vccnz .LBB0_766
	v_cvt_pk_bf16_f32 v10, v6, v7
	v_mul_f32_e32 v6, s26, v6
	v_mul_f32_e32 v7, s26, v7
	v_med3_f32 v16, v6, s33, v236
	v_med3_f32 v7, v7, s33, v236
	s_nop 0
	v_cvt_pk_fp8_f32 v6, v16, v7
	v_cvt_pk_bf16_f32 v11, v8, v9
	v_mul_f32_e32 v8, s26, v8
	v_mul_f32_e32 v7, s26, v9
	v_cvt_pk_bf16_f32 v12, v2, v3
	v_med3_f32 v8, v8, s33, v236
	v_med3_f32 v7, v7, s33, v236
	v_mul_f32_e32 v2, s26, v2
	v_mul_f32_e32 v3, s26, v3
	v_cvt_pk_fp8_f32 v6, v8, v7 op_sel:[0,0,1]
	v_med3_f32 v2, v2, s33, v236
	v_med3_f32 v3, v3, s33, v236
	s_nop 0
	v_cvt_pk_fp8_f32 v7, v2, v3
	v_cvt_pk_bf16_f32 v13, v4, v5
	v_mul_f32_e32 v4, s26, v4
	v_mul_f32_e32 v2, s26, v5
	v_med3_f32 v3, v4, s33, v236
	v_med3_f32 v2, v2, s33, v236
	v_cvt_pk_fp8_f32 v7, v3, v2 op_sel:[0,0,1]
	v_lshl_add_u64 v[14:15], v[188:189], 0, v[84:85]
	v_lshl_add_u64 v[2:3], v[14:15], 1, s[16:17]
	global_store_dwordx4 v[2:3], v[10:13], off
	v_lshl_add_u64 v[2:3], s[14:15], 0, v[14:15]
	global_store_dwordx2 v[2:3], v[6:7], off

.LBB0_768:
	s_and_b64 vcc, exec, s[0:1]
	s_cbranch_vccnz .LBB0_770
	v_cvt_pk_bf16_f32 v10, v6, v7
	v_mul_f32_e32 v6, s26, v6
	v_mul_f32_e32 v7, s26, v7
	v_med3_f32 v16, v6, s33, v236
	v_med3_f32 v7, v7, s33, v236
	s_nop 0
	v_cvt_pk_fp8_f32 v6, v16, v7
	v_cvt_pk_bf16_f32 v11, v8, v9
	v_mul_f32_e32 v8, s26, v8
	v_mul_f32_e32 v7, s26, v9
	v_cvt_pk_bf16_f32 v12, v2, v3
	v_med3_f32 v8, v8, s33, v236
	v_med3_f32 v7, v7, s33, v236
	v_mul_f32_e32 v2, s26, v2
	v_mul_f32_e32 v3, s26, v3
	v_cvt_pk_fp8_f32 v6, v8, v7 op_sel:[0,0,1]
	v_med3_f32 v2, v2, s33, v236
	v_med3_f32 v3, v3, s33, v236
	s_nop 0
	v_cvt_pk_fp8_f32 v7, v2, v3
	v_cvt_pk_bf16_f32 v13, v4, v5
	v_mul_f32_e32 v4, s26, v4
	v_mul_f32_e32 v2, s26, v5
	v_med3_f32 v3, v4, s33, v236
	v_med3_f32 v2, v2, s33, v236
	v_cvt_pk_fp8_f32 v7, v3, v2 op_sel:[0,0,1]
	v_lshl_add_u64 v[14:15], v[176:177], 0, v[84:85]
	v_lshl_add_u64 v[2:3], v[14:15], 1, s[16:17]
	global_store_dwordx4 v[2:3], v[10:13], off
	v_lshl_add_u64 v[2:3], s[14:15], 0, v[14:15]
	global_store_dwordx2 v[2:3], v[6:7], off

.LBB0_772:
	s_and_b64 vcc, exec, s[0:1]
	s_cbranch_vccnz .LBB0_774
	v_cvt_pk_bf16_f32 v10, v6, v7
	v_mul_f32_e32 v0, s26, v6
	v_mul_f32_e32 v6, s26, v7
	v_cvt_pk_bf16_f32 v11, v8, v9
	v_mul_f32_e32 v7, s26, v8
	v_mul_f32_e32 v8, s26, v9
	v_med3_f32 v0, v0, s33, v236
	v_med3_f32 v9, v6, s33, v236
	s_nop 0
	v_cvt_pk_fp8_f32 v6, v0, v9
	v_cvt_pk_bf16_f32 v12, v2, v3
	v_med3_f32 v7, v7, s33, v236
	v_med3_f32 v8, v8, s33, v236
	v_mul_f32_e32 v0, s26, v2
	v_mul_f32_e32 v2, s26, v3
	v_cvt_pk_fp8_f32 v6, v7, v8 op_sel:[0,0,1]
	v_med3_f32 v0, v0, s33, v236
	v_med3_f32 v2, v2, s33, v236
	s_nop 0
	v_cvt_pk_fp8_f32 v7, v0, v2
	v_cvt_pk_bf16_f32 v13, v4, v5
	v_mul_f32_e32 v3, s26, v4
	v_mul_f32_e32 v4, s26, v5
	v_med3_f32 v3, v3, s33, v236
	v_med3_f32 v4, v4, s33, v236
	v_cvt_pk_fp8_f32 v7, v3, v4 op_sel:[0,0,1]
	v_lshl_add_u64 v[14:15], v[174:175], 0, v[84:85]
	v_lshl_add_u64 v[16:17], v[14:15], 1, s[16:17]
	v_lshl_add_u64 v[2:3], s[14:15], 0, v[14:15]
	global_store_dwordx4 v[16:17], v[10:13], off
	global_store_dwordx2 v[2:3], v[6:7], off

.LBB0_1698:
	s_andn2_b64 vcc, exec, s[0:1]
	s_cbranch_vccnz .LBB0_1700
	v_mul_f32_e32 v42, 0x42000000, v42
	v_mul_f32_e32 v43, 0x42000000, v43
	v_med3_f32 v42, v42, s33, v236
	v_med3_f32 v43, v43, s33, v236
	s_nop 0
	v_cvt_pk_fp8_f32 v45, v42, v43
	v_mul_f32_e32 v44, 0x42000000, v44
	v_mul_f32_e32 v41, 0x42000000, v41
	v_med3_f32 v42, v44, s33, v236
	v_med3_f32 v41, v41, s33, v236
	v_cvt_pk_fp8_f32 v45, v42, v41 op_sel:[0,0,1]
	global_store_dword v[6:7], v45, off offset:-1024

.LBB0_1702:
	s_andn2_b64 vcc, exec, s[0:1]
	s_cbranch_vccnz .LBB0_1704
	v_mul_f32_e32 v35, 0x42000000, v35
	v_mul_f32_e32 v36, 0x42000000, v36
	v_med3_f32 v35, v35, s33, v236
	v_med3_f32 v36, v36, s33, v236
	s_nop 0
	v_cvt_pk_fp8_f32 v41, v35, v36
	v_mul_f32_e32 v37, 0x42000000, v37
	v_mul_f32_e32 v34, 0x42000000, v34
	v_med3_f32 v35, v37, s33, v236
	v_med3_f32 v34, v34, s33, v236
	v_cvt_pk_fp8_f32 v41, v35, v34 op_sel:[0,0,1]
	global_store_dword v[6:7], v41, off offset:-768

.LBB0_1706:
	s_andn2_b64 vcc, exec, s[0:1]
	s_cbranch_vccnz .LBB0_1708
	v_mul_f32_e32 v31, 0x42000000, v31
	v_mul_f32_e32 v32, 0x42000000, v32
	v_med3_f32 v31, v31, s33, v236
	v_med3_f32 v32, v32, s33, v236
	s_nop 0
	v_cvt_pk_fp8_f32 v34, v31, v32
	v_mul_f32_e32 v33, 0x42000000, v33
	v_mul_f32_e32 v30, 0x42000000, v30
	v_med3_f32 v31, v33, s33, v236
	v_med3_f32 v30, v30, s33, v236
	v_cvt_pk_fp8_f32 v34, v31, v30 op_sel:[0,0,1]
	global_store_dword v[6:7], v34, off offset:-512

.LBB0_1710:
	s_andn2_b64 vcc, exec, s[0:1]
	s_cbranch_vccnz .LBB0_1712
	v_mul_f32_e32 v27, 0x42000000, v27
	v_mul_f32_e32 v28, 0x42000000, v28
	v_med3_f32 v27, v27, s33, v236
	v_med3_f32 v28, v28, s33, v236
	s_nop 0
	v_cvt_pk_fp8_f32 v30, v27, v28
	v_mul_f32_e32 v29, 0x42000000, v29
	v_mul_f32_e32 v26, 0x42000000, v26
	v_med3_f32 v27, v29, s33, v236
	v_med3_f32 v26, v26, s33, v236
	v_cvt_pk_fp8_f32 v30, v27, v26 op_sel:[0,0,1]
	global_store_dword v[6:7], v30, off offset:-256

.LBB0_1714:
	s_andn2_b64 vcc, exec, s[0:1]
	s_cbranch_vccnz .LBB0_1716
	v_mul_f32_e32 v23, 0x42000000, v23
	v_mul_f32_e32 v24, 0x42000000, v24
	v_med3_f32 v23, v23, s33, v236
	v_med3_f32 v24, v24, s33, v236
	s_nop 0
	v_cvt_pk_fp8_f32 v26, v23, v24
	v_mul_f32_e32 v25, 0x42000000, v25
	v_mul_f32_e32 v22, 0x42000000, v22
	v_med3_f32 v23, v25, s33, v236
	v_med3_f32 v22, v22, s33, v236
	v_cvt_pk_fp8_f32 v26, v23, v22 op_sel:[0,0,1]
	global_store_dword v[6:7], v26, off

.LBB0_1718:
	s_andn2_b64 vcc, exec, s[0:1]
	s_cbranch_vccnz .LBB0_1720
	v_mul_f32_e32 v19, 0x42000000, v19
	v_mul_f32_e32 v20, 0x42000000, v20
	v_med3_f32 v19, v19, s33, v236
	v_med3_f32 v20, v20, s33, v236
	s_nop 0
	v_cvt_pk_fp8_f32 v22, v19, v20
	v_mul_f32_e32 v21, 0x42000000, v21
	v_mul_f32_e32 v18, 0x42000000, v18
	v_med3_f32 v19, v21, s33, v236
	v_med3_f32 v18, v18, s33, v236
	v_cvt_pk_fp8_f32 v22, v19, v18 op_sel:[0,0,1]
	global_store_dword v[6:7], v22, off offset:256

.LBB0_1722:
	s_andn2_b64 vcc, exec, s[0:1]
	s_cbranch_vccnz .LBB0_1724
	v_mul_f32_e32 v13, 0x42000000, v13
	v_mul_f32_e32 v14, 0x42000000, v14
	v_med3_f32 v13, v13, s33, v236
	v_med3_f32 v14, v14, s33, v236
	s_nop 0
	v_cvt_pk_fp8_f32 v18, v13, v14
	v_mul_f32_e32 v15, 0x42000000, v15
	v_mul_f32_e32 v12, 0x42000000, v12
	v_med3_f32 v13, v15, s33, v236
	v_med3_f32 v12, v12, s33, v236
	v_cvt_pk_fp8_f32 v18, v13, v12 op_sel:[0,0,1]
	global_store_dword v[6:7], v18, off offset:512

.LBB0_1726:
	s_andn2_b64 vcc, exec, s[0:1]
	s_cbranch_vccnz .LBB0_1695
	v_mul_f32_e32 v9, 0x42000000, v9
	v_mul_f32_e32 v10, 0x42000000, v10
	v_med3_f32 v9, v9, s33, v236
	v_med3_f32 v10, v10, s33, v236
	s_nop 0
	v_cvt_pk_fp8_f32 v12, v9, v10
	v_mul_f32_e32 v11, 0x42000000, v11
	v_mul_f32_e32 v8, 0x42000000, v8
	v_med3_f32 v9, v11, s33, v236
	v_med3_f32 v8, v8, s33, v236
	v_cvt_pk_fp8_f32 v12, v9, v8 op_sel:[0,0,1]
	global_store_dword v[6:7], v12, off offset:768
	s_branch .LBB0_1695

.LBB0_1832:
	s_or_b64 exec, exec, s[2:3]
	s_lshl_b64 s[0:1], s[76:77], 2
	s_add_u32 s2, s16, s0
	s_addc_u32 s3, s17, s1
	s_add_u32 s0, s6, s0
	s_addc_u32 s1, s7, s1
	v_lshlrev_b64 v[138:139], 2, v[194:195]
	s_waitcnt lgkmcnt(0)
	s_barrier
	v_lshl_add_u64 v[150:151], s[2:3], 0, v[138:139]
	v_lshl_add_u64 v[148:149], s[0:1], 0, v[138:139]
	global_load_dwordx4 v[130:133], v[150:151], off offset:16
	global_load_dwordx4 v[134:137], v[150:151], off
	global_load_dwordx4 v[138:141], v[148:149], off offset:16
	global_load_dwordx4 v[142:145], v[148:149], off
	v_lshl_add_u32 v0, v230, 3, 0
	ds_read_b64 v[152:153], v0 offset:8192
	v_lshlrev_b64 v[146:147], 11, v[228:229]
	v_lshl_add_u64 v[154:155], v[146:147], 0, v[194:195]
	s_mov_b64 s[0:1], 0x80
	s_waitcnt lgkmcnt(0)
	v_pk_fma_f32 v[122:123], v[122:123], v[152:153], v[152:153] op_sel:[0,1,0] op_sel_hi:[1,1,0]
	v_pk_fma_f32 v[124:125], v[124:125], v[152:153], v[152:153] op_sel:[0,1,0] op_sel_hi:[1,1,0]
	s_waitcnt vmcnt(0)
	v_pk_fma_f32 v[158:159], v[134:135], v[122:123], v[142:143]
	v_pk_fma_f32 v[122:123], v[126:127], v[152:153], v[152:153] op_sel:[0,1,0] op_sel_hi:[1,1,0]
	v_pk_fma_f32 v[156:157], v[136:137], v[124:125], v[144:145]
	v_pk_fma_f32 v[124:125], v[128:129], v[152:153], v[152:153] op_sel:[0,1,0] op_sel_hi:[1,1,0]
	v_pk_fma_f32 v[128:129], v[130:131], v[122:123], v[138:139]
	v_cvt_pk_bf16_f32 v122, v158, v159
	v_cvt_pk_bf16_f32 v123, v156, v157
	v_pk_fma_f32 v[126:127], v[132:133], v[124:125], v[140:141]
	v_cvt_pk_bf16_f32 v124, v128, v129
	s_nop 0
	v_cvt_pk_bf16_f32 v125, v126, v127
	global_store_dwordx4 v[226:227], v[122:125], off
	s_nop 1
	v_mul_f32_e32 v122, s22, v158
	v_mul_f32_e32 v123, s22, v159
	v_med3_f32 v152, v122, s33, v236
	v_med3_f32 v123, v123, s33, v236
	s_nop 0
	v_cvt_pk_fp8_f32 v122, v152, v123
	v_mul_f32_e32 v124, s22, v156
	v_mul_f32_e32 v125, s22, v157
	v_med3_f32 v124, v124, s33, v236
	v_med3_f32 v125, v125, s33, v236
	v_cvt_pk_fp8_f32 v122, v124, v125 op_sel:[0,0,1]
	v_mul_f32_e32 v123, s22, v128
	v_mul_f32_e32 v124, s22, v129
	v_mul_f32_e32 v125, s22, v126
	v_mul_f32_e32 v126, s22, v127
	v_med3_f32 v127, v123, s33, v236
	v_med3_f32 v124, v124, s33, v236
	s_nop 0
	v_cvt_pk_fp8_f32 v123, v127, v124
	v_med3_f32 v125, v125, s33, v236
	v_med3_f32 v126, v126, s33, v236
	v_cvt_pk_fp8_f32 v123, v125, v126 op_sel:[0,0,1]
	v_lshl_add_u64 v[124:125], s[10:11], 0, v[154:155]
	global_store_dwordx2 v[124:125], v[122:123], off
	ds_read_b64 v[124:125], v0 offset:8320
	v_lshlrev_b64 v[122:123], 11, v[224:225]
	v_lshl_add_u64 v[126:127], v[122:123], 0, v[194:195]
	s_waitcnt lgkmcnt(0)
	v_pk_fma_f32 v[114:115], v[114:115], v[124:125], v[124:125] op_sel:[0,1,0] op_sel_hi:[1,1,0]
	v_pk_fma_f32 v[116:117], v[116:117], v[124:125], v[124:125] op_sel:[0,1,0] op_sel_hi:[1,1,0]
	v_pk_fma_f32 v[152:153], v[134:135], v[114:115], v[142:143]
	v_pk_fma_f32 v[114:115], v[118:119], v[124:125], v[124:125] op_sel:[0,1,0] op_sel_hi:[1,1,0]
	v_pk_fma_f32 v[128:129], v[136:137], v[116:117], v[144:145]
	v_pk_fma_f32 v[116:117], v[120:121], v[124:125], v[124:125] op_sel:[0,1,0] op_sel_hi:[1,1,0]
	v_pk_fma_f32 v[120:121], v[130:131], v[114:115], v[138:139]
	v_cvt_pk_bf16_f32 v114, v152, v153
	v_cvt_pk_bf16_f32 v115, v128, v129
	v_pk_fma_f32 v[118:119], v[132:133], v[116:117], v[140:141]
	v_cvt_pk_bf16_f32 v116, v120, v121
	s_nop 0
	v_cvt_pk_bf16_f32 v117, v118, v119
	global_store_dwordx4 v[222:223], v[114:117], off
	s_nop 1
	v_mul_f32_e32 v114, s22, v152
	v_mul_f32_e32 v115, s22, v153
	v_med3_f32 v124, v114, s33, v236
	v_med3_f32 v115, v115, s33, v236
	s_nop 0
	v_cvt_pk_fp8_f32 v114, v124, v115
	v_mul_f32_e32 v116, s22, v128
	v_mul_f32_e32 v117, s22, v129
	v_med3_f32 v116, v116, s33, v236
	v_med3_f32 v117, v117, s33, v236
	v_cvt_pk_fp8_f32 v114, v116, v117 op_sel:[0,0,1]
	v_mul_f32_e32 v115, s22, v120
	v_mul_f32_e32 v116, s22, v121
	v_mul_f32_e32 v117, s22, v118
	v_mul_f32_e32 v118, s22, v119
	v_med3_f32 v119, v115, s33, v236
	v_med3_f32 v116, v116, s33, v236
	s_nop 0
	v_cvt_pk_fp8_f32 v115, v119, v116
	v_med3_f32 v117, v117, s33, v236
	v_med3_f32 v118, v118, s33, v236
	v_cvt_pk_fp8_f32 v115, v117, v118 op_sel:[0,0,1]
	ds_read_b64 v[118:119], v0 offset:8448
	v_lshl_add_u64 v[116:117], s[10:11], 0, v[126:127]
	global_store_dwordx2 v[116:117], v[114:115], off
	v_lshlrev_b64 v[114:115], 11, v[220:221]
	s_waitcnt lgkmcnt(0)
	v_pk_fma_f32 v[110:111], v[110:111], v[118:119], v[118:119] op_sel:[0,1,0] op_sel_hi:[1,1,0]
	v_pk_fma_f32 v[112:113], v[112:113], v[118:119], v[118:119] op_sel:[0,1,0] op_sel_hi:[1,1,0]
	v_pk_fma_f32 v[106:107], v[106:107], v[118:119], v[118:119] op_sel:[0,1,0] op_sel_hi:[1,1,0]
	v_pk_fma_f32 v[112:113], v[136:137], v[112:113], v[144:145]
	v_pk_fma_f32 v[110:111], v[134:135], v[110:111], v[142:143]
	v_pk_fma_f32 v[108:109], v[108:109], v[118:119], v[118:119] op_sel:[0,1,0] op_sel_hi:[1,1,0]
	v_pk_fma_f32 v[120:121], v[130:131], v[106:107], v[138:139]
	v_cvt_pk_bf16_f32 v106, v110, v111
	v_cvt_pk_bf16_f32 v107, v112, v113
	v_pk_fma_f32 v[118:119], v[132:133], v[108:109], v[140:141]
	v_cvt_pk_bf16_f32 v108, v120, v121
	v_lshl_add_u64 v[116:117], v[114:115], 0, v[194:195]
	v_cvt_pk_bf16_f32 v109, v118, v119
	global_store_dwordx4 v[218:219], v[106:109], off
	s_nop 1
	v_mul_f32_e32 v106, s22, v110
	v_mul_f32_e32 v107, s22, v111
	v_med3_f32 v110, v106, s33, v236
	v_med3_f32 v107, v107, s33, v236
	s_nop 0
	v_cvt_pk_fp8_f32 v106, v110, v107
	v_mul_f32_e32 v108, s22, v112
	v_mul_f32_e32 v109, s22, v113
	v_med3_f32 v108, v108, s33, v236
	v_med3_f32 v109, v109, s33, v236
	v_cvt_pk_fp8_f32 v106, v108, v109 op_sel:[0,0,1]
	v_mul_f32_e32 v107, s22, v120
	v_mul_f32_e32 v108, s22, v121
	v_med3_f32 v111, v107, s33, v236
	v_med3_f32 v108, v108, s33, v236
	s_nop 0
	v_cvt_pk_fp8_f32 v107, v111, v108
	v_mul_f32_e32 v109, s22, v118
	v_mul_f32_e32 v110, s22, v119
	v_med3_f32 v109, v109, s33, v236
	v_med3_f32 v110, v110, s33, v236
	v_cvt_pk_fp8_f32 v107, v109, v110 op_sel:[0,0,1]
	v_lshl_add_u64 v[108:109], s[10:11], 0, v[116:117]
	global_store_dwordx2 v[108:109], v[106:107], off
	ds_read_b64 v[108:109], v0 offset:8576
	v_lshlrev_b64 v[106:107], 11, v[216:217]
	v_lshl_add_u64 v[110:111], v[106:107], 0, v[194:195]
	s_waitcnt lgkmcnt(0)
	v_pk_fma_f32 v[98:99], v[98:99], v[108:109], v[108:109] op_sel:[0,1,0] op_sel_hi:[1,1,0]
	v_pk_fma_f32 v[100:101], v[100:101], v[108:109], v[108:109] op_sel:[0,1,0] op_sel_hi:[1,1,0]
	v_pk_fma_f32 v[116:117], v[134:135], v[98:99], v[142:143]
	v_pk_fma_f32 v[98:99], v[102:103], v[108:109], v[108:109] op_sel:[0,1,0] op_sel_hi:[1,1,0]
	v_pk_fma_f32 v[112:113], v[136:137], v[100:101], v[144:145]
	v_pk_fma_f32 v[100:101], v[104:105], v[108:109], v[108:109] op_sel:[0,1,0] op_sel_hi:[1,1,0]
	v_pk_fma_f32 v[104:105], v[130:131], v[98:99], v[138:139]
	v_cvt_pk_bf16_f32 v98, v116, v117
	v_cvt_pk_bf16_f32 v99, v112, v113
	v_pk_fma_f32 v[102:103], v[132:133], v[100:101], v[140:141]
	v_cvt_pk_bf16_f32 v100, v104, v105
	s_nop 0
	v_cvt_pk_bf16_f32 v101, v102, v103
	global_store_dwordx4 v[214:215], v[98:101], off
	s_nop 1
	v_mul_f32_e32 v98, s22, v116
	v_mul_f32_e32 v99, s22, v117
	v_med3_f32 v108, v98, s33, v236
	v_med3_f32 v99, v99, s33, v236
	s_nop 0
	v_cvt_pk_fp8_f32 v98, v108, v99
	v_mul_f32_e32 v100, s22, v112
	v_mul_f32_e32 v101, s22, v113
	v_med3_f32 v100, v100, s33, v236
	v_med3_f32 v101, v101, s33, v236
	v_cvt_pk_fp8_f32 v98, v100, v101 op_sel:[0,0,1]
	v_mul_f32_e32 v99, s22, v104
	v_mul_f32_e32 v100, s22, v105
	v_mul_f32_e32 v101, s22, v102
	v_mul_f32_e32 v102, s22, v103
	v_med3_f32 v103, v99, s33, v236
	v_med3_f32 v100, v100, s33, v236
	s_nop 0
	v_cvt_pk_fp8_f32 v99, v103, v100
	v_med3_f32 v101, v101, s33, v236
	v_med3_f32 v102, v102, s33, v236
	v_cvt_pk_fp8_f32 v99, v101, v102 op_sel:[0,0,1]
	v_lshl_add_u64 v[100:101], s[10:11], 0, v[110:111]
	global_store_dwordx2 v[100:101], v[98:99], off
	ds_read_b64 v[100:101], v0 offset:9216
	v_lshlrev_b64 v[98:99], 11, v[212:213]
	v_lshl_add_u64 v[102:103], v[98:99], 0, v[194:195]
	s_waitcnt lgkmcnt(0)
	v_pk_fma_f32 v[90:91], v[90:91], v[100:101], v[100:101] op_sel:[0,1,0] op_sel_hi:[1,1,0]
	v_pk_fma_f32 v[92:93], v[92:93], v[100:101], v[100:101] op_sel:[0,1,0] op_sel_hi:[1,1,0]
	v_pk_fma_f32 v[108:109], v[134:135], v[90:91], v[142:143]
	v_pk_fma_f32 v[90:91], v[94:95], v[100:101], v[100:101] op_sel:[0,1,0] op_sel_hi:[1,1,0]
	v_pk_fma_f32 v[104:105], v[136:137], v[92:93], v[144:145]
	v_pk_fma_f32 v[92:93], v[96:97], v[100:101], v[100:101] op_sel:[0,1,0] op_sel_hi:[1,1,0]
	v_pk_fma_f32 v[96:97], v[130:131], v[90:91], v[138:139]
	v_cvt_pk_bf16_f32 v90, v108, v109
	v_cvt_pk_bf16_f32 v91, v104, v105
	v_pk_fma_f32 v[94:95], v[132:133], v[92:93], v[140:141]
	v_cvt_pk_bf16_f32 v92, v96, v97
	s_nop 0
	v_cvt_pk_bf16_f32 v93, v94, v95
	global_store_dwordx4 v[210:211], v[90:93], off
	s_nop 1
	v_mul_f32_e32 v90, s22, v108
	v_mul_f32_e32 v91, s22, v109
	v_med3_f32 v100, v90, s33, v236
	v_med3_f32 v91, v91, s33, v236
	s_nop 0
	v_cvt_pk_fp8_f32 v90, v100, v91
	v_mul_f32_e32 v92, s22, v104
	v_mul_f32_e32 v93, s22, v105
	v_med3_f32 v92, v92, s33, v236
	v_med3_f32 v93, v93, s33, v236
	v_cvt_pk_fp8_f32 v90, v92, v93 op_sel:[0,0,1]
	v_mul_f32_e32 v91, s22, v96
	v_mul_f32_e32 v92, s22, v97
	v_mul_f32_e32 v93, s22, v94
	v_mul_f32_e32 v94, s22, v95
	v_med3_f32 v95, v91, s33, v236
	v_med3_f32 v92, v92, s33, v236
	s_nop 0
	v_cvt_pk_fp8_f32 v91, v95, v92
	v_med3_f32 v93, v93, s33, v236
	v_med3_f32 v94, v94, s33, v236
	v_cvt_pk_fp8_f32 v91, v93, v94 op_sel:[0,0,1]
	v_lshl_add_u64 v[92:93], s[10:11], 0, v[102:103]
	global_store_dwordx2 v[92:93], v[90:91], off
	ds_read_b64 v[92:93], v0 offset:9344
	v_lshlrev_b64 v[90:91], 11, v[208:209]
	v_lshl_add_u64 v[94:95], v[90:91], 0, v[194:195]
	s_waitcnt lgkmcnt(0)
	v_pk_fma_f32 v[82:83], v[82:83], v[92:93], v[92:93] op_sel:[0,1,0] op_sel_hi:[1,1,0]
	v_pk_fma_f32 v[84:85], v[84:85], v[92:93], v[92:93] op_sel:[0,1,0] op_sel_hi:[1,1,0]
	v_pk_fma_f32 v[100:101], v[134:135], v[82:83], v[142:143]
	v_pk_fma_f32 v[82:83], v[86:87], v[92:93], v[92:93] op_sel:[0,1,0] op_sel_hi:[1,1,0]
	v_pk_fma_f32 v[96:97], v[136:137], v[84:85], v[144:145]
	v_pk_fma_f32 v[84:85], v[88:89], v[92:93], v[92:93] op_sel:[0,1,0] op_sel_hi:[1,1,0]
	v_pk_fma_f32 v[88:89], v[130:131], v[82:83], v[138:139]
	v_cvt_pk_bf16_f32 v82, v100, v101
	v_cvt_pk_bf16_f32 v83, v96, v97
	v_pk_fma_f32 v[86:87], v[132:133], v[84:85], v[140:141]
	v_cvt_pk_bf16_f32 v84, v88, v89
	s_nop 0
	v_cvt_pk_bf16_f32 v85, v86, v87
	global_store_dwordx4 v[206:207], v[82:85], off
	s_nop 1
	v_mul_f32_e32 v82, s22, v100
	v_mul_f32_e32 v83, s22, v101
	v_med3_f32 v92, v82, s33, v236
	v_med3_f32 v83, v83, s33, v236
	s_nop 0
	v_cvt_pk_fp8_f32 v82, v92, v83
	v_mul_f32_e32 v84, s22, v96
	v_mul_f32_e32 v85, s22, v97
	v_med3_f32 v84, v84, s33, v236
	v_med3_f32 v85, v85, s33, v236
	v_cvt_pk_fp8_f32 v82, v84, v85 op_sel:[0,0,1]
	v_mul_f32_e32 v83, s22, v88
	v_mul_f32_e32 v84, s22, v89
	v_mul_f32_e32 v85, s22, v86
	v_mul_f32_e32 v86, s22, v87
	v_med3_f32 v87, v83, s33, v236
	v_med3_f32 v84, v84, s33, v236
	s_nop 0
	v_cvt_pk_fp8_f32 v83, v87, v84
	v_med3_f32 v85, v85, s33, v236
	v_med3_f32 v86, v86, s33, v236
	v_cvt_pk_fp8_f32 v83, v85, v86 op_sel:[0,0,1]
	v_lshl_add_u64 v[84:85], s[10:11], 0, v[94:95]
	global_store_dwordx2 v[84:85], v[82:83], off
	ds_read_b64 v[84:85], v0 offset:9472
	v_lshlrev_b64 v[82:83], 11, v[204:205]
	v_lshl_add_u64 v[86:87], v[82:83], 0, v[194:195]
	s_waitcnt lgkmcnt(0)
	v_pk_fma_f32 v[74:75], v[74:75], v[84:85], v[84:85] op_sel:[0,1,0] op_sel_hi:[1,1,0]
	v_pk_fma_f32 v[76:77], v[76:77], v[84:85], v[84:85] op_sel:[0,1,0] op_sel_hi:[1,1,0]
	v_pk_fma_f32 v[92:93], v[134:135], v[74:75], v[142:143]
	v_pk_fma_f32 v[74:75], v[78:79], v[84:85], v[84:85] op_sel:[0,1,0] op_sel_hi:[1,1,0]
	v_pk_fma_f32 v[88:89], v[136:137], v[76:77], v[144:145]
	v_pk_fma_f32 v[76:77], v[80:81], v[84:85], v[84:85] op_sel:[0,1,0] op_sel_hi:[1,1,0]
	v_pk_fma_f32 v[80:81], v[130:131], v[74:75], v[138:139]
	v_cvt_pk_bf16_f32 v74, v92, v93
	v_cvt_pk_bf16_f32 v75, v88, v89
	v_pk_fma_f32 v[78:79], v[132:133], v[76:77], v[140:141]
	v_cvt_pk_bf16_f32 v76, v80, v81
	s_nop 0
	v_cvt_pk_bf16_f32 v77, v78, v79
	global_store_dwordx4 v[200:201], v[74:77], off
	s_nop 1
	v_mul_f32_e32 v74, s22, v92
	v_mul_f32_e32 v75, s22, v93
	v_med3_f32 v84, v74, s33, v236
	v_med3_f32 v75, v75, s33, v236
	s_nop 0
	v_cvt_pk_fp8_f32 v74, v84, v75
	v_mul_f32_e32 v76, s22, v88
	v_mul_f32_e32 v77, s22, v89
	v_med3_f32 v76, v76, s33, v236
	v_med3_f32 v77, v77, s33, v236
	v_cvt_pk_fp8_f32 v74, v76, v77 op_sel:[0,0,1]
	v_mul_f32_e32 v75, s22, v80
	v_mul_f32_e32 v76, s22, v81
	v_mul_f32_e32 v77, s22, v78
	v_mul_f32_e32 v78, s22, v79
	v_med3_f32 v79, v75, s33, v236
	v_med3_f32 v76, v76, s33, v236
	s_nop 0
	v_cvt_pk_fp8_f32 v75, v79, v76
	v_med3_f32 v77, v77, s33, v236
	v_med3_f32 v78, v78, s33, v236
	v_lshlrev_b64 v[84:85], 11, v[196:197]
	v_cvt_pk_fp8_f32 v75, v77, v78 op_sel:[0,0,1]
	v_lshl_add_u64 v[76:77], s[10:11], 0, v[86:87]
	v_lshl_add_u64 v[86:87], v[194:195], 0, s[0:1]
	v_lshl_add_u64 v[92:93], v[146:147], 0, v[86:87]
	global_store_dwordx2 v[76:77], v[74:75], off
	ds_read_b64 v[74:75], v0 offset:9600
	v_lshl_add_u64 v[76:77], v[84:85], 0, v[194:195]
	s_waitcnt lgkmcnt(0)
	v_pk_fma_f32 v[66:67], v[66:67], v[74:75], v[74:75] op_sel:[0,1,0] op_sel_hi:[1,1,0]
	v_pk_fma_f32 v[68:69], v[68:69], v[74:75], v[74:75] op_sel:[0,1,0] op_sel_hi:[1,1,0]
	v_pk_fma_f32 v[80:81], v[134:135], v[66:67], v[142:143]
	v_pk_fma_f32 v[66:67], v[70:71], v[74:75], v[74:75] op_sel:[0,1,0] op_sel_hi:[1,1,0]
	v_pk_fma_f32 v[78:79], v[136:137], v[68:69], v[144:145]
	v_pk_fma_f32 v[68:69], v[72:73], v[74:75], v[74:75] op_sel:[0,1,0] op_sel_hi:[1,1,0]
	v_pk_fma_f32 v[72:73], v[130:131], v[66:67], v[138:139]
	v_cvt_pk_bf16_f32 v66, v80, v81
	v_cvt_pk_bf16_f32 v67, v78, v79
	v_pk_fma_f32 v[70:71], v[132:133], v[68:69], v[140:141]
	v_cvt_pk_bf16_f32 v68, v72, v73
	s_nop 0
	v_cvt_pk_bf16_f32 v69, v70, v71
	global_store_dwordx4 v[198:199], v[66:69], off
	s_nop 1
	v_mul_f32_e32 v66, s22, v80
	v_mul_f32_e32 v67, s22, v81
	v_med3_f32 v74, v66, s33, v236
	v_med3_f32 v67, v67, s33, v236
	s_nop 0
	v_cvt_pk_fp8_f32 v66, v74, v67
	v_mul_f32_e32 v68, s22, v78
	v_mul_f32_e32 v69, s22, v79
	v_med3_f32 v68, v68, s33, v236
	v_med3_f32 v69, v69, s33, v236
	v_cvt_pk_fp8_f32 v66, v68, v69 op_sel:[0,0,1]
	v_mul_f32_e32 v67, s22, v72
	v_mul_f32_e32 v68, s22, v73
	v_mul_f32_e32 v69, s22, v70
	v_mul_f32_e32 v70, s22, v71
	v_med3_f32 v71, v67, s33, v236
	v_med3_f32 v68, v68, s33, v236
	s_nop 0
	v_cvt_pk_fp8_f32 v67, v71, v68
	v_med3_f32 v69, v69, s33, v236
	v_med3_f32 v70, v70, s33, v236
	v_cvt_pk_fp8_f32 v67, v69, v70 op_sel:[0,0,1]
	v_lshl_add_u64 v[68:69], s[10:11], 0, v[76:77]
	global_store_dwordx2 v[68:69], v[66:67], off
	global_load_dwordx4 v[66:69], v[150:151], off offset:528
	global_load_dwordx4 v[74:77], v[150:151], off offset:512
	global_load_dwordx4 v[70:73], v[148:149], off offset:528
	global_load_dwordx4 v[78:81], v[148:149], off offset:512
	ds_read_b64 v[88:89], v0 offset:8192
	s_waitcnt lgkmcnt(0)
	v_pk_fma_f32 v[58:59], v[58:59], v[88:89], v[88:89] op_sel:[0,1,0] op_sel_hi:[1,1,0]
	v_pk_fma_f32 v[60:61], v[60:61], v[88:89], v[88:89] op_sel:[0,1,0] op_sel_hi:[1,1,0]
	s_waitcnt vmcnt(0)
	v_pk_fma_f32 v[96:97], v[74:75], v[58:59], v[78:79]
	v_pk_fma_f32 v[58:59], v[62:63], v[88:89], v[88:89] op_sel:[0,1,0] op_sel_hi:[1,1,0]
	v_pk_fma_f32 v[94:95], v[76:77], v[60:61], v[80:81]
	v_pk_fma_f32 v[60:61], v[64:65], v[88:89], v[88:89] op_sel:[0,1,0] op_sel_hi:[1,1,0]
	v_pk_fma_f32 v[64:65], v[66:67], v[58:59], v[70:71]
	v_cvt_pk_bf16_f32 v58, v96, v97
	v_cvt_pk_bf16_f32 v59, v94, v95
	v_lshl_add_u64 v[88:89], v[92:93], 1, s[12:13]
	v_pk_fma_f32 v[62:63], v[68:69], v[60:61], v[72:73]
	v_cvt_pk_bf16_f32 v60, v64, v65
	s_nop 0
	v_cvt_pk_bf16_f32 v61, v62, v63
	global_store_dwordx4 v[88:89], v[58:61], off
	s_nop 1
	v_mul_f32_e32 v58, s22, v96
	v_mul_f32_e32 v59, s22, v97
	v_med3_f32 v88, v58, s33, v236
	v_med3_f32 v59, v59, s33, v236
	s_nop 0
	v_cvt_pk_fp8_f32 v58, v88, v59
	v_mul_f32_e32 v60, s22, v94
	v_mul_f32_e32 v61, s22, v95
	v_med3_f32 v60, v60, s33, v236
	v_med3_f32 v61, v61, s33, v236
	v_cvt_pk_fp8_f32 v58, v60, v61 op_sel:[0,0,1]
	v_mul_f32_e32 v59, s22, v64
	v_mul_f32_e32 v60, s22, v65
	v_mul_f32_e32 v61, s22, v62
	v_mul_f32_e32 v62, s22, v63
	v_med3_f32 v63, v59, s33, v236
	v_med3_f32 v60, v60, s33, v236
	s_nop 0
	v_cvt_pk_fp8_f32 v59, v63, v60
	v_med3_f32 v61, v61, s33, v236
	v_med3_f32 v62, v62, s33, v236
	v_cvt_pk_fp8_f32 v59, v61, v62 op_sel:[0,0,1]
	v_lshl_add_u64 v[60:61], s[10:11], 0, v[92:93]
	global_store_dwordx2 v[60:61], v[58:59], off
	ds_read_b64 v[58:59], v0 offset:8320
	v_lshl_add_u64 v[60:61], v[122:123], 0, v[86:87]
	s_waitcnt lgkmcnt(0)
	v_pk_fma_f32 v[50:51], v[50:51], v[58:59], v[58:59] op_sel:[0,1,0] op_sel_hi:[1,1,0]
	v_pk_fma_f32 v[52:53], v[52:53], v[58:59], v[58:59] op_sel:[0,1,0] op_sel_hi:[1,1,0]
	v_pk_fma_f32 v[64:65], v[74:75], v[50:51], v[78:79]
	v_pk_fma_f32 v[50:51], v[54:55], v[58:59], v[58:59] op_sel:[0,1,0] op_sel_hi:[1,1,0]
	v_pk_fma_f32 v[62:63], v[76:77], v[52:53], v[80:81]
	v_pk_fma_f32 v[52:53], v[56:57], v[58:59], v[58:59] op_sel:[0,1,0] op_sel_hi:[1,1,0]
	v_pk_fma_f32 v[56:57], v[66:67], v[50:51], v[70:71]
	v_cvt_pk_bf16_f32 v50, v64, v65
	v_cvt_pk_bf16_f32 v51, v62, v63
	v_lshl_add_u64 v[58:59], v[60:61], 1, s[12:13]
	v_pk_fma_f32 v[54:55], v[68:69], v[52:53], v[72:73]
	v_cvt_pk_bf16_f32 v52, v56, v57
	s_nop 0
	v_cvt_pk_bf16_f32 v53, v54, v55
	global_store_dwordx4 v[58:59], v[50:53], off
	s_nop 1
	v_mul_f32_e32 v50, s22, v64
	v_mul_f32_e32 v51, s22, v65
	v_med3_f32 v58, v50, s33, v236
	v_med3_f32 v51, v51, s33, v236
	s_nop 0
	v_cvt_pk_fp8_f32 v50, v58, v51
	v_mul_f32_e32 v52, s22, v62
	v_mul_f32_e32 v53, s22, v63
	v_med3_f32 v52, v52, s33, v236
	v_med3_f32 v53, v53, s33, v236
	v_cvt_pk_fp8_f32 v50, v52, v53 op_sel:[0,0,1]
	v_mul_f32_e32 v51, s22, v56
	v_mul_f32_e32 v52, s22, v57
	v_mul_f32_e32 v53, s22, v54
	v_mul_f32_e32 v54, s22, v55
	v_med3_f32 v55, v51, s33, v236
	v_med3_f32 v52, v52, s33, v236
	s_nop 0
	v_cvt_pk_fp8_f32 v51, v55, v52
	v_med3_f32 v53, v53, s33, v236
	v_med3_f32 v54, v54, s33, v236
	v_cvt_pk_fp8_f32 v51, v53, v54 op_sel:[0,0,1]
	v_lshl_add_u64 v[52:53], s[10:11], 0, v[60:61]
	global_store_dwordx2 v[52:53], v[50:51], off
	ds_read_b64 v[50:51], v0 offset:8448
	v_lshl_add_u64 v[52:53], v[114:115], 0, v[86:87]
	s_waitcnt lgkmcnt(0)
	v_pk_fma_f32 v[42:43], v[42:43], v[50:51], v[50:51] op_sel:[0,1,0] op_sel_hi:[1,1,0]
	v_pk_fma_f32 v[44:45], v[44:45], v[50:51], v[50:51] op_sel:[0,1,0] op_sel_hi:[1,1,0]
	v_pk_fma_f32 v[56:57], v[74:75], v[42:43], v[78:79]
	v_pk_fma_f32 v[42:43], v[46:47], v[50:51], v[50:51] op_sel:[0,1,0] op_sel_hi:[1,1,0]
	v_pk_fma_f32 v[54:55], v[76:77], v[44:45], v[80:81]
	v_pk_fma_f32 v[44:45], v[48:49], v[50:51], v[50:51] op_sel:[0,1,0] op_sel_hi:[1,1,0]
	v_pk_fma_f32 v[48:49], v[66:67], v[42:43], v[70:71]
	v_cvt_pk_bf16_f32 v42, v56, v57
	v_cvt_pk_bf16_f32 v43, v54, v55
	v_lshl_add_u64 v[50:51], v[52:53], 1, s[12:13]
	v_pk_fma_f32 v[46:47], v[68:69], v[44:45], v[72:73]
	v_cvt_pk_bf16_f32 v44, v48, v49
	s_nop 0
	v_cvt_pk_bf16_f32 v45, v46, v47
	global_store_dwordx4 v[50:51], v[42:45], off
	s_nop 1
	v_mul_f32_e32 v42, s22, v56
	v_mul_f32_e32 v43, s22, v57
	v_med3_f32 v50, v42, s33, v236
	v_med3_f32 v43, v43, s33, v236
	s_nop 0
	v_cvt_pk_fp8_f32 v42, v50, v43
	v_mul_f32_e32 v44, s22, v54
	v_mul_f32_e32 v45, s22, v55
	v_med3_f32 v44, v44, s33, v236
	v_med3_f32 v45, v45, s33, v236
	v_cvt_pk_fp8_f32 v42, v44, v45 op_sel:[0,0,1]
	v_mul_f32_e32 v43, s22, v48
	v_mul_f32_e32 v44, s22, v49
	v_mul_f32_e32 v45, s22, v46
	v_mul_f32_e32 v46, s22, v47
	v_med3_f32 v47, v43, s33, v236
	v_med3_f32 v44, v44, s33, v236
	s_nop 0
	v_cvt_pk_fp8_f32 v43, v47, v44
	v_med3_f32 v45, v45, s33, v236
	v_med3_f32 v46, v46, s33, v236
	v_cvt_pk_fp8_f32 v43, v45, v46 op_sel:[0,0,1]
	v_lshl_add_u64 v[44:45], s[10:11], 0, v[52:53]
	global_store_dwordx2 v[44:45], v[42:43], off
	ds_read_b64 v[42:43], v0 offset:8576
	v_lshl_add_u64 v[44:45], v[106:107], 0, v[86:87]
	s_waitcnt lgkmcnt(0)
	v_pk_fma_f32 v[34:35], v[34:35], v[42:43], v[42:43] op_sel:[0,1,0] op_sel_hi:[1,1,0]
	v_pk_fma_f32 v[36:37], v[36:37], v[42:43], v[42:43] op_sel:[0,1,0] op_sel_hi:[1,1,0]
	v_pk_fma_f32 v[48:49], v[74:75], v[34:35], v[78:79]
	v_pk_fma_f32 v[34:35], v[38:39], v[42:43], v[42:43] op_sel:[0,1,0] op_sel_hi:[1,1,0]
	v_pk_fma_f32 v[46:47], v[76:77], v[36:37], v[80:81]
	v_pk_fma_f32 v[36:37], v[40:41], v[42:43], v[42:43] op_sel:[0,1,0] op_sel_hi:[1,1,0]
	v_pk_fma_f32 v[40:41], v[66:67], v[34:35], v[70:71]
	v_cvt_pk_bf16_f32 v34, v48, v49
	v_cvt_pk_bf16_f32 v35, v46, v47
	v_lshl_add_u64 v[42:43], v[44:45], 1, s[12:13]
	v_pk_fma_f32 v[38:39], v[68:69], v[36:37], v[72:73]
	v_cvt_pk_bf16_f32 v36, v40, v41
	s_nop 0
	v_cvt_pk_bf16_f32 v37, v38, v39
	global_store_dwordx4 v[42:43], v[34:37], off
	s_nop 1
	v_mul_f32_e32 v34, s22, v48
	v_mul_f32_e32 v35, s22, v49
	v_med3_f32 v42, v34, s33, v236
	v_med3_f32 v35, v35, s33, v236
	s_nop 0
	v_cvt_pk_fp8_f32 v34, v42, v35
	v_mul_f32_e32 v36, s22, v46
	v_mul_f32_e32 v37, s22, v47
	v_med3_f32 v36, v36, s33, v236
	v_med3_f32 v37, v37, s33, v236
	v_cvt_pk_fp8_f32 v34, v36, v37 op_sel:[0,0,1]
	v_mul_f32_e32 v35, s22, v40
	v_mul_f32_e32 v36, s22, v41
	v_mul_f32_e32 v37, s22, v38
	v_mul_f32_e32 v38, s22, v39
	v_med3_f32 v39, v35, s33, v236
	v_med3_f32 v36, v36, s33, v236
	s_nop 0
	v_cvt_pk_fp8_f32 v35, v39, v36
	v_med3_f32 v37, v37, s33, v236
	v_med3_f32 v38, v38, s33, v236
	v_cvt_pk_fp8_f32 v35, v37, v38 op_sel:[0,0,1]
	v_lshl_add_u64 v[36:37], s[10:11], 0, v[44:45]
	global_store_dwordx2 v[36:37], v[34:35], off
	ds_read_b64 v[34:35], v0 offset:9216
	v_lshl_add_u64 v[36:37], v[98:99], 0, v[86:87]
	s_waitcnt lgkmcnt(0)
	v_pk_fma_f32 v[26:27], v[26:27], v[34:35], v[34:35] op_sel:[0,1,0] op_sel_hi:[1,1,0]
	v_pk_fma_f32 v[28:29], v[28:29], v[34:35], v[34:35] op_sel:[0,1,0] op_sel_hi:[1,1,0]
	v_pk_fma_f32 v[40:41], v[74:75], v[26:27], v[78:79]
	v_pk_fma_f32 v[26:27], v[30:31], v[34:35], v[34:35] op_sel:[0,1,0] op_sel_hi:[1,1,0]
	v_pk_fma_f32 v[38:39], v[76:77], v[28:29], v[80:81]
	v_pk_fma_f32 v[28:29], v[32:33], v[34:35], v[34:35] op_sel:[0,1,0] op_sel_hi:[1,1,0]
	v_pk_fma_f32 v[32:33], v[66:67], v[26:27], v[70:71]
	v_cvt_pk_bf16_f32 v26, v40, v41
	v_cvt_pk_bf16_f32 v27, v38, v39
	v_lshl_add_u64 v[34:35], v[36:37], 1, s[12:13]
	v_pk_fma_f32 v[30:31], v[68:69], v[28:29], v[72:73]
	v_cvt_pk_bf16_f32 v28, v32, v33
	s_nop 0
	v_cvt_pk_bf16_f32 v29, v30, v31
	global_store_dwordx4 v[34:35], v[26:29], off
	s_nop 1
	v_mul_f32_e32 v26, s22, v40
	v_mul_f32_e32 v27, s22, v41
	v_med3_f32 v34, v26, s33, v236
	v_med3_f32 v27, v27, s33, v236
	s_nop 0
	v_cvt_pk_fp8_f32 v26, v34, v27
	v_mul_f32_e32 v28, s22, v38
	v_mul_f32_e32 v29, s22, v39
	v_med3_f32 v28, v28, s33, v236
	v_med3_f32 v29, v29, s33, v236
	v_cvt_pk_fp8_f32 v26, v28, v29 op_sel:[0,0,1]
	v_mul_f32_e32 v27, s22, v32
	v_mul_f32_e32 v28, s22, v33
	v_mul_f32_e32 v29, s22, v30
	v_mul_f32_e32 v30, s22, v31
	v_med3_f32 v31, v27, s33, v236
	v_med3_f32 v28, v28, s33, v236
	s_nop 0
	v_cvt_pk_fp8_f32 v27, v31, v28
	v_med3_f32 v29, v29, s33, v236
	v_med3_f32 v30, v30, s33, v236
	v_cvt_pk_fp8_f32 v27, v29, v30 op_sel:[0,0,1]
	v_lshl_add_u64 v[28:29], s[10:11], 0, v[36:37]
	global_store_dwordx2 v[28:29], v[26:27], off
	ds_read_b64 v[26:27], v0 offset:9344
	v_lshl_add_u64 v[28:29], v[90:91], 0, v[86:87]
	s_waitcnt lgkmcnt(0)
	v_pk_fma_f32 v[18:19], v[18:19], v[26:27], v[26:27] op_sel:[0,1,0] op_sel_hi:[1,1,0]
	v_pk_fma_f32 v[20:21], v[20:21], v[26:27], v[26:27] op_sel:[0,1,0] op_sel_hi:[1,1,0]
	v_pk_fma_f32 v[32:33], v[74:75], v[18:19], v[78:79]
	v_pk_fma_f32 v[18:19], v[22:23], v[26:27], v[26:27] op_sel:[0,1,0] op_sel_hi:[1,1,0]
	v_pk_fma_f32 v[30:31], v[76:77], v[20:21], v[80:81]
	v_pk_fma_f32 v[20:21], v[24:25], v[26:27], v[26:27] op_sel:[0,1,0] op_sel_hi:[1,1,0]
	v_pk_fma_f32 v[24:25], v[66:67], v[18:19], v[70:71]
	v_cvt_pk_bf16_f32 v18, v32, v33
	v_cvt_pk_bf16_f32 v19, v30, v31
	v_lshl_add_u64 v[26:27], v[28:29], 1, s[12:13]
	v_pk_fma_f32 v[22:23], v[68:69], v[20:21], v[72:73]
	v_cvt_pk_bf16_f32 v20, v24, v25
	s_nop 0
	v_cvt_pk_bf16_f32 v21, v22, v23
	global_store_dwordx4 v[26:27], v[18:21], off
	s_nop 1
	v_mul_f32_e32 v18, s22, v32
	v_mul_f32_e32 v19, s22, v33
	v_med3_f32 v26, v18, s33, v236
	v_med3_f32 v19, v19, s33, v236
	s_nop 0
	v_cvt_pk_fp8_f32 v18, v26, v19
	v_mul_f32_e32 v20, s22, v30
	v_mul_f32_e32 v21, s22, v31
	v_med3_f32 v20, v20, s33, v236
	v_med3_f32 v21, v21, s33, v236
	v_cvt_pk_fp8_f32 v18, v20, v21 op_sel:[0,0,1]
	v_mul_f32_e32 v19, s22, v24
	v_mul_f32_e32 v20, s22, v25
	v_mul_f32_e32 v21, s22, v22
	v_mul_f32_e32 v22, s22, v23
	v_med3_f32 v23, v19, s33, v236
	v_med3_f32 v20, v20, s33, v236
	s_nop 0
	v_cvt_pk_fp8_f32 v19, v23, v20
	v_med3_f32 v21, v21, s33, v236
	v_med3_f32 v22, v22, s33, v236
	v_cvt_pk_fp8_f32 v19, v21, v22 op_sel:[0,0,1]
	v_lshl_add_u64 v[20:21], s[10:11], 0, v[28:29]
	global_store_dwordx2 v[20:21], v[18:19], off
	ds_read_b64 v[18:19], v0 offset:9472
	v_lshl_add_u64 v[20:21], v[82:83], 0, v[86:87]
	s_waitcnt lgkmcnt(0)
	v_pk_fma_f32 v[10:11], v[10:11], v[18:19], v[18:19] op_sel:[0,1,0] op_sel_hi:[1,1,0]
	v_pk_fma_f32 v[12:13], v[12:13], v[18:19], v[18:19] op_sel:[0,1,0] op_sel_hi:[1,1,0]
	v_pk_fma_f32 v[24:25], v[74:75], v[10:11], v[78:79]
	v_pk_fma_f32 v[10:11], v[14:15], v[18:19], v[18:19] op_sel:[0,1,0] op_sel_hi:[1,1,0]
	v_pk_fma_f32 v[22:23], v[76:77], v[12:13], v[80:81]
	v_pk_fma_f32 v[12:13], v[16:17], v[18:19], v[18:19] op_sel:[0,1,0] op_sel_hi:[1,1,0]
	v_pk_fma_f32 v[16:17], v[66:67], v[10:11], v[70:71]
	v_cvt_pk_bf16_f32 v10, v24, v25
	v_cvt_pk_bf16_f32 v11, v22, v23
	v_lshl_add_u64 v[18:19], v[20:21], 1, s[12:13]
	v_pk_fma_f32 v[14:15], v[68:69], v[12:13], v[72:73]
	v_cvt_pk_bf16_f32 v12, v16, v17
	s_nop 0
	v_cvt_pk_bf16_f32 v13, v14, v15
	global_store_dwordx4 v[18:19], v[10:13], off
	s_nop 1
	v_mul_f32_e32 v10, s22, v24
	v_mul_f32_e32 v11, s22, v25
	v_med3_f32 v18, v10, s33, v236
	v_med3_f32 v11, v11, s33, v236
	s_nop 0
	v_cvt_pk_fp8_f32 v10, v18, v11
	v_mul_f32_e32 v12, s22, v22
	v_mul_f32_e32 v13, s22, v23
	v_med3_f32 v12, v12, s33, v236
	v_med3_f32 v13, v13, s33, v236
	v_cvt_pk_fp8_f32 v10, v12, v13 op_sel:[0,0,1]
	v_mul_f32_e32 v11, s22, v16
	v_mul_f32_e32 v12, s22, v17
	v_mul_f32_e32 v13, s22, v14
	v_mul_f32_e32 v14, s22, v15
	v_med3_f32 v15, v11, s33, v236
	v_med3_f32 v12, v12, s33, v236
	s_nop 0
	v_cvt_pk_fp8_f32 v11, v15, v12
	v_med3_f32 v13, v13, s33, v236
	v_med3_f32 v14, v14, s33, v236
	v_cvt_pk_fp8_f32 v11, v13, v14 op_sel:[0,0,1]
	v_lshl_add_u64 v[12:13], s[10:11], 0, v[20:21]
	global_store_dwordx2 v[12:13], v[10:11], off
	ds_read_b64 v[10:11], v0 offset:9600
	v_lshl_add_u64 v[12:13], v[84:85], 0, v[86:87]
	s_waitcnt lgkmcnt(0)
	v_pk_fma_f32 v[2:3], v[2:3], v[10:11], v[10:11] op_sel:[0,1,0] op_sel_hi:[1,1,0]
	v_pk_fma_f32 v[4:5], v[4:5], v[10:11], v[10:11] op_sel:[0,1,0] op_sel_hi:[1,1,0]
	v_pk_fma_f32 v[16:17], v[74:75], v[2:3], v[78:79]
	v_pk_fma_f32 v[2:3], v[6:7], v[10:11], v[10:11] op_sel:[0,1,0] op_sel_hi:[1,1,0]
	v_pk_fma_f32 v[14:15], v[76:77], v[4:5], v[80:81]
	v_pk_fma_f32 v[4:5], v[8:9], v[10:11], v[10:11] op_sel:[0,1,0] op_sel_hi:[1,1,0]
	v_pk_fma_f32 v[8:9], v[66:67], v[2:3], v[70:71]
	v_cvt_pk_bf16_f32 v2, v16, v17
	v_lshl_add_u64 v[10:11], v[12:13], 1, s[12:13]
	v_pk_fma_f32 v[6:7], v[68:69], v[4:5], v[72:73]
	v_cvt_pk_bf16_f32 v3, v14, v15
	v_cvt_pk_bf16_f32 v4, v8, v9
	v_mul_f32_e32 v0, s22, v16
	v_cvt_pk_bf16_f32 v5, v6, v7
	global_store_dwordx4 v[10:11], v[2:5], off
	v_med3_f32 v0, v0, s33, v236
	s_nop 0
	v_mul_f32_e32 v2, s22, v17
	v_med3_f32 v5, v2, s33, v236
	s_nop 0
	v_cvt_pk_fp8_f32 v2, v0, v5
	v_mul_f32_e32 v3, s22, v14
	v_mul_f32_e32 v4, s22, v15
	v_med3_f32 v3, v3, s33, v236
	v_med3_f32 v4, v4, s33, v236
	v_cvt_pk_fp8_f32 v2, v3, v4 op_sel:[0,0,1]
	v_mul_f32_e32 v0, s22, v8
	v_mul_f32_e32 v3, s22, v9
	v_mul_f32_e32 v4, s22, v6
	v_med3_f32 v0, v0, s33, v236
	v_med3_f32 v6, v3, s33, v236
	s_nop 0
	v_cvt_pk_fp8_f32 v3, v0, v6
	v_mul_f32_e32 v5, s22, v7
	v_med3_f32 v4, v4, s33, v236
	v_med3_f32 v5, v5, s33, v236
	v_cvt_pk_fp8_f32 v3, v4, v5 op_sel:[0,0,1]
	v_lshl_add_u64 v[4:5], s[10:11], 0, v[12:13]
	global_store_dwordx2 v[4:5], v[2:3], off

.LBB0_1877:
	s_or_b64 exec, exec, s[6:7]
	s_lshl_b64 s[0:1], s[76:77], 2
	s_add_u32 s4, s16, s0
	s_addc_u32 s5, s17, s1
	s_add_u32 s0, s2, s0
	s_addc_u32 s1, s3, s1
	v_lshlrev_b64 v[138:139], 2, v[198:199]
	s_waitcnt lgkmcnt(0)
	s_barrier
	v_lshl_add_u64 v[150:151], s[4:5], 0, v[138:139]
	v_lshl_add_u64 v[148:149], s[0:1], 0, v[138:139]
	global_load_dwordx4 v[122:125], v[150:151], off offset:16
	global_load_dwordx4 v[126:129], v[150:151], off
	global_load_dwordx4 v[138:141], v[148:149], off offset:16
	global_load_dwordx4 v[142:145], v[148:149], off
	v_lshl_add_u32 v0, v238, 3, 0
	ds_read_b64 v[152:153], v0 offset:8192
	v_lshlrev_b64 v[146:147], 11, v[232:233]
	v_lshl_add_u64 v[154:155], v[146:147], 0, v[198:199]
	s_mov_b64 s[0:1], 0x80
	s_waitcnt lgkmcnt(0)
	v_pk_fma_f32 v[134:135], v[134:135], v[152:153], v[152:153] op_sel:[0,1,0] op_sel_hi:[1,1,0]
	v_pk_fma_f32 v[136:137], v[136:137], v[152:153], v[152:153] op_sel:[0,1,0] op_sel_hi:[1,1,0]
	v_pk_fma_f32 v[130:131], v[130:131], v[152:153], v[152:153] op_sel:[0,1,0] op_sel_hi:[1,1,0]
	v_pk_fma_f32 v[132:133], v[132:133], v[152:153], v[152:153] op_sel:[0,1,0] op_sel_hi:[1,1,0]
	s_waitcnt vmcnt(1)
	v_pk_fma_f32 v[156:157], v[122:123], v[130:131], v[138:139]
	s_waitcnt vmcnt(0)
	v_pk_fma_f32 v[136:137], v[128:129], v[136:137], v[144:145]
	v_pk_fma_f32 v[134:135], v[126:127], v[134:135], v[142:143]
	v_pk_fma_f32 v[152:153], v[124:125], v[132:133], v[140:141]
	v_cvt_pk_bf16_f32 v130, v134, v135
	v_cvt_pk_bf16_f32 v131, v136, v137
	v_cvt_pk_bf16_f32 v132, v156, v157
	s_nop 0
	v_cvt_pk_bf16_f32 v133, v152, v153
	global_store_dwordx4 v[230:231], v[130:133], off
	s_nop 1
	v_mul_f32_e32 v130, s20, v134
	v_mul_f32_e32 v131, s20, v135
	v_med3_f32 v134, v130, s33, v236
	v_med3_f32 v131, v131, s33, v236
	s_nop 0
	v_cvt_pk_fp8_f32 v130, v134, v131
	v_mul_f32_e32 v132, s20, v136
	v_mul_f32_e32 v133, s20, v137
	v_med3_f32 v132, v132, s33, v236
	v_med3_f32 v133, v133, s33, v236
	v_cvt_pk_fp8_f32 v130, v132, v133 op_sel:[0,0,1]
	v_mul_f32_e32 v131, s20, v156
	v_mul_f32_e32 v132, s20, v157
	v_med3_f32 v135, v131, s33, v236
	v_med3_f32 v132, v132, s33, v236
	s_nop 0
	v_cvt_pk_fp8_f32 v131, v135, v132
	v_mul_f32_e32 v133, s20, v152
	v_mul_f32_e32 v134, s20, v153
	v_med3_f32 v133, v133, s33, v236
	v_med3_f32 v134, v134, s33, v236
	v_cvt_pk_fp8_f32 v131, v133, v134 op_sel:[0,0,1]
	v_lshl_add_u64 v[132:133], s[10:11], 0, v[154:155]
	global_store_dwordx2 v[132:133], v[130:131], off
	ds_read_b64 v[132:133], v0 offset:8320
	v_lshlrev_b64 v[130:131], 11, v[228:229]
	v_lshl_add_u64 v[134:135], v[130:131], 0, v[198:199]
	s_waitcnt lgkmcnt(0)
	v_pk_fma_f32 v[114:115], v[114:115], v[132:133], v[132:133] op_sel:[0,1,0] op_sel_hi:[1,1,0]
	v_pk_fma_f32 v[116:117], v[116:117], v[132:133], v[132:133] op_sel:[0,1,0] op_sel_hi:[1,1,0]
	v_pk_fma_f32 v[152:153], v[126:127], v[114:115], v[142:143]
	v_pk_fma_f32 v[114:115], v[118:119], v[132:133], v[132:133] op_sel:[0,1,0] op_sel_hi:[1,1,0]
	v_pk_fma_f32 v[136:137], v[128:129], v[116:117], v[144:145]
	v_pk_fma_f32 v[116:117], v[120:121], v[132:133], v[132:133] op_sel:[0,1,0] op_sel_hi:[1,1,0]
	v_pk_fma_f32 v[120:121], v[122:123], v[114:115], v[138:139]
	v_cvt_pk_bf16_f32 v114, v152, v153
	v_cvt_pk_bf16_f32 v115, v136, v137
	v_pk_fma_f32 v[118:119], v[124:125], v[116:117], v[140:141]
	v_cvt_pk_bf16_f32 v116, v120, v121
	s_nop 0
	v_cvt_pk_bf16_f32 v117, v118, v119
	global_store_dwordx4 v[226:227], v[114:117], off
	s_nop 1
	v_mul_f32_e32 v114, s20, v152
	v_mul_f32_e32 v115, s20, v153
	v_med3_f32 v132, v114, s33, v236
	v_med3_f32 v115, v115, s33, v236
	s_nop 0
	v_cvt_pk_fp8_f32 v114, v132, v115
	v_mul_f32_e32 v116, s20, v136
	v_mul_f32_e32 v117, s20, v137
	v_med3_f32 v116, v116, s33, v236
	v_med3_f32 v117, v117, s33, v236
	v_cvt_pk_fp8_f32 v114, v116, v117 op_sel:[0,0,1]
	v_mul_f32_e32 v115, s20, v120
	v_mul_f32_e32 v116, s20, v121
	v_mul_f32_e32 v117, s20, v118
	v_mul_f32_e32 v118, s20, v119
	v_med3_f32 v119, v115, s33, v236
	v_med3_f32 v116, v116, s33, v236
	s_nop 0
	v_cvt_pk_fp8_f32 v115, v119, v116
	v_med3_f32 v117, v117, s33, v236
	v_med3_f32 v118, v118, s33, v236
	v_cvt_pk_fp8_f32 v115, v117, v118 op_sel:[0,0,1]
	ds_read_b64 v[118:119], v0 offset:8448
	v_lshl_add_u64 v[116:117], s[10:11], 0, v[134:135]
	global_store_dwordx2 v[116:117], v[114:115], off
	v_lshlrev_b64 v[114:115], 11, v[224:225]
	s_waitcnt lgkmcnt(0)
	v_pk_fma_f32 v[110:111], v[110:111], v[118:119], v[118:119] op_sel:[0,1,0] op_sel_hi:[1,1,0]
	v_pk_fma_f32 v[112:113], v[112:113], v[118:119], v[118:119] op_sel:[0,1,0] op_sel_hi:[1,1,0]
	v_pk_fma_f32 v[106:107], v[106:107], v[118:119], v[118:119] op_sel:[0,1,0] op_sel_hi:[1,1,0]
	v_pk_fma_f32 v[112:113], v[128:129], v[112:113], v[144:145]
	v_pk_fma_f32 v[110:111], v[126:127], v[110:111], v[142:143]
	v_pk_fma_f32 v[108:109], v[108:109], v[118:119], v[118:119] op_sel:[0,1,0] op_sel_hi:[1,1,0]
	v_pk_fma_f32 v[120:121], v[122:123], v[106:107], v[138:139]
	v_cvt_pk_bf16_f32 v106, v110, v111
	v_cvt_pk_bf16_f32 v107, v112, v113
	v_pk_fma_f32 v[118:119], v[124:125], v[108:109], v[140:141]
	v_cvt_pk_bf16_f32 v108, v120, v121
	v_lshl_add_u64 v[116:117], v[114:115], 0, v[198:199]
	v_cvt_pk_bf16_f32 v109, v118, v119
	global_store_dwordx4 v[222:223], v[106:109], off
	s_nop 1
	v_mul_f32_e32 v106, s20, v110
	v_mul_f32_e32 v107, s20, v111
	v_med3_f32 v110, v106, s33, v236
	v_med3_f32 v107, v107, s33, v236
	s_nop 0
	v_cvt_pk_fp8_f32 v106, v110, v107
	v_mul_f32_e32 v108, s20, v112
	v_mul_f32_e32 v109, s20, v113
	v_med3_f32 v108, v108, s33, v236
	v_med3_f32 v109, v109, s33, v236
	v_cvt_pk_fp8_f32 v106, v108, v109 op_sel:[0,0,1]
	v_mul_f32_e32 v107, s20, v120
	v_mul_f32_e32 v108, s20, v121
	v_med3_f32 v111, v107, s33, v236
	v_med3_f32 v108, v108, s33, v236
	s_nop 0
	v_cvt_pk_fp8_f32 v107, v111, v108
	v_mul_f32_e32 v109, s20, v118
	v_mul_f32_e32 v110, s20, v119
	v_med3_f32 v109, v109, s33, v236
	v_med3_f32 v110, v110, s33, v236
	v_cvt_pk_fp8_f32 v107, v109, v110 op_sel:[0,0,1]
	v_lshl_add_u64 v[108:109], s[10:11], 0, v[116:117]
	global_store_dwordx2 v[108:109], v[106:107], off
	ds_read_b64 v[108:109], v0 offset:8576
	v_lshlrev_b64 v[106:107], 11, v[220:221]
	v_lshl_add_u64 v[110:111], v[106:107], 0, v[198:199]
	s_waitcnt lgkmcnt(0)
	v_pk_fma_f32 v[98:99], v[98:99], v[108:109], v[108:109] op_sel:[0,1,0] op_sel_hi:[1,1,0]
	v_pk_fma_f32 v[100:101], v[100:101], v[108:109], v[108:109] op_sel:[0,1,0] op_sel_hi:[1,1,0]
	v_pk_fma_f32 v[116:117], v[126:127], v[98:99], v[142:143]
	v_pk_fma_f32 v[98:99], v[102:103], v[108:109], v[108:109] op_sel:[0,1,0] op_sel_hi:[1,1,0]
	v_pk_fma_f32 v[112:113], v[128:129], v[100:101], v[144:145]
	v_pk_fma_f32 v[100:101], v[104:105], v[108:109], v[108:109] op_sel:[0,1,0] op_sel_hi:[1,1,0]
	v_pk_fma_f32 v[104:105], v[122:123], v[98:99], v[138:139]
	v_cvt_pk_bf16_f32 v98, v116, v117
	v_cvt_pk_bf16_f32 v99, v112, v113
	v_pk_fma_f32 v[102:103], v[124:125], v[100:101], v[140:141]
	v_cvt_pk_bf16_f32 v100, v104, v105
	s_nop 0
	v_cvt_pk_bf16_f32 v101, v102, v103
	global_store_dwordx4 v[218:219], v[98:101], off
	s_nop 1
	v_mul_f32_e32 v98, s20, v116
	v_mul_f32_e32 v99, s20, v117
	v_med3_f32 v108, v98, s33, v236
	v_med3_f32 v99, v99, s33, v236
	s_nop 0
	v_cvt_pk_fp8_f32 v98, v108, v99
	v_mul_f32_e32 v100, s20, v112
	v_mul_f32_e32 v101, s20, v113
	v_med3_f32 v100, v100, s33, v236
	v_med3_f32 v101, v101, s33, v236
	v_cvt_pk_fp8_f32 v98, v100, v101 op_sel:[0,0,1]
	v_mul_f32_e32 v99, s20, v104
	v_mul_f32_e32 v100, s20, v105
	v_mul_f32_e32 v101, s20, v102
	v_mul_f32_e32 v102, s20, v103
	v_med3_f32 v103, v99, s33, v236
	v_med3_f32 v100, v100, s33, v236
	s_nop 0
	v_cvt_pk_fp8_f32 v99, v103, v100
	v_med3_f32 v101, v101, s33, v236
	v_med3_f32 v102, v102, s33, v236
	v_cvt_pk_fp8_f32 v99, v101, v102 op_sel:[0,0,1]
	v_lshl_add_u64 v[100:101], s[10:11], 0, v[110:111]
	global_store_dwordx2 v[100:101], v[98:99], off
	ds_read_b64 v[100:101], v0 offset:9216
	v_lshlrev_b64 v[98:99], 11, v[216:217]
	v_lshl_add_u64 v[102:103], v[98:99], 0, v[198:199]
	s_waitcnt lgkmcnt(0)
	v_pk_fma_f32 v[90:91], v[90:91], v[100:101], v[100:101] op_sel:[0,1,0] op_sel_hi:[1,1,0]
	v_pk_fma_f32 v[92:93], v[92:93], v[100:101], v[100:101] op_sel:[0,1,0] op_sel_hi:[1,1,0]
	v_pk_fma_f32 v[108:109], v[126:127], v[90:91], v[142:143]
	v_pk_fma_f32 v[90:91], v[94:95], v[100:101], v[100:101] op_sel:[0,1,0] op_sel_hi:[1,1,0]
	v_pk_fma_f32 v[104:105], v[128:129], v[92:93], v[144:145]
	v_pk_fma_f32 v[92:93], v[96:97], v[100:101], v[100:101] op_sel:[0,1,0] op_sel_hi:[1,1,0]
	v_pk_fma_f32 v[96:97], v[122:123], v[90:91], v[138:139]
	v_cvt_pk_bf16_f32 v90, v108, v109
	v_cvt_pk_bf16_f32 v91, v104, v105
	v_pk_fma_f32 v[94:95], v[124:125], v[92:93], v[140:141]
	v_cvt_pk_bf16_f32 v92, v96, v97
	s_nop 0
	v_cvt_pk_bf16_f32 v93, v94, v95
	global_store_dwordx4 v[214:215], v[90:93], off
	s_nop 1
	v_mul_f32_e32 v90, s20, v108
	v_mul_f32_e32 v91, s20, v109
	v_med3_f32 v100, v90, s33, v236
	v_med3_f32 v91, v91, s33, v236
	s_nop 0
	v_cvt_pk_fp8_f32 v90, v100, v91
	v_mul_f32_e32 v92, s20, v104
	v_mul_f32_e32 v93, s20, v105
	v_med3_f32 v92, v92, s33, v236
	v_med3_f32 v93, v93, s33, v236
	v_cvt_pk_fp8_f32 v90, v92, v93 op_sel:[0,0,1]
	v_mul_f32_e32 v91, s20, v96
	v_mul_f32_e32 v92, s20, v97
	v_mul_f32_e32 v93, s20, v94
	v_mul_f32_e32 v94, s20, v95
	v_med3_f32 v95, v91, s33, v236
	v_med3_f32 v92, v92, s33, v236
	s_nop 0
	v_cvt_pk_fp8_f32 v91, v95, v92
	v_med3_f32 v93, v93, s33, v236
	v_med3_f32 v94, v94, s33, v236
	v_cvt_pk_fp8_f32 v91, v93, v94 op_sel:[0,0,1]
	v_lshl_add_u64 v[92:93], s[10:11], 0, v[102:103]
	global_store_dwordx2 v[92:93], v[90:91], off
	ds_read_b64 v[92:93], v0 offset:9344
	v_lshlrev_b64 v[90:91], 11, v[212:213]
	v_lshl_add_u64 v[94:95], v[90:91], 0, v[198:199]
	s_waitcnt lgkmcnt(0)
	v_pk_fma_f32 v[82:83], v[82:83], v[92:93], v[92:93] op_sel:[0,1,0] op_sel_hi:[1,1,0]
	v_pk_fma_f32 v[84:85], v[84:85], v[92:93], v[92:93] op_sel:[0,1,0] op_sel_hi:[1,1,0]
	v_pk_fma_f32 v[100:101], v[126:127], v[82:83], v[142:143]
	v_pk_fma_f32 v[82:83], v[86:87], v[92:93], v[92:93] op_sel:[0,1,0] op_sel_hi:[1,1,0]
	v_pk_fma_f32 v[96:97], v[128:129], v[84:85], v[144:145]
	v_pk_fma_f32 v[84:85], v[88:89], v[92:93], v[92:93] op_sel:[0,1,0] op_sel_hi:[1,1,0]
	v_pk_fma_f32 v[88:89], v[122:123], v[82:83], v[138:139]
	v_cvt_pk_bf16_f32 v82, v100, v101
	v_cvt_pk_bf16_f32 v83, v96, v97
	v_pk_fma_f32 v[86:87], v[124:125], v[84:85], v[140:141]
	v_cvt_pk_bf16_f32 v84, v88, v89
	s_nop 0
	v_cvt_pk_bf16_f32 v85, v86, v87
	global_store_dwordx4 v[210:211], v[82:85], off
	s_nop 1
	v_mul_f32_e32 v82, s20, v100
	v_mul_f32_e32 v83, s20, v101
	v_med3_f32 v92, v82, s33, v236
	v_med3_f32 v83, v83, s33, v236
	s_nop 0
	v_cvt_pk_fp8_f32 v82, v92, v83
	v_mul_f32_e32 v84, s20, v96
	v_mul_f32_e32 v85, s20, v97
	v_med3_f32 v84, v84, s33, v236
	v_med3_f32 v85, v85, s33, v236
	v_cvt_pk_fp8_f32 v82, v84, v85 op_sel:[0,0,1]
	v_mul_f32_e32 v83, s20, v88
	v_mul_f32_e32 v84, s20, v89
	v_mul_f32_e32 v85, s20, v86
	v_mul_f32_e32 v86, s20, v87
	v_med3_f32 v87, v83, s33, v236
	v_med3_f32 v84, v84, s33, v236
	s_nop 0
	v_cvt_pk_fp8_f32 v83, v87, v84
	v_med3_f32 v85, v85, s33, v236
	v_med3_f32 v86, v86, s33, v236
	v_cvt_pk_fp8_f32 v83, v85, v86 op_sel:[0,0,1]
	v_lshl_add_u64 v[84:85], s[10:11], 0, v[94:95]
	global_store_dwordx2 v[84:85], v[82:83], off
	ds_read_b64 v[84:85], v0 offset:9472
	v_lshlrev_b64 v[82:83], 11, v[208:209]
	v_lshl_add_u64 v[86:87], v[82:83], 0, v[198:199]
	s_waitcnt lgkmcnt(0)
	v_pk_fma_f32 v[74:75], v[74:75], v[84:85], v[84:85] op_sel:[0,1,0] op_sel_hi:[1,1,0]
	v_pk_fma_f32 v[76:77], v[76:77], v[84:85], v[84:85] op_sel:[0,1,0] op_sel_hi:[1,1,0]
	v_pk_fma_f32 v[92:93], v[126:127], v[74:75], v[142:143]
	v_pk_fma_f32 v[74:75], v[78:79], v[84:85], v[84:85] op_sel:[0,1,0] op_sel_hi:[1,1,0]
	v_pk_fma_f32 v[88:89], v[128:129], v[76:77], v[144:145]
	v_pk_fma_f32 v[76:77], v[80:81], v[84:85], v[84:85] op_sel:[0,1,0] op_sel_hi:[1,1,0]
	v_pk_fma_f32 v[80:81], v[122:123], v[74:75], v[138:139]
	v_cvt_pk_bf16_f32 v74, v92, v93
	v_cvt_pk_bf16_f32 v75, v88, v89
	v_pk_fma_f32 v[78:79], v[124:125], v[76:77], v[140:141]
	v_cvt_pk_bf16_f32 v76, v80, v81
	s_nop 0
	v_cvt_pk_bf16_f32 v77, v78, v79
	global_store_dwordx4 v[206:207], v[74:77], off
	s_nop 1
	v_mul_f32_e32 v74, s20, v92
	v_mul_f32_e32 v75, s20, v93
	v_med3_f32 v84, v74, s33, v236
	v_med3_f32 v75, v75, s33, v236
	s_nop 0
	v_cvt_pk_fp8_f32 v74, v84, v75
	v_mul_f32_e32 v76, s20, v88
	v_mul_f32_e32 v77, s20, v89
	v_med3_f32 v76, v76, s33, v236
	v_med3_f32 v77, v77, s33, v236
	v_cvt_pk_fp8_f32 v74, v76, v77 op_sel:[0,0,1]
	v_mul_f32_e32 v75, s20, v80
	v_mul_f32_e32 v76, s20, v81
	v_mul_f32_e32 v77, s20, v78
	v_mul_f32_e32 v78, s20, v79
	v_med3_f32 v79, v75, s33, v236
	v_med3_f32 v76, v76, s33, v236
	s_nop 0
	v_cvt_pk_fp8_f32 v75, v79, v76
	v_med3_f32 v77, v77, s33, v236
	v_med3_f32 v78, v78, s33, v236
	v_lshlrev_b64 v[84:85], 11, v[200:201]
	v_cvt_pk_fp8_f32 v75, v77, v78 op_sel:[0,0,1]
	v_lshl_add_u64 v[76:77], s[10:11], 0, v[86:87]
	v_lshl_add_u64 v[86:87], v[198:199], 0, s[0:1]
	v_lshl_add_u64 v[92:93], v[146:147], 0, v[86:87]
	global_store_dwordx2 v[76:77], v[74:75], off
	ds_read_b64 v[74:75], v0 offset:9600
	v_lshl_add_u64 v[76:77], v[84:85], 0, v[198:199]
	v_lshl_add_u64 v[96:97], v[92:93], 1, s[12:13]
	s_waitcnt lgkmcnt(0)
	v_pk_fma_f32 v[66:67], v[66:67], v[74:75], v[74:75] op_sel:[0,1,0] op_sel_hi:[1,1,0]
	v_pk_fma_f32 v[68:69], v[68:69], v[74:75], v[74:75] op_sel:[0,1,0] op_sel_hi:[1,1,0]
	v_pk_fma_f32 v[80:81], v[126:127], v[66:67], v[142:143]
	v_pk_fma_f32 v[66:67], v[70:71], v[74:75], v[74:75] op_sel:[0,1,0] op_sel_hi:[1,1,0]
	v_pk_fma_f32 v[78:79], v[128:129], v[68:69], v[144:145]
	v_pk_fma_f32 v[68:69], v[72:73], v[74:75], v[74:75] op_sel:[0,1,0] op_sel_hi:[1,1,0]
	v_pk_fma_f32 v[72:73], v[122:123], v[66:67], v[138:139]
	v_cvt_pk_bf16_f32 v66, v80, v81
	v_cvt_pk_bf16_f32 v67, v78, v79
	v_pk_fma_f32 v[70:71], v[124:125], v[68:69], v[140:141]
	v_cvt_pk_bf16_f32 v68, v72, v73
	s_nop 0
	v_cvt_pk_bf16_f32 v69, v70, v71
	global_store_dwordx4 v[204:205], v[66:69], off
	s_nop 1
	v_mul_f32_e32 v66, s20, v80
	v_mul_f32_e32 v67, s20, v81
	v_med3_f32 v74, v66, s33, v236
	v_med3_f32 v67, v67, s33, v236
	s_nop 0
	v_cvt_pk_fp8_f32 v66, v74, v67
	v_mul_f32_e32 v68, s20, v78
	v_mul_f32_e32 v69, s20, v79
	v_med3_f32 v68, v68, s33, v236
	v_med3_f32 v69, v69, s33, v236
	v_cvt_pk_fp8_f32 v66, v68, v69 op_sel:[0,0,1]
	v_mul_f32_e32 v67, s20, v72
	v_mul_f32_e32 v68, s20, v73
	v_mul_f32_e32 v69, s20, v70
	v_mul_f32_e32 v70, s20, v71
	v_med3_f32 v71, v67, s33, v236
	v_med3_f32 v68, v68, s33, v236
	s_nop 0
	v_cvt_pk_fp8_f32 v67, v71, v68
	v_med3_f32 v69, v69, s33, v236
	v_med3_f32 v70, v70, s33, v236
	v_cvt_pk_fp8_f32 v67, v69, v70 op_sel:[0,0,1]
	v_lshl_add_u64 v[68:69], s[10:11], 0, v[76:77]
	global_store_dwordx2 v[68:69], v[66:67], off
	global_load_dwordx4 v[66:69], v[150:151], off offset:528
	global_load_dwordx4 v[74:77], v[150:151], off offset:512
	global_load_dwordx4 v[70:73], v[148:149], off offset:528
	global_load_dwordx4 v[78:81], v[148:149], off offset:512
	ds_read_b64 v[88:89], v0 offset:8192
	s_waitcnt lgkmcnt(0)
	v_pk_fma_f32 v[62:63], v[62:63], v[88:89], v[88:89] op_sel:[0,1,0] op_sel_hi:[1,1,0]
	v_pk_fma_f32 v[64:65], v[64:65], v[88:89], v[88:89] op_sel:[0,1,0] op_sel_hi:[1,1,0]
	v_pk_fma_f32 v[58:59], v[58:59], v[88:89], v[88:89] op_sel:[0,1,0] op_sel_hi:[1,1,0]
	v_pk_fma_f32 v[60:61], v[60:61], v[88:89], v[88:89] op_sel:[0,1,0] op_sel_hi:[1,1,0]
	s_waitcnt vmcnt(1)
	v_pk_fma_f32 v[94:95], v[66:67], v[58:59], v[70:71]
	s_waitcnt vmcnt(0)
	v_pk_fma_f32 v[64:65], v[76:77], v[64:65], v[80:81]
	v_pk_fma_f32 v[62:63], v[74:75], v[62:63], v[78:79]
	v_pk_fma_f32 v[88:89], v[68:69], v[60:61], v[72:73]
	v_cvt_pk_bf16_f32 v58, v62, v63
	v_cvt_pk_bf16_f32 v59, v64, v65
	v_cvt_pk_bf16_f32 v60, v94, v95
	s_nop 0
	v_cvt_pk_bf16_f32 v61, v88, v89
	global_store_dwordx4 v[96:97], v[58:61], off
	s_nop 1
	v_mul_f32_e32 v58, s20, v62
	v_mul_f32_e32 v59, s20, v63
	v_med3_f32 v62, v58, s33, v236
	v_med3_f32 v59, v59, s33, v236
	s_nop 0
	v_cvt_pk_fp8_f32 v58, v62, v59
	v_mul_f32_e32 v60, s20, v64
	v_mul_f32_e32 v61, s20, v65
	v_med3_f32 v60, v60, s33, v236
	v_med3_f32 v61, v61, s33, v236
	v_cvt_pk_fp8_f32 v58, v60, v61 op_sel:[0,0,1]
	v_mul_f32_e32 v59, s20, v94
	v_mul_f32_e32 v60, s20, v95
	v_med3_f32 v63, v59, s33, v236
	v_med3_f32 v60, v60, s33, v236
	s_nop 0
	v_cvt_pk_fp8_f32 v59, v63, v60
	v_mul_f32_e32 v61, s20, v88
	v_mul_f32_e32 v62, s20, v89
	v_med3_f32 v61, v61, s33, v236
	v_med3_f32 v62, v62, s33, v236
	v_cvt_pk_fp8_f32 v59, v61, v62 op_sel:[0,0,1]
	v_lshl_add_u64 v[60:61], s[10:11], 0, v[92:93]
	global_store_dwordx2 v[60:61], v[58:59], off
	ds_read_b64 v[58:59], v0 offset:8320
	v_lshl_add_u64 v[60:61], v[130:131], 0, v[86:87]
	s_waitcnt lgkmcnt(0)
	v_pk_fma_f32 v[50:51], v[50:51], v[58:59], v[58:59] op_sel:[0,1,0] op_sel_hi:[1,1,0]
	v_pk_fma_f32 v[52:53], v[52:53], v[58:59], v[58:59] op_sel:[0,1,0] op_sel_hi:[1,1,0]
	v_pk_fma_f32 v[64:65], v[74:75], v[50:51], v[78:79]
	v_pk_fma_f32 v[50:51], v[54:55], v[58:59], v[58:59] op_sel:[0,1,0] op_sel_hi:[1,1,0]
	v_pk_fma_f32 v[62:63], v[76:77], v[52:53], v[80:81]
	v_pk_fma_f32 v[52:53], v[56:57], v[58:59], v[58:59] op_sel:[0,1,0] op_sel_hi:[1,1,0]
	v_pk_fma_f32 v[56:57], v[66:67], v[50:51], v[70:71]
	v_cvt_pk_bf16_f32 v50, v64, v65
	v_cvt_pk_bf16_f32 v51, v62, v63
	v_lshl_add_u64 v[58:59], v[60:61], 1, s[12:13]
	v_pk_fma_f32 v[54:55], v[68:69], v[52:53], v[72:73]
	v_cvt_pk_bf16_f32 v52, v56, v57
	s_nop 0
	v_cvt_pk_bf16_f32 v53, v54, v55
	global_store_dwordx4 v[58:59], v[50:53], off
	s_nop 1
	v_mul_f32_e32 v50, s20, v64
	v_mul_f32_e32 v51, s20, v65
	v_med3_f32 v58, v50, s33, v236
	v_med3_f32 v51, v51, s33, v236
	s_nop 0
	v_cvt_pk_fp8_f32 v50, v58, v51
	v_mul_f32_e32 v52, s20, v62
	v_mul_f32_e32 v53, s20, v63
	v_med3_f32 v52, v52, s33, v236
	v_med3_f32 v53, v53, s33, v236
	v_cvt_pk_fp8_f32 v50, v52, v53 op_sel:[0,0,1]
	v_mul_f32_e32 v51, s20, v56
	v_mul_f32_e32 v52, s20, v57
	v_mul_f32_e32 v53, s20, v54
	v_mul_f32_e32 v54, s20, v55
	v_med3_f32 v55, v51, s33, v236
	v_med3_f32 v52, v52, s33, v236
	s_nop 0
	v_cvt_pk_fp8_f32 v51, v55, v52
	v_med3_f32 v53, v53, s33, v236
	v_med3_f32 v54, v54, s33, v236
	v_cvt_pk_fp8_f32 v51, v53, v54 op_sel:[0,0,1]
	v_lshl_add_u64 v[52:53], s[10:11], 0, v[60:61]
	global_store_dwordx2 v[52:53], v[50:51], off
	ds_read_b64 v[50:51], v0 offset:8448
	v_lshl_add_u64 v[52:53], v[114:115], 0, v[86:87]
	s_waitcnt lgkmcnt(0)
	v_pk_fma_f32 v[42:43], v[42:43], v[50:51], v[50:51] op_sel:[0,1,0] op_sel_hi:[1,1,0]
	v_pk_fma_f32 v[44:45], v[44:45], v[50:51], v[50:51] op_sel:[0,1,0] op_sel_hi:[1,1,0]
	v_pk_fma_f32 v[56:57], v[74:75], v[42:43], v[78:79]
	v_pk_fma_f32 v[42:43], v[46:47], v[50:51], v[50:51] op_sel:[0,1,0] op_sel_hi:[1,1,0]
	v_pk_fma_f32 v[54:55], v[76:77], v[44:45], v[80:81]
	v_pk_fma_f32 v[44:45], v[48:49], v[50:51], v[50:51] op_sel:[0,1,0] op_sel_hi:[1,1,0]
	v_pk_fma_f32 v[48:49], v[66:67], v[42:43], v[70:71]
	v_cvt_pk_bf16_f32 v42, v56, v57
	v_cvt_pk_bf16_f32 v43, v54, v55
	v_lshl_add_u64 v[50:51], v[52:53], 1, s[12:13]
	v_pk_fma_f32 v[46:47], v[68:69], v[44:45], v[72:73]
	v_cvt_pk_bf16_f32 v44, v48, v49
	s_nop 0
	v_cvt_pk_bf16_f32 v45, v46, v47
	global_store_dwordx4 v[50:51], v[42:45], off
	s_nop 1
	v_mul_f32_e32 v42, s20, v56
	v_mul_f32_e32 v43, s20, v57
	v_med3_f32 v50, v42, s33, v236
	v_med3_f32 v43, v43, s33, v236
	s_nop 0
	v_cvt_pk_fp8_f32 v42, v50, v43
	v_mul_f32_e32 v44, s20, v54
	v_mul_f32_e32 v45, s20, v55
	v_med3_f32 v44, v44, s33, v236
	v_med3_f32 v45, v45, s33, v236
	v_cvt_pk_fp8_f32 v42, v44, v45 op_sel:[0,0,1]
	v_mul_f32_e32 v43, s20, v48
	v_mul_f32_e32 v44, s20, v49
	v_mul_f32_e32 v45, s20, v46
	v_mul_f32_e32 v46, s20, v47
	v_med3_f32 v47, v43, s33, v236
	v_med3_f32 v44, v44, s33, v236
	s_nop 0
	v_cvt_pk_fp8_f32 v43, v47, v44
	v_med3_f32 v45, v45, s33, v236
	v_med3_f32 v46, v46, s33, v236
	v_cvt_pk_fp8_f32 v43, v45, v46 op_sel:[0,0,1]
	v_lshl_add_u64 v[44:45], s[10:11], 0, v[52:53]
	global_store_dwordx2 v[44:45], v[42:43], off
	ds_read_b64 v[42:43], v0 offset:8576
	v_lshl_add_u64 v[44:45], v[106:107], 0, v[86:87]
	s_waitcnt lgkmcnt(0)
	v_pk_fma_f32 v[34:35], v[34:35], v[42:43], v[42:43] op_sel:[0,1,0] op_sel_hi:[1,1,0]
	v_pk_fma_f32 v[36:37], v[36:37], v[42:43], v[42:43] op_sel:[0,1,0] op_sel_hi:[1,1,0]
	v_pk_fma_f32 v[48:49], v[74:75], v[34:35], v[78:79]
	v_pk_fma_f32 v[34:35], v[38:39], v[42:43], v[42:43] op_sel:[0,1,0] op_sel_hi:[1,1,0]
	v_pk_fma_f32 v[46:47], v[76:77], v[36:37], v[80:81]
	v_pk_fma_f32 v[36:37], v[40:41], v[42:43], v[42:43] op_sel:[0,1,0] op_sel_hi:[1,1,0]
	v_pk_fma_f32 v[40:41], v[66:67], v[34:35], v[70:71]
	v_cvt_pk_bf16_f32 v34, v48, v49
	v_cvt_pk_bf16_f32 v35, v46, v47
	v_lshl_add_u64 v[42:43], v[44:45], 1, s[12:13]
	v_pk_fma_f32 v[38:39], v[68:69], v[36:37], v[72:73]
	v_cvt_pk_bf16_f32 v36, v40, v41
	s_nop 0
	v_cvt_pk_bf16_f32 v37, v38, v39
	global_store_dwordx4 v[42:43], v[34:37], off
	s_nop 1
	v_mul_f32_e32 v34, s20, v48
	v_mul_f32_e32 v35, s20, v49
	v_med3_f32 v42, v34, s33, v236
	v_med3_f32 v35, v35, s33, v236
	s_nop 0
	v_cvt_pk_fp8_f32 v34, v42, v35
	v_mul_f32_e32 v36, s20, v46
	v_mul_f32_e32 v37, s20, v47
	v_med3_f32 v36, v36, s33, v236
	v_med3_f32 v37, v37, s33, v236
	v_cvt_pk_fp8_f32 v34, v36, v37 op_sel:[0,0,1]
	v_mul_f32_e32 v35, s20, v40
	v_mul_f32_e32 v36, s20, v41
	v_mul_f32_e32 v37, s20, v38
	v_mul_f32_e32 v38, s20, v39
	v_med3_f32 v39, v35, s33, v236
	v_med3_f32 v36, v36, s33, v236
	s_nop 0
	v_cvt_pk_fp8_f32 v35, v39, v36
	v_med3_f32 v37, v37, s33, v236
	v_med3_f32 v38, v38, s33, v236
	v_cvt_pk_fp8_f32 v35, v37, v38 op_sel:[0,0,1]
	v_lshl_add_u64 v[36:37], s[10:11], 0, v[44:45]
	global_store_dwordx2 v[36:37], v[34:35], off
	ds_read_b64 v[34:35], v0 offset:9216
	v_lshl_add_u64 v[36:37], v[98:99], 0, v[86:87]
	s_waitcnt lgkmcnt(0)
	v_pk_fma_f32 v[26:27], v[26:27], v[34:35], v[34:35] op_sel:[0,1,0] op_sel_hi:[1,1,0]
	v_pk_fma_f32 v[28:29], v[28:29], v[34:35], v[34:35] op_sel:[0,1,0] op_sel_hi:[1,1,0]
	v_pk_fma_f32 v[40:41], v[74:75], v[26:27], v[78:79]
	v_pk_fma_f32 v[26:27], v[30:31], v[34:35], v[34:35] op_sel:[0,1,0] op_sel_hi:[1,1,0]
	v_pk_fma_f32 v[38:39], v[76:77], v[28:29], v[80:81]
	v_pk_fma_f32 v[28:29], v[32:33], v[34:35], v[34:35] op_sel:[0,1,0] op_sel_hi:[1,1,0]
	v_pk_fma_f32 v[32:33], v[66:67], v[26:27], v[70:71]
	v_cvt_pk_bf16_f32 v26, v40, v41
	v_cvt_pk_bf16_f32 v27, v38, v39
	v_lshl_add_u64 v[34:35], v[36:37], 1, s[12:13]
	v_pk_fma_f32 v[30:31], v[68:69], v[28:29], v[72:73]
	v_cvt_pk_bf16_f32 v28, v32, v33
	s_nop 0
	v_cvt_pk_bf16_f32 v29, v30, v31
	global_store_dwordx4 v[34:35], v[26:29], off
	s_nop 1
	v_mul_f32_e32 v26, s20, v40
	v_mul_f32_e32 v27, s20, v41
	v_med3_f32 v34, v26, s33, v236
	v_med3_f32 v27, v27, s33, v236
	s_nop 0
	v_cvt_pk_fp8_f32 v26, v34, v27
	v_mul_f32_e32 v28, s20, v38
	v_mul_f32_e32 v29, s20, v39
	v_med3_f32 v28, v28, s33, v236
	v_med3_f32 v29, v29, s33, v236
	v_cvt_pk_fp8_f32 v26, v28, v29 op_sel:[0,0,1]
	v_mul_f32_e32 v27, s20, v32
	v_mul_f32_e32 v28, s20, v33
	v_mul_f32_e32 v29, s20, v30
	v_mul_f32_e32 v30, s20, v31
	v_med3_f32 v31, v27, s33, v236
	v_med3_f32 v28, v28, s33, v236
	s_nop 0
	v_cvt_pk_fp8_f32 v27, v31, v28
	v_med3_f32 v29, v29, s33, v236
	v_med3_f32 v30, v30, s33, v236
	v_cvt_pk_fp8_f32 v27, v29, v30 op_sel:[0,0,1]
	v_lshl_add_u64 v[28:29], s[10:11], 0, v[36:37]
	global_store_dwordx2 v[28:29], v[26:27], off
	ds_read_b64 v[26:27], v0 offset:9344
	v_lshl_add_u64 v[28:29], v[90:91], 0, v[86:87]
	s_waitcnt lgkmcnt(0)
	v_pk_fma_f32 v[18:19], v[18:19], v[26:27], v[26:27] op_sel:[0,1,0] op_sel_hi:[1,1,0]
	v_pk_fma_f32 v[20:21], v[20:21], v[26:27], v[26:27] op_sel:[0,1,0] op_sel_hi:[1,1,0]
	v_pk_fma_f32 v[32:33], v[74:75], v[18:19], v[78:79]
	v_pk_fma_f32 v[18:19], v[22:23], v[26:27], v[26:27] op_sel:[0,1,0] op_sel_hi:[1,1,0]
	v_pk_fma_f32 v[30:31], v[76:77], v[20:21], v[80:81]
	v_pk_fma_f32 v[20:21], v[24:25], v[26:27], v[26:27] op_sel:[0,1,0] op_sel_hi:[1,1,0]
	v_pk_fma_f32 v[24:25], v[66:67], v[18:19], v[70:71]
	v_cvt_pk_bf16_f32 v18, v32, v33
	v_cvt_pk_bf16_f32 v19, v30, v31
	v_lshl_add_u64 v[26:27], v[28:29], 1, s[12:13]
	v_pk_fma_f32 v[22:23], v[68:69], v[20:21], v[72:73]
	v_cvt_pk_bf16_f32 v20, v24, v25
	s_nop 0
	v_cvt_pk_bf16_f32 v21, v22, v23
	global_store_dwordx4 v[26:27], v[18:21], off
	s_nop 1
	v_mul_f32_e32 v18, s20, v32
	v_mul_f32_e32 v19, s20, v33
	v_med3_f32 v26, v18, s33, v236
	v_med3_f32 v19, v19, s33, v236
	s_nop 0
	v_cvt_pk_fp8_f32 v18, v26, v19
	v_mul_f32_e32 v20, s20, v30
	v_mul_f32_e32 v21, s20, v31
	v_med3_f32 v20, v20, s33, v236
	v_med3_f32 v21, v21, s33, v236
	v_cvt_pk_fp8_f32 v18, v20, v21 op_sel:[0,0,1]
	v_mul_f32_e32 v19, s20, v24
	v_mul_f32_e32 v20, s20, v25
	v_mul_f32_e32 v21, s20, v22
	v_mul_f32_e32 v22, s20, v23
	v_med3_f32 v23, v19, s33, v236
	v_med3_f32 v20, v20, s33, v236
	s_nop 0
	v_cvt_pk_fp8_f32 v19, v23, v20
	v_med3_f32 v21, v21, s33, v236
	v_med3_f32 v22, v22, s33, v236
	v_cvt_pk_fp8_f32 v19, v21, v22 op_sel:[0,0,1]
	v_lshl_add_u64 v[20:21], s[10:11], 0, v[28:29]
	global_store_dwordx2 v[20:21], v[18:19], off
	ds_read_b64 v[18:19], v0 offset:9472
	v_lshl_add_u64 v[20:21], v[82:83], 0, v[86:87]
	s_waitcnt lgkmcnt(0)
	v_pk_fma_f32 v[10:11], v[10:11], v[18:19], v[18:19] op_sel:[0,1,0] op_sel_hi:[1,1,0]
	v_pk_fma_f32 v[12:13], v[12:13], v[18:19], v[18:19] op_sel:[0,1,0] op_sel_hi:[1,1,0]
	v_pk_fma_f32 v[24:25], v[74:75], v[10:11], v[78:79]
	v_pk_fma_f32 v[10:11], v[14:15], v[18:19], v[18:19] op_sel:[0,1,0] op_sel_hi:[1,1,0]
	v_pk_fma_f32 v[22:23], v[76:77], v[12:13], v[80:81]
	v_pk_fma_f32 v[12:13], v[16:17], v[18:19], v[18:19] op_sel:[0,1,0] op_sel_hi:[1,1,0]
	v_pk_fma_f32 v[16:17], v[66:67], v[10:11], v[70:71]
	v_cvt_pk_bf16_f32 v10, v24, v25
	v_cvt_pk_bf16_f32 v11, v22, v23
	v_lshl_add_u64 v[18:19], v[20:21], 1, s[12:13]
	v_pk_fma_f32 v[14:15], v[68:69], v[12:13], v[72:73]
	v_cvt_pk_bf16_f32 v12, v16, v17
	s_nop 0
	v_cvt_pk_bf16_f32 v13, v14, v15
	global_store_dwordx4 v[18:19], v[10:13], off
	s_nop 1
	v_mul_f32_e32 v10, s20, v24
	v_mul_f32_e32 v11, s20, v25
	v_med3_f32 v18, v10, s33, v236
	v_med3_f32 v11, v11, s33, v236
	s_nop 0
	v_cvt_pk_fp8_f32 v10, v18, v11
	v_mul_f32_e32 v12, s20, v22
	v_mul_f32_e32 v13, s20, v23
	v_med3_f32 v12, v12, s33, v236
	v_med3_f32 v13, v13, s33, v236
	v_cvt_pk_fp8_f32 v10, v12, v13 op_sel:[0,0,1]
	v_mul_f32_e32 v11, s20, v16
	v_mul_f32_e32 v12, s20, v17
	v_mul_f32_e32 v13, s20, v14
	v_mul_f32_e32 v14, s20, v15
	v_med3_f32 v15, v11, s33, v236
	v_med3_f32 v12, v12, s33, v236
	s_nop 0
	v_cvt_pk_fp8_f32 v11, v15, v12
	v_med3_f32 v13, v13, s33, v236
	v_med3_f32 v14, v14, s33, v236
	v_cvt_pk_fp8_f32 v11, v13, v14 op_sel:[0,0,1]
	v_lshl_add_u64 v[12:13], s[10:11], 0, v[20:21]
	global_store_dwordx2 v[12:13], v[10:11], off
	ds_read_b64 v[10:11], v0 offset:9600
	v_lshl_add_u64 v[12:13], v[84:85], 0, v[86:87]
	s_waitcnt lgkmcnt(0)
	v_pk_fma_f32 v[2:3], v[2:3], v[10:11], v[10:11] op_sel:[0,1,0] op_sel_hi:[1,1,0]
	v_pk_fma_f32 v[4:5], v[4:5], v[10:11], v[10:11] op_sel:[0,1,0] op_sel_hi:[1,1,0]
	v_pk_fma_f32 v[16:17], v[74:75], v[2:3], v[78:79]
	v_pk_fma_f32 v[2:3], v[6:7], v[10:11], v[10:11] op_sel:[0,1,0] op_sel_hi:[1,1,0]
	v_pk_fma_f32 v[14:15], v[76:77], v[4:5], v[80:81]
	v_pk_fma_f32 v[4:5], v[8:9], v[10:11], v[10:11] op_sel:[0,1,0] op_sel_hi:[1,1,0]
	v_pk_fma_f32 v[8:9], v[66:67], v[2:3], v[70:71]
	v_cvt_pk_bf16_f32 v2, v16, v17
	v_lshl_add_u64 v[10:11], v[12:13], 1, s[12:13]
	v_pk_fma_f32 v[6:7], v[68:69], v[4:5], v[72:73]
	v_cvt_pk_bf16_f32 v3, v14, v15
	v_cvt_pk_bf16_f32 v4, v8, v9
	v_mul_f32_e32 v0, s20, v16
	v_cvt_pk_bf16_f32 v5, v6, v7
	global_store_dwordx4 v[10:11], v[2:5], off
	v_med3_f32 v0, v0, s33, v236
	s_nop 0
	v_mul_f32_e32 v2, s20, v17
	v_med3_f32 v5, v2, s33, v236
	s_nop 0
	v_cvt_pk_fp8_f32 v2, v0, v5
	v_mul_f32_e32 v3, s20, v14
	v_mul_f32_e32 v4, s20, v15
	v_med3_f32 v3, v3, s33, v236
	v_med3_f32 v4, v4, s33, v236
	v_cvt_pk_fp8_f32 v2, v3, v4 op_sel:[0,0,1]
	v_mul_f32_e32 v0, s20, v8
	v_mul_f32_e32 v3, s20, v9
	v_mul_f32_e32 v4, s20, v6
	v_med3_f32 v0, v0, s33, v236
	v_med3_f32 v6, v3, s33, v236
	s_nop 0
	v_cvt_pk_fp8_f32 v3, v0, v6
	v_mul_f32_e32 v5, s20, v7
	v_med3_f32 v4, v4, s33, v236
	v_med3_f32 v5, v5, s33, v236
	v_cvt_pk_fp8_f32 v3, v4, v5 op_sel:[0,0,1]
	v_lshl_add_u64 v[4:5], s[10:11], 0, v[12:13]
	global_store_dwordx2 v[4:5], v[2:3], off
